# c13
# speedup vs baseline: 1.0081x; 1.0057x over previous
.LBB2_6:
	s_mov_b32 s6, 0
	s_ashr_i32 s7, s6, 31
	v_add_u32_e32 v144, s6, v0
	v_ashrrev_i32_e32 v0, 7, v144
	v_and_b32_e32 v0, -2, v0
	v_bfe_u32 v147, v144, 5, 1
	v_lshl_add_u32 v148, s14, 2, v0
	v_bfe_u32 v146, v144, 4, 1
	v_or_b32_e32 v0, v148, v147
	v_lshlrev_b32_e32 v42, 5, v0
	v_lshlrev_b32_e32 v0, 2, v146
	s_lshl_b64 s[4:5], s[6:7], 2
	v_or_b32_e32 v0, v42, v0
	s_add_u32 s0, s8, s4
	v_ashrrev_i32_e32 v1, 31, v0
	s_addc_u32 s1, s9, s5
	v_lshlrev_b64 v[38:39], 2, v[0:1]
	v_lshl_add_u64 v[150:151], s[0:1], 0, v[38:39]
	global_load_dwordx4 v[34:37], v[150:151], off
	s_add_u32 s4, s10, s4
	s_addc_u32 s5, s11, s5
	v_lshl_add_u64 v[152:153], s[4:5], 0, v[38:39]
	v_ashrrev_i32_e32 v1, 31, v42
	global_load_dwordx4 v[38:41], v[152:153], off
	v_lshlrev_b64 v[42:43], 2, v[0:1]
	v_lshl_add_u64 v[154:155], s[0:1], 0, v[42:43]
	v_lshl_add_u64 v[156:157], s[4:5], 0, v[42:43]
	global_load_dwordx4 v[42:45], v[154:155], off offset:64
	global_load_dwordx4 v[164:167], v[156:157], off offset:64
	global_load_dwordx4 v[168:171], v[154:155], off offset:32
	global_load_dwordx4 v[172:175], v[156:157], off offset:32
	v_or_b32_e32 v0, 8, v0
	v_lshlrev_b64 v[0:1], 2, v[0:1]
	v_lshl_add_u64 v[158:159], s[0:1], 0, v[0:1]
	v_lshl_add_u64 v[160:161], s[4:5], 0, v[0:1]
	global_load_dwordx4 v[176:179], v[158:159], off offset:64
	global_load_dwordx4 v[180:183], v[160:161], off offset:64
	v_ashrrev_i32_e32 v0, 1, v148
	v_lshl_add_u32 v0, s2, 6, v0
	s_movk_i32 s3, 0x6000
	v_mov_b64_e32 v[46:47], s[12:13]
	v_ashrrev_i32_e32 v1, 31, v0
	v_mad_i64_i32 v[148:149], s[2:3], v0, s3, v[46:47]
	v_lshlrev_b64 v[0:1], 10, v[0:1]
	s_mov_b64 s[6:7], 0x3000000
	v_permlane32_swap_b32_e32 v30, v14
	v_permlane32_swap_b32_e32 v31, v15
	v_lshl_add_u64 v[0:1], s[12:13], 0, v[0:1]
	v_permlane32_swap_b32_e32 v32, v16
	v_permlane32_swap_b32_e32 v33, v17
	s_mov_b32 s4, 0xbfb8aa3b
	v_and_b32_e32 v163, 0xcf, v144
	v_lshlrev_b32_e32 v162, 9, v147
	v_mul_u32_u24_e32 v144, 12, v146
	v_cmp_eq_u32_e64 s[0:1], 0, v146
	v_lshl_add_u64 v[146:147], v[0:1], 0, s[6:7]
	v_permlane32_swap_b32_e32 v26, v10
	v_permlane32_swap_b32_e32 v27, v11
	v_permlane32_swap_b32_e32 v22, v6
	v_permlane32_swap_b32_e32 v23, v7
	v_permlane32_swap_b32_e32 v28, v12
	v_permlane32_swap_b32_e32 v29, v13
	v_permlane32_swap_b32_e32 v24, v8
	v_permlane32_swap_b32_e32 v25, v9
	v_permlane32_swap_b32_e32 v18, v2
	v_permlane32_swap_b32_e32 v19, v3
	v_permlane32_swap_b32_e32 v20, v4
	v_permlane32_swap_b32_e32 v21, v5
	s_mov_b32 s3, 0x700000
	s_mov_b32 s8, 0x42000000
	s_mov_b32 s2, 0xc2000000
	v_mov_b32_e32 v145, 0
	s_waitcnt vmcnt(0)
	v_pk_mul_f32 v[0:1], v[34:35], v[30:31]
	v_pk_mul_f32 v[30:31], v[36:37], v[32:33]
	v_pk_mul_f32 v[32:33], v[0:1], s[4:5] op_sel_hi:[1,0]
	v_pk_mul_f32 v[34:35], v[30:31], s[4:5] op_sel_hi:[1,0]
	v_exp_f32_e32 v32, v32
	v_exp_f32_e32 v33, v33
	v_exp_f32_e32 v34, v34
	v_exp_f32_e32 v35, v35
	v_pk_mul_f32 v[26:27], v[38:39], v[26:27]
	v_pk_add_f32 v[32:33], v[32:33], 1.0 op_sel_hi:[1,0]
	v_pk_mul_f32 v[22:23], v[42:43], v[22:23]
	v_rcp_f32_e32 v32, v32
	v_rcp_f32_e32 v33, v33
	v_pk_add_f32 v[34:35], v[34:35], 1.0 op_sel_hi:[1,0]
	v_pk_mul_f32 v[24:25], v[44:45], v[24:25]
	v_rcp_f32_e32 v34, v34
	v_rcp_f32_e32 v35, v35
	v_pk_mul_f32 v[0:1], v[0:1], v[32:33]
	v_pk_mul_f32 v[18:19], v[164:165], v[18:19]
	v_pk_mul_f32 v[0:1], v[26:27], v[0:1]
	v_pk_mul_f32 v[26:27], v[40:41], v[28:29]
	v_pk_mul_f32 v[28:29], v[30:31], v[34:35]
	v_pk_mul_f32 v[30:31], v[24:25], s[4:5] op_sel_hi:[1,0]
	v_pk_mul_f32 v[26:27], v[26:27], v[28:29]
	v_pk_mul_f32 v[28:29], v[22:23], s[4:5] op_sel_hi:[1,0]
	v_exp_f32_e32 v30, v30
	v_exp_f32_e32 v28, v28
	v_exp_f32_e32 v29, v29
	v_exp_f32_e32 v31, v31
	v_pk_mul_f32 v[20:21], v[166:167], v[20:21]
	v_pk_mul_f32 v[14:15], v[168:169], v[14:15]
	v_pk_add_f32 v[28:29], v[28:29], 1.0 op_sel_hi:[1,0]
	v_pk_add_f32 v[30:31], v[30:31], 1.0 op_sel_hi:[1,0]
	v_rcp_f32_e32 v28, v28
	v_rcp_f32_e32 v29, v29
	v_rcp_f32_e32 v30, v30
	v_rcp_f32_e32 v31, v31
	v_pk_mul_f32 v[16:17], v[170:171], v[16:17]
	v_pk_mul_f32 v[22:23], v[22:23], v[28:29]
	v_pk_mul_f32 v[10:11], v[172:173], v[10:11]
	v_pk_mul_f32 v[18:19], v[18:19], v[22:23]
	v_pk_mul_f32 v[22:23], v[24:25], v[30:31]
	v_pk_mul_f32 v[24:25], v[16:17], s[4:5] op_sel_hi:[1,0]
	v_pk_mul_f32 v[20:21], v[20:21], v[22:23]
	v_pk_mul_f32 v[22:23], v[14:15], s[4:5] op_sel_hi:[1,0]
	v_exp_f32_e32 v24, v24
	v_exp_f32_e32 v22, v22
	v_exp_f32_e32 v23, v23
	v_exp_f32_e32 v25, v25
	v_pk_mul_f32 v[12:13], v[174:175], v[12:13]
	v_pk_mul_f32 v[6:7], v[176:177], v[6:7]
	v_pk_add_f32 v[22:23], v[22:23], 1.0 op_sel_hi:[1,0]
	v_pk_add_f32 v[24:25], v[24:25], 1.0 op_sel_hi:[1,0]
	v_rcp_f32_e32 v22, v22
	v_rcp_f32_e32 v23, v23
	v_rcp_f32_e32 v24, v24
	v_rcp_f32_e32 v25, v25
	v_pk_mul_f32 v[8:9], v[178:179], v[8:9]
	v_pk_mul_f32 v[14:15], v[14:15], v[22:23]
	v_pk_mul_f32 v[2:3], v[180:181], v[2:3]
	v_pk_mul_f32 v[10:11], v[10:11], v[14:15]
	v_pk_mul_f32 v[14:15], v[16:17], v[24:25]
	v_pk_mul_f32 v[16:17], v[8:9], s[4:5] op_sel_hi:[1,0]
	v_pk_mul_f32 v[12:13], v[12:13], v[14:15]
	v_pk_mul_f32 v[14:15], v[6:7], s[4:5] op_sel_hi:[1,0]
	v_exp_f32_e32 v16, v16
	v_exp_f32_e32 v14, v14
	v_exp_f32_e32 v15, v15
	v_exp_f32_e32 v17, v17
	v_pk_mul_f32 v[4:5], v[182:183], v[4:5]
	v_mov_b32_e32 v164, 0xffffff7f
	v_pk_add_f32 v[14:15], v[14:15], 1.0 op_sel_hi:[1,0]
	v_pk_add_f32 v[16:17], v[16:17], 1.0 op_sel_hi:[1,0]
	v_rcp_f32_e32 v14, v14
	v_rcp_f32_e32 v15, v15
	v_rcp_f32_e32 v16, v16
	v_rcp_f32_e32 v17, v17
	s_movk_i32 s5, 0xff9c
	v_pk_mul_f32 v[6:7], v[6:7], v[14:15]
	v_mov_b32_e32 v165, 0x64
	v_pk_mul_f32 v[2:3], v[2:3], v[6:7]
	v_pk_mul_f32 v[6:7], v[8:9], v[16:17]
	v_max_f32_e64 v8, |v20|, |v21|
	v_pk_mul_f32 v[4:5], v[4:5], v[6:7]
	v_max_f32_e64 v6, |v0|, |v1|
	v_max_f32_e64 v7, |v26|, |v27|
	v_max3_f32 v6, v6, 0, v7
	v_max_f32_e64 v7, |v18|, |v19|
	v_max3_f32 v6, v6, v7, v8
	v_max_f32_e64 v7, |v10|, |v11|
	v_max_f32_e64 v8, |v12|, |v13|
	v_max3_f32 v6, v6, v7, v8
	v_max_f32_e64 v7, |v2|, |v3|
	v_max_f32_e64 v8, |v4|, |v5|
	v_max3_f32 v6, v6, v7, v8
	v_mov_b32_e32 v7, v6
	s_nop 1
	v_permlane16_swap_b32_e32 v6, v7
	v_max_f32_e32 v7, v7, v7
	v_max_f32_e32 v6, v6, v6
	v_max_f32_e32 v6, v6, v7
	v_lshrrev_b32_e32 v7, 23, v6
	v_and_b32_e32 v6, 0x7fffff, v6
	v_cmp_lt_u32_e32 vcc, s3, v6
	s_nop 1
	v_addc_co_u32_e32 v6, vcc, v7, v164, vcc
	v_med3_i32 v166, v6, s5, v165
	v_lshlrev_b32_e32 v6, 23, v166
	v_sub_u32_e32 v6, 1.0, v6
	v_pk_mul_f32 v[40:41], v[6:7], v[10:11] op_sel_hi:[0,1]
	v_pk_mul_f32 v[42:43], v[6:7], v[12:13] op_sel_hi:[0,1]
	v_pk_mul_f32 v[44:45], v[6:7], v[2:3] op_sel_hi:[0,1]
	v_pk_mul_f32 v[46:47], v[6:7], v[4:5] op_sel_hi:[0,1]
	v_pk_mul_f32 v[32:33], v[6:7], v[0:1] op_sel_hi:[0,1]
	v_pk_mul_f32 v[34:35], v[6:7], v[26:27] op_sel_hi:[0,1]
	v_pk_mul_f32 v[36:37], v[6:7], v[18:19] op_sel_hi:[0,1]
	v_pk_mul_f32 v[38:39], v[6:7], v[20:21] op_sel_hi:[0,1]
	v_cvt_scalef32_2xpk16_fp6_f32 v[168:173], v[32:47], v[40:55], 1.0
	v_cvt_scalef32_pk32_f32_fp6 v[0:31], v[168:173], s8
	v_fma_f32 v16, v32, s2, v0
	v_fma_f32 v17, v33, s2, v2
	v_fma_f32 v18, v34, s2, v4
	v_fma_f32 v19, v35, s2, v6
	v_fma_f32 v20, v36, s2, v8
	v_fma_f32 v21, v37, s2, v10
	v_fma_f32 v22, v38, s2, v12
	v_fma_f32 v23, v39, s2, v14
	v_fma_f32 v24, v40, s2, v1
	v_fma_f32 v25, v41, s2, v3
	v_fma_f32 v26, v42, s2, v5
	v_fma_f32 v27, v43, s2, v7
	v_fma_f32 v28, v44, s2, v9
	v_fma_f32 v29, v45, s2, v11
	v_fma_f32 v30, v46, s2, v13
	v_fma_f32 v31, v47, s2, v15
	v_cvt_scalef32_2xpk16_fp6_f32 v[0:5], v[16:31], v[24:39], 1.0
	v_or_b32_e32 v3, v163, v162
	v_mul_u32_u24_e32 v4, 24, v3
	v_mov_b32_e32 v5, v145
	v_lshl_add_u64 v[4:5], v[148:149], 0, v[4:5]
	v_lshl_add_u64 v[4:5], v[4:5], 0, v[144:145]
	global_store_dwordx3 v[4:5], v[168:170], off nt
	v_add_co_u32_e32 v4, vcc, 0x1000, v4
	v_xor_b32_e32 v0, 0x20820820, v0
	v_xor_b32_e32 v1, 0x8208208, v1
	v_xor_b32_e32 v2, 0x82082082, v2
	v_addc_co_u32_e32 v5, vcc, 0, v5, vcc
	global_store_dwordx3 v[4:5], v[0:2], off offset:2048 nt
	s_and_saveexec_b64 s[6:7], s[0:1]
	s_cbranch_execz .LBB2_8
	v_mov_b32_e32 v1, 0x7a00
	v_add_u32_e32 v0, 0x7f, v166
	v_lshl_add_u32 v1, v166, 8, v1
	v_or_b32_e32 v2, v1, v0
	v_lshl_or_b32 v0, v163, 1, v162
	v_mov_b32_e32 v1, v145
	v_lshl_add_u64 v[0:1], v[146:147], 0, v[0:1]
	global_store_short v[0:1], v2, off
.LBB2_8:
	s_or_b64 exec, exec, s[6:7]
	global_load_dwordx4 v[0:3], v[150:151], off
	global_load_dwordx4 v[4:7], v[152:153], off
	global_load_dwordx4 v[8:11], v[154:155], off offset:64
	global_load_dwordx4 v[12:15], v[156:157], off offset:64
	global_load_dwordx4 v[16:19], v[154:155], off offset:32
	global_load_dwordx4 v[20:23], v[156:157], off offset:32
	global_load_dwordx4 v[24:27], v[158:159], off offset:64
	global_load_dwordx4 v[28:31], v[160:161], off offset:64
	v_permlane32_swap_b32_e32 v132, v124
	v_permlane32_swap_b32_e32 v133, v125
	v_permlane32_swap_b32_e32 v128, v116
	v_permlane32_swap_b32_e32 v129, v117
	v_permlane32_swap_b32_e32 v134, v126
	v_permlane32_swap_b32_e32 v135, v127
	v_permlane32_swap_b32_e32 v130, v118
	v_permlane32_swap_b32_e32 v131, v119
	v_permlane32_swap_b32_e32 v140, v120
	v_permlane32_swap_b32_e32 v141, v121
	v_permlane32_swap_b32_e32 v136, v112
	v_permlane32_swap_b32_e32 v137, v113
	v_permlane32_swap_b32_e32 v142, v122
	v_permlane32_swap_b32_e32 v143, v123
	v_permlane32_swap_b32_e32 v138, v114
	v_permlane32_swap_b32_e32 v139, v115
	s_waitcnt vmcnt(7)
	v_pk_mul_f32 v[0:1], v[0:1], v[132:133]
	s_nop 0
	v_pk_mul_f32 v[32:33], v[0:1], s[4:5] op_sel_hi:[1,0]
	s_waitcnt vmcnt(5)
	v_pk_mul_f32 v[8:9], v[8:9], v[128:129]
	v_exp_f32_e32 v32, v32
	v_pk_mul_f32 v[36:37], v[8:9], s[4:5] op_sel_hi:[1,0]
	v_exp_f32_e32 v33, v33
	v_exp_f32_e32 v36, v36
	v_exp_f32_e32 v37, v37
	s_waitcnt vmcnt(3)
	v_pk_mul_f32 v[18:19], v[18:19], v[126:127]
	v_pk_mul_f32 v[2:3], v[2:3], v[134:135]
	v_pk_mul_f32 v[10:11], v[10:11], v[130:131]
	v_pk_mul_f32 v[42:43], v[18:19], s[4:5] op_sel_hi:[1,0]
	v_pk_add_f32 v[32:33], v[32:33], 1.0 op_sel_hi:[1,0]
	v_pk_add_f32 v[36:37], v[36:37], 1.0 op_sel_hi:[1,0]
	v_pk_mul_f32 v[16:17], v[16:17], v[124:125]
	v_pk_mul_f32 v[34:35], v[2:3], s[4:5] op_sel_hi:[1,0]
	v_pk_mul_f32 v[38:39], v[10:11], s[4:5] op_sel_hi:[1,0]
	v_exp_f32_e32 v42, v42
	v_exp_f32_e32 v43, v43
	v_rcp_f32_e32 v32, v32
	v_rcp_f32_e32 v33, v33
	v_rcp_f32_e32 v36, v36
	v_rcp_f32_e32 v37, v37
	v_pk_mul_f32 v[40:41], v[16:17], s[4:5] op_sel_hi:[1,0]
	v_exp_f32_e32 v34, v34
	v_exp_f32_e32 v35, v35
	v_exp_f32_e32 v38, v38
	v_exp_f32_e32 v39, v39
	v_exp_f32_e32 v40, v40
	v_exp_f32_e32 v41, v41
	v_pk_mul_f32 v[4:5], v[4:5], v[140:141]
	v_pk_mul_f32 v[12:13], v[12:13], v[136:137]
	v_pk_add_f32 v[42:43], v[42:43], 1.0 op_sel_hi:[1,0]
	v_pk_mul_f32 v[0:1], v[0:1], v[32:33]
	v_pk_mul_f32 v[8:9], v[8:9], v[36:37]
	v_pk_add_f32 v[34:35], v[34:35], 1.0 op_sel_hi:[1,0]
	v_pk_add_f32 v[38:39], v[38:39], 1.0 op_sel_hi:[1,0]
	v_pk_mul_f32 v[0:1], v[4:5], v[0:1]
	v_pk_mul_f32 v[4:5], v[12:13], v[8:9]
	v_rcp_f32_e32 v8, v42
	v_rcp_f32_e32 v9, v43
	v_pk_add_f32 v[40:41], v[40:41], 1.0 op_sel_hi:[1,0]
	v_rcp_f32_e32 v34, v34
	v_rcp_f32_e32 v35, v35
	v_rcp_f32_e32 v38, v38
	v_rcp_f32_e32 v39, v39
	v_rcp_f32_e32 v40, v40
	v_rcp_f32_e32 v41, v41
	s_waitcnt vmcnt(2)
	v_pk_mul_f32 v[12:13], v[22:23], v[122:123]
	v_pk_mul_f32 v[8:9], v[18:19], v[8:9]
	v_pk_mul_f32 v[6:7], v[6:7], v[142:143]
	v_pk_mul_f32 v[14:15], v[14:15], v[138:139]
	v_pk_mul_f32 v[2:3], v[2:3], v[34:35]
	v_pk_mul_f32 v[10:11], v[10:11], v[38:39]
	v_pk_mul_f32 v[8:9], v[12:13], v[8:9]
	s_waitcnt vmcnt(1)
	v_pk_mul_f32 v[12:13], v[24:25], v[116:117]
	v_pk_mul_f32 v[20:21], v[20:21], v[120:121]
	v_pk_mul_f32 v[2:3], v[6:7], v[2:3]
	v_pk_mul_f32 v[6:7], v[14:15], v[10:11]
	v_pk_mul_f32 v[10:11], v[16:17], v[40:41]
	v_pk_mul_f32 v[16:17], v[12:13], s[4:5] op_sel_hi:[1,0]
	v_pk_mul_f32 v[18:19], v[26:27], v[118:119]
	v_pk_mul_f32 v[10:11], v[20:21], v[10:11]
	v_exp_f32_e32 v16, v16
	v_exp_f32_e32 v17, v17
	v_pk_mul_f32 v[20:21], v[18:19], s[4:5] op_sel_hi:[1,0]
	s_waitcnt vmcnt(0)
	v_pk_mul_f32 v[14:15], v[28:29], v[112:113]
	v_exp_f32_e32 v20, v20
	v_exp_f32_e32 v21, v21
	v_pk_add_f32 v[16:17], v[16:17], 1.0 op_sel_hi:[1,0]
	v_pk_add_f32 v[20:21], v[20:21], 1.0 op_sel_hi:[1,0]
	v_rcp_f32_e32 v16, v16
	v_rcp_f32_e32 v17, v17
	v_rcp_f32_e32 v20, v20
	v_rcp_f32_e32 v21, v21
	v_pk_mul_f32 v[12:13], v[12:13], v[16:17]
	s_nop 0
	v_pk_mul_f32 v[12:13], v[14:15], v[12:13]
	v_pk_mul_f32 v[14:15], v[30:31], v[114:115]
	v_pk_mul_f32 v[16:17], v[18:19], v[20:21]
	v_max_f32_e64 v18, |v6|, |v7|
	v_pk_mul_f32 v[14:15], v[14:15], v[16:17]
	v_max_f32_e64 v16, |v0|, |v1|
	v_max_f32_e64 v17, |v2|, |v3|
	v_max3_f32 v16, v16, 0, v17
	v_max_f32_e64 v17, |v4|, |v5|
	v_max3_f32 v16, v16, v17, v18
	v_max_f32_e64 v17, |v10|, |v11|
	v_max_f32_e64 v18, |v8|, |v9|
	v_max3_f32 v16, v16, v17, v18
	v_max_f32_e64 v17, |v12|, |v13|
	v_max_f32_e64 v18, |v14|, |v15|
	v_max3_f32 v16, v16, v17, v18
	v_mov_b32_e32 v17, v16
	s_nop 1
	v_permlane16_swap_b32_e32 v16, v17
	v_max_f32_e32 v17, v17, v17
	v_max_f32_e32 v16, v16, v16
	v_max_f32_e32 v16, v16, v17
	v_lshrrev_b32_e32 v17, 23, v16
	v_and_b32_e32 v16, 0x7fffff, v16
	v_cmp_lt_u32_e32 vcc, s3, v16
	s_nop 1
	v_addc_co_u32_e32 v16, vcc, v17, v164, vcc
	v_med3_i32 v112, v16, s5, v165
	v_lshlrev_b32_e32 v16, 23, v112
	v_sub_u32_e32 v16, 1.0, v16
	v_pk_mul_f32 v[40:41], v[16:17], v[10:11] op_sel_hi:[0,1]
	v_pk_mul_f32 v[42:43], v[16:17], v[8:9] op_sel_hi:[0,1]
	v_pk_mul_f32 v[44:45], v[16:17], v[12:13] op_sel_hi:[0,1]
	v_pk_mul_f32 v[46:47], v[16:17], v[14:15] op_sel_hi:[0,1]
	v_pk_mul_f32 v[32:33], v[16:17], v[0:1] op_sel_hi:[0,1]
	v_pk_mul_f32 v[34:35], v[16:17], v[2:3] op_sel_hi:[0,1]
	v_pk_mul_f32 v[36:37], v[16:17], v[4:5] op_sel_hi:[0,1]
	v_pk_mul_f32 v[38:39], v[16:17], v[6:7] op_sel_hi:[0,1]
	v_cvt_scalef32_2xpk16_fp6_f32 v[114:119], v[32:47], v[40:55], 1.0
	v_cvt_scalef32_pk32_f32_fp6 v[0:31], v[114:119], s8
	v_fma_f32 v16, v32, s2, v0
	v_fma_f32 v17, v33, s2, v2
	v_fma_f32 v18, v34, s2, v4
	v_fma_f32 v19, v35, s2, v6
	v_fma_f32 v20, v36, s2, v8
	v_fma_f32 v21, v37, s2, v10
	v_fma_f32 v22, v38, s2, v12
	v_fma_f32 v23, v39, s2, v14
	v_fma_f32 v24, v40, s2, v1
	v_fma_f32 v25, v41, s2, v3
	v_fma_f32 v26, v42, s2, v5
	v_fma_f32 v27, v43, s2, v7
	v_fma_f32 v28, v44, s2, v9
	v_fma_f32 v29, v45, s2, v11
	v_fma_f32 v30, v46, s2, v13
	v_fma_f32 v31, v47, s2, v15
	v_cvt_scalef32_2xpk16_fp6_f32 v[0:5], v[16:31], v[24:39], 1.0
	v_xor_b32_e32 v4, 0x20820820, v0
	v_or_b32_e32 v0, 16, v163
	v_xor_b32_e32 v5, 0x8208208, v1
	v_or_b32_e32 v1, v0, v162
	v_xor_b32_e32 v6, 0x82082082, v2
	v_mul_u32_u24_e32 v2, 24, v1
	v_mov_b32_e32 v3, v145
	v_lshl_add_u64 v[2:3], v[148:149], 0, v[2:3]
	v_lshl_add_u64 v[2:3], v[2:3], 0, v[144:145]
	global_store_dwordx3 v[2:3], v[114:116], off nt
	v_add_co_u32_e32 v2, vcc, 0x1000, v2
	s_nop 1
	v_addc_co_u32_e32 v3, vcc, 0, v3, vcc
	global_store_dwordx3 v[2:3], v[4:6], off offset:2048 nt
	s_and_saveexec_b64 s[2:3], s[0:1]
	s_cbranch_execz .LBB2_10
	v_mov_b32_e32 v2, 0x7a00
	v_add_u32_e32 v1, 0x7f, v112
	v_lshl_add_u32 v2, v112, 8, v2
	v_or_b32_e32 v2, v2, v1
	v_lshl_or_b32 v0, v0, 1, v162
	v_mov_b32_e32 v1, 0
	v_lshl_add_u64 v[0:1], v[146:147], 0, v[0:1]
	global_store_short v[0:1], v2, off
.LBB2_10:
	s_or_b64 exec, exec, s[2:3]
	global_load_dwordx4 v[0:3], v[150:151], off
	global_load_dwordx4 v[4:7], v[152:153], off
	global_load_dwordx4 v[8:11], v[154:155], off offset:64
	global_load_dwordx4 v[12:15], v[156:157], off offset:64
	global_load_dwordx4 v[16:19], v[154:155], off offset:32
	global_load_dwordx4 v[20:23], v[156:157], off offset:32
	global_load_dwordx4 v[24:27], v[158:159], off offset:64
	global_load_dwordx4 v[28:31], v[160:161], off offset:64
	v_permlane32_swap_b32_e32 v100, v92
	v_permlane32_swap_b32_e32 v101, v93
	v_permlane32_swap_b32_e32 v96, v84
	v_permlane32_swap_b32_e32 v97, v85
	s_mov_b32 s2, 0xbfb8aa3b
	v_permlane32_swap_b32_e32 v102, v94
	v_permlane32_swap_b32_e32 v103, v95
	v_permlane32_swap_b32_e32 v98, v86
	v_permlane32_swap_b32_e32 v99, v87
	v_permlane32_swap_b32_e32 v108, v88
	v_permlane32_swap_b32_e32 v109, v89
	v_permlane32_swap_b32_e32 v104, v80
	v_permlane32_swap_b32_e32 v105, v81
	v_permlane32_swap_b32_e32 v110, v90
	v_permlane32_swap_b32_e32 v111, v91
	v_permlane32_swap_b32_e32 v106, v82
	v_permlane32_swap_b32_e32 v107, v83
	s_mov_b32 s4, 0xc2000000
	s_waitcnt vmcnt(7)
	v_pk_mul_f32 v[0:1], v[0:1], v[100:101]
	s_nop 0
	v_pk_mul_f32 v[32:33], v[0:1], s[2:3] op_sel_hi:[1,0]
	s_waitcnt vmcnt(5)
	v_pk_mul_f32 v[8:9], v[8:9], v[96:97]
	v_exp_f32_e32 v32, v32
	v_pk_mul_f32 v[36:37], v[8:9], s[2:3] op_sel_hi:[1,0]
	v_exp_f32_e32 v33, v33
	v_exp_f32_e32 v36, v36
	v_exp_f32_e32 v37, v37
	s_waitcnt vmcnt(3)
	v_pk_mul_f32 v[18:19], v[18:19], v[94:95]
	v_pk_add_f32 v[32:33], v[32:33], 1.0 op_sel_hi:[1,0]
	v_pk_mul_f32 v[2:3], v[2:3], v[102:103]
	v_pk_add_f32 v[36:37], v[36:37], 1.0 op_sel_hi:[1,0]
	v_pk_mul_f32 v[10:11], v[10:11], v[98:99]
	v_pk_mul_f32 v[42:43], v[18:19], s[2:3] op_sel_hi:[1,0]
	v_rcp_f32_e32 v32, v32
	v_rcp_f32_e32 v33, v33
	v_rcp_f32_e32 v36, v36
	v_rcp_f32_e32 v37, v37
	v_pk_mul_f32 v[16:17], v[16:17], v[92:93]
	v_pk_mul_f32 v[34:35], v[2:3], s[2:3] op_sel_hi:[1,0]
	v_pk_mul_f32 v[38:39], v[10:11], s[2:3] op_sel_hi:[1,0]
	v_exp_f32_e32 v42, v42
	v_exp_f32_e32 v43, v43
	v_pk_mul_f32 v[40:41], v[16:17], s[2:3] op_sel_hi:[1,0]
	v_exp_f32_e32 v34, v34
	v_exp_f32_e32 v35, v35
	v_exp_f32_e32 v38, v38
	v_exp_f32_e32 v39, v39
	v_exp_f32_e32 v40, v40
	v_exp_f32_e32 v41, v41
	v_pk_mul_f32 v[4:5], v[4:5], v[108:109]
	v_pk_mul_f32 v[12:13], v[12:13], v[104:105]
	v_pk_mul_f32 v[0:1], v[0:1], v[32:33]
	v_pk_mul_f32 v[8:9], v[8:9], v[36:37]
	v_pk_mul_f32 v[0:1], v[4:5], v[0:1]
	v_pk_mul_f32 v[4:5], v[12:13], v[8:9]
	v_pk_add_f32 v[8:9], v[42:43], 1.0 op_sel_hi:[1,0]
	v_pk_add_f32 v[34:35], v[34:35], 1.0 op_sel_hi:[1,0]
	v_pk_add_f32 v[38:39], v[38:39], 1.0 op_sel_hi:[1,0]
	v_rcp_f32_e32 v8, v8
	v_rcp_f32_e32 v9, v9
	v_pk_add_f32 v[40:41], v[40:41], 1.0 op_sel_hi:[1,0]
	v_rcp_f32_e32 v34, v34
	v_rcp_f32_e32 v35, v35
	v_rcp_f32_e32 v38, v38
	v_rcp_f32_e32 v39, v39
	v_rcp_f32_e32 v40, v40
	v_rcp_f32_e32 v41, v41
	s_waitcnt vmcnt(2)
	v_pk_mul_f32 v[12:13], v[22:23], v[90:91]
	v_pk_mul_f32 v[8:9], v[18:19], v[8:9]
	v_pk_mul_f32 v[6:7], v[6:7], v[110:111]
	v_pk_mul_f32 v[14:15], v[14:15], v[106:107]
	v_pk_mul_f32 v[2:3], v[2:3], v[34:35]
	v_pk_mul_f32 v[10:11], v[10:11], v[38:39]
	v_pk_mul_f32 v[8:9], v[12:13], v[8:9]
	s_waitcnt vmcnt(1)
	v_pk_mul_f32 v[12:13], v[24:25], v[84:85]
	v_pk_mul_f32 v[20:21], v[20:21], v[88:89]
	v_pk_mul_f32 v[2:3], v[6:7], v[2:3]
	v_pk_mul_f32 v[6:7], v[14:15], v[10:11]
	v_pk_mul_f32 v[10:11], v[16:17], v[40:41]
	v_pk_mul_f32 v[16:17], v[12:13], s[2:3] op_sel_hi:[1,0]
	v_pk_mul_f32 v[18:19], v[26:27], v[86:87]
	v_pk_mul_f32 v[10:11], v[20:21], v[10:11]
	v_exp_f32_e32 v16, v16
	v_exp_f32_e32 v17, v17
	v_pk_mul_f32 v[20:21], v[18:19], s[2:3] op_sel_hi:[1,0]
	s_waitcnt vmcnt(0)
	v_pk_mul_f32 v[14:15], v[28:29], v[80:81]
	v_exp_f32_e32 v20, v20
	v_exp_f32_e32 v21, v21
	v_pk_add_f32 v[16:17], v[16:17], 1.0 op_sel_hi:[1,0]
	s_mov_b32 s3, 0x700000
	v_rcp_f32_e32 v16, v16
	v_rcp_f32_e32 v17, v17
	v_pk_add_f32 v[20:21], v[20:21], 1.0 op_sel_hi:[1,0]
	v_mov_b32_e32 v81, 0
	v_rcp_f32_e32 v20, v20
	v_rcp_f32_e32 v21, v21
	v_pk_mul_f32 v[12:13], v[12:13], v[16:17]
	v_pk_mul_f32 v[16:17], v[18:19], v[20:21]
	v_pk_mul_f32 v[12:13], v[14:15], v[12:13]
	v_pk_mul_f32 v[14:15], v[30:31], v[82:83]
	v_max_f32_e64 v18, |v6|, |v7|
	v_pk_mul_f32 v[14:15], v[14:15], v[16:17]
	v_max_f32_e64 v16, |v0|, |v1|
	v_max_f32_e64 v17, |v2|, |v3|
	v_max3_f32 v16, v16, 0, v17
	v_max_f32_e64 v17, |v4|, |v5|
	v_max3_f32 v16, v16, v17, v18
	v_max_f32_e64 v17, |v10|, |v11|
	v_max_f32_e64 v18, |v8|, |v9|
	v_max3_f32 v16, v16, v17, v18
	v_max_f32_e64 v17, |v12|, |v13|
	v_max_f32_e64 v18, |v14|, |v15|
	v_max3_f32 v16, v16, v17, v18
	v_mov_b32_e32 v17, v16
	s_nop 1
	v_permlane16_swap_b32_e32 v16, v17
	v_max_f32_e32 v17, v17, v17
	v_max_f32_e32 v16, v16, v16
	v_max_f32_e32 v16, v16, v17
	v_lshrrev_b32_e32 v17, 23, v16
	v_and_b32_e32 v16, 0x7fffff, v16
	v_mov_b32_e32 v82, 0xffffff7f
	v_cmp_lt_u32_e32 vcc, s3, v16
	v_mov_b32_e32 v83, 0x64
	s_nop 0
	v_addc_co_u32_e32 v16, vcc, v17, v82, vcc
	v_med3_i32 v84, v16, s5, v83
	v_lshlrev_b32_e32 v16, 23, v84
	v_sub_u32_e32 v16, 1.0, v16
	v_pk_mul_f32 v[40:41], v[16:17], v[10:11] op_sel_hi:[0,1]
	v_pk_mul_f32 v[42:43], v[16:17], v[8:9] op_sel_hi:[0,1]
	v_pk_mul_f32 v[44:45], v[16:17], v[12:13] op_sel_hi:[0,1]
	v_pk_mul_f32 v[46:47], v[16:17], v[14:15] op_sel_hi:[0,1]
	v_pk_mul_f32 v[32:33], v[16:17], v[0:1] op_sel_hi:[0,1]
	v_pk_mul_f32 v[34:35], v[16:17], v[2:3] op_sel_hi:[0,1]
	v_pk_mul_f32 v[36:37], v[16:17], v[4:5] op_sel_hi:[0,1]
	v_pk_mul_f32 v[38:39], v[16:17], v[6:7] op_sel_hi:[0,1]
	v_cvt_scalef32_2xpk16_fp6_f32 v[86:91], v[32:47], v[40:55], 1.0
	v_cvt_scalef32_pk32_f32_fp6 v[0:31], v[86:91], s8
	v_fma_f32 v16, v32, s4, v0
	v_fma_f32 v17, v33, s4, v2
	v_fma_f32 v18, v34, s4, v4
	v_fma_f32 v19, v35, s4, v6
	v_fma_f32 v20, v36, s4, v8
	v_fma_f32 v21, v37, s4, v10
	v_fma_f32 v22, v38, s4, v12
	v_fma_f32 v23, v39, s4, v14
	v_fma_f32 v24, v40, s4, v1
	v_fma_f32 v25, v41, s4, v3
	v_fma_f32 v26, v42, s4, v5
	v_fma_f32 v27, v43, s4, v7
	v_fma_f32 v28, v44, s4, v9
	v_fma_f32 v29, v45, s4, v11
	v_fma_f32 v30, v46, s4, v13
	v_fma_f32 v31, v47, s4, v15
	v_cvt_scalef32_2xpk16_fp6_f32 v[0:5], v[16:31], v[24:39], 1.0
	v_xor_b32_e32 v4, 0x20820820, v0
	v_or_b32_e32 v0, 32, v163
	v_xor_b32_e32 v5, 0x8208208, v1
	v_or_b32_e32 v1, v0, v162
	v_mul_u32_u24_e32 v80, 24, v1
	v_xor_b32_e32 v6, 0x82082082, v2
	v_lshl_add_u64 v[2:3], v[148:149], 0, v[80:81]
	v_lshl_add_u64 v[2:3], v[2:3], 0, v[144:145]
	global_store_dwordx3 v[2:3], v[86:88], off nt
	v_add_co_u32_e32 v2, vcc, 0x1000, v2
	s_nop 1
	v_addc_co_u32_e32 v3, vcc, 0, v3, vcc
	global_store_dwordx3 v[2:3], v[4:6], off offset:2048 nt
	s_and_saveexec_b64 s[6:7], s[0:1]
	s_cbranch_execz .LBB2_12
	v_mov_b32_e32 v2, 0x7a00
	v_add_u32_e32 v1, 0x7f, v84
	v_lshl_add_u32 v2, v84, 8, v2
	v_lshl_or_b32 v80, v0, 1, v162
	v_or_b32_e32 v2, v2, v1
	v_lshl_add_u64 v[0:1], v[146:147], 0, v[80:81]
	global_store_short v[0:1], v2, off
.LBB2_12:
	s_or_b64 exec, exec, s[6:7]
	global_load_dwordx4 v[0:3], v[150:151], off
	global_load_dwordx4 v[4:7], v[152:153], off
	global_load_dwordx4 v[8:11], v[154:155], off offset:64
	global_load_dwordx4 v[12:15], v[156:157], off offset:64
	global_load_dwordx4 v[16:19], v[154:155], off offset:32
	global_load_dwordx4 v[20:23], v[156:157], off offset:32
	global_load_dwordx4 v[24:27], v[158:159], off offset:64
	global_load_dwordx4 v[28:31], v[160:161], off offset:64
	v_permlane32_swap_b32_e32 v68, v60
	v_permlane32_swap_b32_e32 v69, v61
	v_permlane32_swap_b32_e32 v64, v52
	v_permlane32_swap_b32_e32 v65, v53
	v_permlane32_swap_b32_e32 v70, v62
	v_permlane32_swap_b32_e32 v71, v63
	v_permlane32_swap_b32_e32 v66, v54
	v_permlane32_swap_b32_e32 v67, v55
	v_permlane32_swap_b32_e32 v76, v56
	v_permlane32_swap_b32_e32 v77, v57
	v_permlane32_swap_b32_e32 v72, v48
	v_permlane32_swap_b32_e32 v73, v49
	v_permlane32_swap_b32_e32 v78, v58
	v_permlane32_swap_b32_e32 v79, v59
	v_permlane32_swap_b32_e32 v74, v50
	v_permlane32_swap_b32_e32 v75, v51
	s_waitcnt vmcnt(7)
	v_pk_mul_f32 v[0:1], v[0:1], v[68:69]
	s_nop 0
	v_pk_mul_f32 v[32:33], v[0:1], s[2:3] op_sel_hi:[1,0]
	s_waitcnt vmcnt(5)
	v_pk_mul_f32 v[8:9], v[8:9], v[64:65]
	v_exp_f32_e32 v32, v32
	v_pk_mul_f32 v[36:37], v[8:9], s[2:3] op_sel_hi:[1,0]
	v_exp_f32_e32 v33, v33
	v_exp_f32_e32 v36, v36
	v_exp_f32_e32 v37, v37
	s_waitcnt vmcnt(3)
	v_pk_mul_f32 v[18:19], v[18:19], v[62:63]
	v_pk_mul_f32 v[2:3], v[2:3], v[70:71]
	v_pk_mul_f32 v[10:11], v[10:11], v[66:67]
	v_pk_mul_f32 v[42:43], v[18:19], s[2:3] op_sel_hi:[1,0]
	v_pk_add_f32 v[32:33], v[32:33], 1.0 op_sel_hi:[1,0]
	v_pk_add_f32 v[36:37], v[36:37], 1.0 op_sel_hi:[1,0]
	v_pk_mul_f32 v[16:17], v[16:17], v[60:61]
	v_pk_mul_f32 v[34:35], v[2:3], s[2:3] op_sel_hi:[1,0]
	v_pk_mul_f32 v[38:39], v[10:11], s[2:3] op_sel_hi:[1,0]
	v_exp_f32_e32 v42, v42
	v_exp_f32_e32 v43, v43
	v_rcp_f32_e32 v32, v32
	v_rcp_f32_e32 v33, v33
	v_rcp_f32_e32 v36, v36
	v_rcp_f32_e32 v37, v37
	v_pk_mul_f32 v[40:41], v[16:17], s[2:3] op_sel_hi:[1,0]
	v_exp_f32_e32 v34, v34
	v_exp_f32_e32 v35, v35
	v_exp_f32_e32 v38, v38
	v_exp_f32_e32 v39, v39
	v_exp_f32_e32 v40, v40
	v_exp_f32_e32 v41, v41
	v_pk_mul_f32 v[4:5], v[4:5], v[76:77]
	v_pk_mul_f32 v[12:13], v[12:13], v[72:73]
	v_pk_add_f32 v[42:43], v[42:43], 1.0 op_sel_hi:[1,0]
	v_pk_mul_f32 v[0:1], v[0:1], v[32:33]
	v_pk_mul_f32 v[8:9], v[8:9], v[36:37]
	v_pk_add_f32 v[34:35], v[34:35], 1.0 op_sel_hi:[1,0]
	v_pk_add_f32 v[38:39], v[38:39], 1.0 op_sel_hi:[1,0]
	v_pk_mul_f32 v[0:1], v[4:5], v[0:1]
	v_pk_mul_f32 v[4:5], v[12:13], v[8:9]
	v_rcp_f32_e32 v8, v42
	v_rcp_f32_e32 v9, v43
	v_pk_add_f32 v[40:41], v[40:41], 1.0 op_sel_hi:[1,0]
	v_rcp_f32_e32 v34, v34
	v_rcp_f32_e32 v35, v35
	v_rcp_f32_e32 v38, v38
	v_rcp_f32_e32 v39, v39
	v_rcp_f32_e32 v40, v40
	v_rcp_f32_e32 v41, v41
	s_waitcnt vmcnt(2)
	v_pk_mul_f32 v[12:13], v[22:23], v[58:59]
	v_pk_mul_f32 v[8:9], v[18:19], v[8:9]
	v_pk_mul_f32 v[6:7], v[6:7], v[78:79]
	v_pk_mul_f32 v[14:15], v[14:15], v[74:75]
	v_pk_mul_f32 v[2:3], v[2:3], v[34:35]
	v_pk_mul_f32 v[10:11], v[10:11], v[38:39]
	v_pk_mul_f32 v[8:9], v[12:13], v[8:9]
	s_waitcnt vmcnt(1)
	v_pk_mul_f32 v[12:13], v[24:25], v[52:53]
	v_pk_mul_f32 v[20:21], v[20:21], v[56:57]
	v_pk_mul_f32 v[2:3], v[6:7], v[2:3]
	v_pk_mul_f32 v[6:7], v[14:15], v[10:11]
	v_pk_mul_f32 v[10:11], v[16:17], v[40:41]
	v_pk_mul_f32 v[16:17], v[12:13], s[2:3] op_sel_hi:[1,0]
	v_pk_mul_f32 v[18:19], v[26:27], v[54:55]
	v_pk_mul_f32 v[10:11], v[20:21], v[10:11]
	v_exp_f32_e32 v16, v16
	v_exp_f32_e32 v17, v17
	v_pk_mul_f32 v[20:21], v[18:19], s[2:3] op_sel_hi:[1,0]
	s_waitcnt vmcnt(0)
	v_pk_mul_f32 v[14:15], v[28:29], v[48:49]
	v_exp_f32_e32 v20, v20
	v_exp_f32_e32 v21, v21
	v_pk_add_f32 v[16:17], v[16:17], 1.0 op_sel_hi:[1,0]
	v_pk_add_f32 v[20:21], v[20:21], 1.0 op_sel_hi:[1,0]
	v_rcp_f32_e32 v16, v16
	v_rcp_f32_e32 v17, v17
	v_rcp_f32_e32 v20, v20
	v_rcp_f32_e32 v21, v21
	v_pk_mul_f32 v[12:13], v[12:13], v[16:17]
	s_nop 0
	v_pk_mul_f32 v[12:13], v[14:15], v[12:13]
	v_pk_mul_f32 v[14:15], v[30:31], v[50:51]
	v_pk_mul_f32 v[16:17], v[18:19], v[20:21]
	v_max_f32_e64 v18, |v6|, |v7|
	v_pk_mul_f32 v[14:15], v[14:15], v[16:17]
	v_max_f32_e64 v16, |v0|, |v1|
	v_max_f32_e64 v17, |v2|, |v3|
	v_max3_f32 v16, v16, 0, v17
	v_max_f32_e64 v17, |v4|, |v5|
	v_max3_f32 v16, v16, v17, v18
	v_max_f32_e64 v17, |v10|, |v11|
	v_max_f32_e64 v18, |v8|, |v9|
	v_max3_f32 v16, v16, v17, v18
	v_max_f32_e64 v17, |v12|, |v13|
	v_max_f32_e64 v18, |v14|, |v15|
	v_max3_f32 v16, v16, v17, v18
	v_mov_b32_e32 v17, v16
	s_nop 1
	v_permlane16_swap_b32_e32 v16, v17
	v_max_f32_e32 v17, v17, v17
	v_max_f32_e32 v16, v16, v16
	v_max_f32_e32 v16, v16, v17
	v_lshrrev_b32_e32 v17, 23, v16
	v_and_b32_e32 v16, 0x7fffff, v16
	v_cmp_lt_u32_e32 vcc, s3, v16
	s_nop 1
	v_addc_co_u32_e32 v16, vcc, v17, v82, vcc
	v_med3_i32 v48, v16, s5, v83
	v_lshlrev_b32_e32 v16, 23, v48
	v_sub_u32_e32 v16, 1.0, v16
	v_pk_mul_f32 v[40:41], v[16:17], v[10:11] op_sel_hi:[0,1]
	v_pk_mul_f32 v[42:43], v[16:17], v[8:9] op_sel_hi:[0,1]
	v_pk_mul_f32 v[44:45], v[16:17], v[12:13] op_sel_hi:[0,1]
	v_pk_mul_f32 v[46:47], v[16:17], v[14:15] op_sel_hi:[0,1]
	v_pk_mul_f32 v[32:33], v[16:17], v[0:1] op_sel_hi:[0,1]
	v_pk_mul_f32 v[34:35], v[16:17], v[2:3] op_sel_hi:[0,1]
	v_pk_mul_f32 v[36:37], v[16:17], v[4:5] op_sel_hi:[0,1]
	v_pk_mul_f32 v[38:39], v[16:17], v[6:7] op_sel_hi:[0,1]
	v_cvt_scalef32_2xpk16_fp6_f32 v[50:55], v[32:47], v[40:55], 1.0
	v_cvt_scalef32_pk32_f32_fp6 v[0:31], v[50:55], s8
	v_fma_f32 v16, v32, s4, v0
	v_fma_f32 v17, v33, s4, v2
	v_fma_f32 v18, v34, s4, v4
	v_fma_f32 v19, v35, s4, v6
	v_fma_f32 v20, v36, s4, v8
	v_fma_f32 v21, v37, s4, v10
	v_fma_f32 v22, v38, s4, v12
	v_fma_f32 v23, v39, s4, v14
	v_fma_f32 v24, v40, s4, v1
	v_fma_f32 v25, v41, s4, v3
	v_fma_f32 v26, v42, s4, v5
	v_fma_f32 v27, v43, s4, v7
	v_fma_f32 v28, v44, s4, v9
	v_fma_f32 v29, v45, s4, v11
	v_fma_f32 v30, v46, s4, v13
	v_fma_f32 v31, v47, s4, v15
	v_cvt_scalef32_2xpk16_fp6_f32 v[0:5], v[16:31], v[24:39], 1.0
	v_xor_b32_e32 v4, 0x20820820, v0
	v_or_b32_e32 v0, 48, v163
	v_xor_b32_e32 v5, 0x8208208, v1
	v_or_b32_e32 v1, v0, v162
	v_mul_u32_u24_e32 v80, 24, v1
	v_xor_b32_e32 v6, 0x82082082, v2
	v_lshl_add_u64 v[2:3], v[148:149], 0, v[80:81]
	v_lshl_add_u64 v[2:3], v[2:3], 0, v[144:145]
	global_store_dwordx3 v[2:3], v[50:52], off nt
	v_add_co_u32_e32 v2, vcc, 0x1000, v2
	s_nop 1
	v_addc_co_u32_e32 v3, vcc, 0, v3, vcc
	global_store_dwordx3 v[2:3], v[4:6], off offset:2048 nt
	s_and_saveexec_b64 s[2:3], s[0:1]
	s_cbranch_execz .LBB2_14
	v_mov_b32_e32 v2, 0x7a00
	v_add_u32_e32 v1, 0x7f, v48
	v_lshl_add_u32 v2, v48, 8, v2
	v_or_b32_e32 v2, v2, v1
	v_lshl_or_b32 v0, v0, 1, v162
	v_mov_b32_e32 v1, 0
	v_lshl_add_u64 v[0:1], v[146:147], 0, v[0:1]
	global_store_short v[0:1], v2, off

.LBB3_6:
	s_mov_b32 s0, 0
	s_ashr_i32 s1, s0, 31
	v_add_u32_e32 v26, s0, v0
	v_ashrrev_i32_e32 v0, 6, v26
	v_and_b32_e32 v0, -4, v0
	v_bfe_u32 v177, v26, 5, 1
	v_lshl_add_u32 v178, s12, 3, v0
	v_bfe_u32 v27, v26, 4, 1
	v_or_b32_e32 v0, v178, v177
	s_lshl_b64 s[4:5], s[0:1], 2
	v_lshlrev_b32_e32 v36, 5, v0
	v_lshlrev_b32_e32 v179, 2, v27
	s_add_u32 s4, s10, s4
	v_or_b32_e32 v30, v36, v179
	s_addc_u32 s5, s11, s5
	v_ashrrev_i32_e32 v31, 31, v30
	v_lshl_add_u64 v[170:171], v[30:31], 2, s[4:5]
	global_load_dwordx4 v[192:195], v[170:171], off
	v_ashrrev_i32_e32 v31, 31, v36
	v_lshl_add_u64 v[172:173], v[30:31], 2, s[4:5]
	global_load_dwordx4 v[196:199], v[172:173], off offset:64
	v_and_b32_e32 v181, 0xcf, v26
	v_mul_u32_u24_e32 v160, 12, v27
	v_cmp_eq_u32_e64 s[0:1], 0, v27
	global_load_dwordx4 v[200:203], v[172:173], off offset:32
	s_lshl_b32 s11, s8, 6
	v_ashrrev_i32_e32 v30, 1, v178
	v_or_b32_e32 v176, 8, v179
	v_add_u32_e32 v34, s11, v30
	s_movk_i32 s9, 0x6000
	v_mov_b64_e32 v[32:33], s[2:3]
	s_add_u32 s6, s2, 0x3000000
	v_ashrrev_i32_e32 v35, 31, v34
	v_or_b32_e32 v30, v36, v176
	s_addc_u32 s7, s3, 0
	v_mad_i64_i32 v[168:169], s[8:9], v34, s9, v[32:33]
	v_lshlrev_b64 v[32:33], 10, v[34:35]
	v_lshl_add_u64 v[174:175], v[30:31], 2, s[4:5]
	v_lshl_add_u64 v[166:167], s[6:7], 0, v[32:33]
	global_load_dwordx4 v[204:207], v[174:175], off offset:64
	global_load_dwordx4 v[208:211], v[170:171], off offset:256
	global_load_dwordx4 v[212:215], v[172:173], off offset:320
	global_load_dwordx4 v[216:219], v[172:173], off offset:288
	global_load_dwordx4 v[220:223], v[174:175], off offset:320
	v_permlane32_swap_b32_e32 v14, v6
	v_permlane32_swap_b32_e32 v15, v7
	v_permlane32_swap_b32_e32 v16, v8
	v_permlane32_swap_b32_e32 v17, v9
	v_permlane32_swap_b32_e32 v10, v2
	v_permlane32_swap_b32_e32 v11, v3
	s_mov_b32 s20, 0x3e6d3388
	s_mov_b32 s22, 0xbf3a00e3
	s_mov_b32 s16, 0x3f07dc22
	s_mov_b32 s14, 0xbf38aa3b
	v_mov_b64_e32 v[0:1], s[22:23]
	s_mov_b32 s18, 0x3f35f0e3
	s_mov_b32 s10, 0xbe11a98e
	s_mov_b32 s12, 0x3e027906
	v_permlane32_swap_b32_e32 v12, v4
	v_permlane32_swap_b32_e32 v13, v5
	s_mov_b32 s9, 0x700000
	v_mov_b32_e32 v182, 0xffffff7f
	v_mov_b32_e32 v183, 0x64
	s_mov_b32 s8, 0xc2000000
	v_lshlrev_b32_e32 v180, 9, v177
	v_mov_b32_e32 v161, 0
	v_mov_b32_e32 v165, v161
	v_lshl_or_b32 v162, v181, 1, v180
	s_waitcnt vmcnt(4)
	v_pk_mul_f32 v[14:15], v[192:193], v[14:15]
	s_nop 0
	v_and_b32_e32 v19, 0x7fffffff, v15
	v_and_b32_e32 v18, 0x7fffffff, v14
	v_pk_mul_f32 v[16:17], v[194:195], v[16:17]
	v_pk_mul_f32 v[10:11], v[196:197], v[10:11]
	v_pk_fma_f32 v[22:23], v[18:19], s[20:21], 1.0 op_sel_hi:[1,0,0]
	v_and_b32_e32 v35, 0x7fffffff, v17
	v_and_b32_e32 v34, 0x7fffffff, v16
	v_rcp_f32_e32 v22, v22
	v_rcp_f32_e32 v23, v23
	v_pk_fma_f32 v[38:39], v[34:35], s[20:21], 1.0 op_sel_hi:[1,0,0]
	v_pk_mul_f32 v[20:21], v[14:15], v[14:15]
	v_rcp_f32_e32 v38, v38
	v_rcp_f32_e32 v39, v39
	v_pk_mul_f32 v[20:21], v[20:21], s[14:15] op_sel_hi:[1,0]
	v_pk_fma_f32 v[44:45], v[22:23], s[16:17], v[0:1] op_sel_hi:[1,0,0]
	v_pk_mul_f32 v[36:37], v[16:17], v[16:17]
	v_exp_f32_e32 v20, v20
	v_exp_f32_e32 v21, v21
	v_pk_fma_f32 v[44:45], v[22:23], v[44:45], s[18:19] op_sel_hi:[1,1,0]
	v_pk_mul_f32 v[36:37], v[36:37], s[14:15] op_sel_hi:[1,0]
	v_pk_fma_f32 v[46:47], v[38:39], s[16:17], v[0:1] op_sel_hi:[1,0,0]
	v_pk_fma_f32 v[44:45], v[22:23], v[44:45], s[10:11] op_sel_hi:[1,1,0]
	v_and_b32_e32 v41, 0x7fffffff, v11
	v_and_b32_e32 v40, 0x7fffffff, v10
	v_exp_f32_e32 v36, v36
	v_exp_f32_e32 v37, v37
	v_pk_fma_f32 v[46:47], v[38:39], v[46:47], s[18:19] op_sel_hi:[1,1,0]
	v_pk_fma_f32 v[44:45], v[22:23], v[44:45], s[12:13] op_sel_hi:[1,1,0]
	v_pk_fma_f32 v[42:43], v[40:41], s[20:21], 1.0 op_sel_hi:[1,0,0]
	v_pk_fma_f32 v[46:47], v[38:39], v[46:47], s[10:11] op_sel_hi:[1,1,0]
	v_pk_mul_f32 v[22:23], v[22:23], v[44:45]
	v_rcp_f32_e32 v42, v42
	v_pk_fma_f32 v[46:47], v[38:39], v[46:47], s[12:13] op_sel_hi:[1,1,0]
	v_pk_fma_f32 v[20:21], v[20:21], v[22:23], 0.5 op_sel_hi:[1,1,0] neg_lo:[1,0,0] neg_hi:[1,0,0]
	v_rcp_f32_e32 v43, v43
	v_pk_mul_f32 v[38:39], v[38:39], v[46:47]
	v_pk_mul_f32 v[18:19], v[18:19], v[20:21]
	v_pk_mul_f32 v[20:21], v[10:11], v[10:11]
	v_pk_fma_f32 v[14:15], v[14:15], 0.5, v[18:19] op_sel_hi:[1,0,1]
	v_pk_fma_f32 v[18:19], v[36:37], v[38:39], 0.5 op_sel_hi:[1,1,0] neg_lo:[1,0,0] neg_hi:[1,0,0]
	v_pk_mul_f32 v[20:21], v[20:21], s[14:15] op_sel_hi:[1,0]
	v_pk_mul_f32 v[18:19], v[34:35], v[18:19]
	v_pk_mul_f32 v[12:13], v[198:199], v[12:13]
	v_pk_fma_f32 v[16:17], v[16:17], 0.5, v[18:19] op_sel_hi:[1,0,1]
	v_pk_fma_f32 v[18:19], v[42:43], s[16:17], v[0:1] op_sel_hi:[1,0,0]
	v_exp_f32_e32 v20, v20
	v_pk_fma_f32 v[18:19], v[42:43], v[18:19], s[18:19] op_sel_hi:[1,1,0]
	v_exp_f32_e32 v21, v21
	v_and_b32_e32 v23, 0x7fffffff, v13
	v_and_b32_e32 v22, 0x7fffffff, v12
	v_pk_fma_f32 v[18:19], v[42:43], v[18:19], s[10:11] op_sel_hi:[1,1,0]
	v_pk_fma_f32 v[24:25], v[22:23], s[20:21], 1.0 op_sel_hi:[1,0,0]
	v_pk_fma_f32 v[18:19], v[42:43], v[18:19], s[12:13] op_sel_hi:[1,1,0]
	v_rcp_f32_e32 v24, v24
	v_rcp_f32_e32 v25, v25
	v_pk_mul_f32 v[18:19], v[42:43], v[18:19]
	v_pk_mul_f32 v[6:7], v[200:201], v[6:7]
	v_pk_fma_f32 v[18:19], v[20:21], v[18:19], 0.5 op_sel_hi:[1,1,0] neg_lo:[1,0,0] neg_hi:[1,0,0]
	v_pk_mul_f32 v[20:21], v[12:13], v[12:13]
	v_pk_mul_f32 v[18:19], v[40:41], v[18:19]
	v_pk_mul_f32 v[20:21], v[20:21], s[14:15] op_sel_hi:[1,0]
	v_pk_fma_f32 v[10:11], v[10:11], 0.5, v[18:19] op_sel_hi:[1,0,1]
	v_pk_fma_f32 v[18:19], v[24:25], s[16:17], v[0:1] op_sel_hi:[1,0,0]
	v_exp_f32_e32 v20, v20
	v_pk_fma_f32 v[18:19], v[24:25], v[18:19], s[18:19] op_sel_hi:[1,1,0]
	v_exp_f32_e32 v21, v21
	v_pk_fma_f32 v[18:19], v[24:25], v[18:19], s[10:11] op_sel_hi:[1,1,0]
	v_pk_mul_f32 v[8:9], v[202:203], v[8:9]
	v_pk_fma_f32 v[18:19], v[24:25], v[18:19], s[12:13] op_sel_hi:[1,1,0]
	v_pk_mul_f32 v[2:3], v[204:205], v[2:3]
	v_pk_mul_f32 v[18:19], v[24:25], v[18:19]
	v_and_b32_e32 v25, 0x7fffffff, v7
	v_and_b32_e32 v24, 0x7fffffff, v6
	v_pk_fma_f32 v[26:27], v[24:25], s[20:21], 1.0 op_sel_hi:[1,0,0]
	v_pk_fma_f32 v[18:19], v[20:21], v[18:19], 0.5 op_sel_hi:[1,1,0] neg_lo:[1,0,0] neg_hi:[1,0,0]
	v_rcp_f32_e32 v26, v26
	v_rcp_f32_e32 v27, v27
	v_pk_mul_f32 v[18:19], v[22:23], v[18:19]
	v_pk_mul_f32 v[20:21], v[6:7], v[6:7]
	v_pk_fma_f32 v[12:13], v[12:13], 0.5, v[18:19] op_sel_hi:[1,0,1]
	v_pk_fma_f32 v[18:19], v[26:27], s[16:17], v[0:1] op_sel_hi:[1,0,0]
	v_pk_mul_f32 v[20:21], v[20:21], s[14:15] op_sel_hi:[1,0]
	v_pk_fma_f32 v[18:19], v[26:27], v[18:19], s[18:19] op_sel_hi:[1,1,0]
	v_exp_f32_e32 v20, v20
	v_pk_fma_f32 v[18:19], v[26:27], v[18:19], s[10:11] op_sel_hi:[1,1,0]
	v_exp_f32_e32 v21, v21
	v_pk_fma_f32 v[18:19], v[26:27], v[18:19], s[12:13] op_sel_hi:[1,1,0]
	v_and_b32_e32 v23, 0x7fffffff, v9
	v_and_b32_e32 v22, 0x7fffffff, v8
	v_pk_mul_f32 v[18:19], v[26:27], v[18:19]
	v_pk_fma_f32 v[26:27], v[22:23], s[20:21], 1.0 op_sel_hi:[1,0,0]
	v_pk_fma_f32 v[18:19], v[20:21], v[18:19], 0.5 op_sel_hi:[1,1,0] neg_lo:[1,0,0] neg_hi:[1,0,0]
	v_rcp_f32_e32 v26, v26
	v_rcp_f32_e32 v27, v27
	v_pk_mul_f32 v[18:19], v[24:25], v[18:19]
	v_pk_mul_f32 v[20:21], v[8:9], v[8:9]
	v_pk_fma_f32 v[6:7], v[6:7], 0.5, v[18:19] op_sel_hi:[1,0,1]
	v_pk_fma_f32 v[18:19], v[26:27], s[16:17], v[0:1] op_sel_hi:[1,0,0]
	v_pk_mul_f32 v[20:21], v[20:21], s[14:15] op_sel_hi:[1,0]
	v_pk_fma_f32 v[18:19], v[26:27], v[18:19], s[18:19] op_sel_hi:[1,1,0]
	v_exp_f32_e32 v20, v20
	v_pk_fma_f32 v[18:19], v[26:27], v[18:19], s[10:11] op_sel_hi:[1,1,0]
	v_exp_f32_e32 v21, v21
	v_pk_fma_f32 v[18:19], v[26:27], v[18:19], s[12:13] op_sel_hi:[1,1,0]
	v_and_b32_e32 v25, 0x7fffffff, v3
	v_and_b32_e32 v24, 0x7fffffff, v2
	v_pk_mul_f32 v[18:19], v[26:27], v[18:19]
	v_pk_fma_f32 v[26:27], v[24:25], s[20:21], 1.0 op_sel_hi:[1,0,0]
	v_pk_fma_f32 v[18:19], v[20:21], v[18:19], 0.5 op_sel_hi:[1,1,0] neg_lo:[1,0,0] neg_hi:[1,0,0]
	v_rcp_f32_e32 v26, v26
	v_rcp_f32_e32 v27, v27
	v_pk_mul_f32 v[18:19], v[22:23], v[18:19]
	v_pk_mul_f32 v[20:21], v[2:3], v[2:3]
	v_pk_fma_f32 v[8:9], v[8:9], 0.5, v[18:19] op_sel_hi:[1,0,1]
	v_pk_fma_f32 v[18:19], v[26:27], s[16:17], v[0:1] op_sel_hi:[1,0,0]
	v_pk_mul_f32 v[20:21], v[20:21], s[14:15] op_sel_hi:[1,0]
	v_pk_fma_f32 v[18:19], v[26:27], v[18:19], s[18:19] op_sel_hi:[1,1,0]
	v_exp_f32_e32 v20, v20
	v_pk_fma_f32 v[18:19], v[26:27], v[18:19], s[10:11] op_sel_hi:[1,1,0]
	v_exp_f32_e32 v21, v21
	v_pk_mul_f32 v[4:5], v[206:207], v[4:5]
	v_pk_fma_f32 v[18:19], v[26:27], v[18:19], s[12:13] op_sel_hi:[1,1,0]
	v_and_b32_e32 v23, 0x7fffffff, v5
	v_and_b32_e32 v22, 0x7fffffff, v4
	v_pk_mul_f32 v[18:19], v[26:27], v[18:19]
	v_pk_fma_f32 v[26:27], v[22:23], s[20:21], 1.0 op_sel_hi:[1,0,0]
	v_pk_fma_f32 v[18:19], v[20:21], v[18:19], 0.5 op_sel_hi:[1,1,0] neg_lo:[1,0,0] neg_hi:[1,0,0]
	v_rcp_f32_e32 v26, v26
	v_rcp_f32_e32 v27, v27
	v_pk_mul_f32 v[18:19], v[24:25], v[18:19]
	v_pk_fma_f32 v[0:1], v[26:27], s[16:17], v[0:1] op_sel_hi:[1,0,0]
	v_pk_fma_f32 v[2:3], v[2:3], 0.5, v[18:19] op_sel_hi:[1,0,1]
	v_pk_mul_f32 v[18:19], v[4:5], v[4:5]
	v_pk_fma_f32 v[0:1], v[26:27], v[0:1], s[18:19] op_sel_hi:[1,1,0]
	v_pk_mul_f32 v[18:19], v[18:19], s[14:15] op_sel_hi:[1,0]
	v_pk_fma_f32 v[0:1], v[26:27], v[0:1], s[10:11] op_sel_hi:[1,1,0]
	v_exp_f32_e32 v18, v18
	v_exp_f32_e32 v19, v19
	v_pk_fma_f32 v[0:1], v[26:27], v[0:1], s[12:13] op_sel_hi:[1,1,0]
	s_movk_i32 s13, 0xff9c
	v_pk_mul_f32 v[0:1], v[26:27], v[0:1]
	s_mov_b32 s15, 0x42000000
	v_pk_fma_f32 v[0:1], v[18:19], v[0:1], 0.5 op_sel_hi:[1,1,0] neg_lo:[1,0,0] neg_hi:[1,0,0]
	v_max_f32_e64 v18, |v12|, |v13|
	v_pk_mul_f32 v[0:1], v[22:23], v[0:1]
	s_nop 0
	v_pk_fma_f32 v[0:1], v[4:5], 0.5, v[0:1] op_sel_hi:[1,0,1]
	v_max_f32_e64 v4, |v14|, |v15|
	v_max_f32_e64 v5, |v16|, |v17|
	v_max3_f32 v4, v4, 0, v5
	v_max_f32_e64 v5, |v10|, |v11|
	v_max3_f32 v4, v4, v5, v18
	v_max_f32_e64 v5, |v6|, |v7|
	v_max_f32_e64 v18, |v8|, |v9|
	v_max3_f32 v4, v4, v5, v18
	v_max_f32_e64 v5, |v2|, |v3|
	v_max_f32_e64 v18, |v0|, |v1|
	v_max3_f32 v4, v4, v5, v18
	v_mov_b32_e32 v5, v4
	s_nop 1
	v_permlane16_swap_b32_e32 v4, v5
	v_max_f32_e32 v5, v5, v5
	v_max_f32_e32 v4, v4, v4
	v_max_f32_e32 v4, v4, v5
	v_lshrrev_b32_e32 v5, 23, v4
	v_and_b32_e32 v4, 0x7fffff, v4
	v_cmp_lt_u32_e32 vcc, s9, v4
	s_nop 1
	v_addc_co_u32_e32 v4, vcc, v5, v182, vcc
	v_med3_i32 v163, v4, s13, v183
	v_lshlrev_b32_e32 v4, 23, v163
	v_sub_u32_e32 v4, 1.0, v4
	v_pk_mul_f32 v[40:41], v[4:5], v[6:7] op_sel_hi:[0,1]
	v_pk_mul_f32 v[42:43], v[4:5], v[8:9] op_sel_hi:[0,1]
	v_pk_mul_f32 v[44:45], v[4:5], v[2:3] op_sel_hi:[0,1]
	v_pk_mul_f32 v[46:47], v[4:5], v[0:1] op_sel_hi:[0,1]
	v_pk_mul_f32 v[32:33], v[4:5], v[14:15] op_sel_hi:[0,1]
	v_pk_mul_f32 v[34:35], v[4:5], v[16:17] op_sel_hi:[0,1]
	v_pk_mul_f32 v[36:37], v[4:5], v[10:11] op_sel_hi:[0,1]
	v_pk_mul_f32 v[38:39], v[4:5], v[12:13] op_sel_hi:[0,1]
	v_cvt_scalef32_2xpk16_fp6_f32 v[184:189], v[32:47], v[40:55], 1.0
	v_cvt_scalef32_pk32_f32_fp6 v[0:31], v[184:189], s15
	v_fma_f32 v16, v32, s8, v0
	v_fma_f32 v17, v33, s8, v2
	v_fma_f32 v18, v34, s8, v4
	v_fma_f32 v19, v35, s8, v6
	v_fma_f32 v20, v36, s8, v8
	v_fma_f32 v21, v37, s8, v10
	v_fma_f32 v22, v38, s8, v12
	v_fma_f32 v23, v39, s8, v14
	v_fma_f32 v24, v40, s8, v1
	v_fma_f32 v25, v41, s8, v3
	v_fma_f32 v26, v42, s8, v5
	v_fma_f32 v27, v43, s8, v7
	v_fma_f32 v28, v44, s8, v9
	v_fma_f32 v29, v45, s8, v11
	v_fma_f32 v30, v46, s8, v13
	v_fma_f32 v31, v47, s8, v15
	v_cvt_scalef32_2xpk16_fp6_f32 v[0:5], v[16:31], v[24:39], 1.0
	v_or_b32_e32 v3, v181, v180
	v_mul_u32_u24_e32 v164, 24, v3
	v_lshl_add_u64 v[4:5], v[168:169], 0, v[164:165]
	v_lshl_add_u64 v[4:5], v[4:5], 0, v[160:161]
	global_store_dwordx3 v[4:5], v[184:186], off nt
	v_add_co_u32_e32 v4, vcc, 0x1000, v4
	v_xor_b32_e32 v0, 0x20820820, v0
	v_xor_b32_e32 v1, 0x8208208, v1
	v_xor_b32_e32 v2, 0x82082082, v2
	v_addc_co_u32_e32 v5, vcc, 0, v5, vcc
	global_store_dwordx3 v[4:5], v[0:2], off offset:2048 nt
	s_and_saveexec_b64 s[24:25], s[0:1]
	s_cbranch_execz .LBB3_8
	v_mov_b32_e32 v1, 0x7a00
	v_add_u32_e32 v0, 0x7f, v163
	v_lshl_add_u32 v1, v163, 8, v1
	v_mov_b32_e32 v163, v161
	v_or_b32_e32 v2, v1, v0
	v_lshl_add_u64 v[0:1], v[166:167], 0, v[162:163]
	global_store_short v[0:1], v2, off
.LBB3_8:
	s_or_b64 exec, exec, s[24:25]
	v_permlane32_swap_b32_e32 v156, v148
	v_permlane32_swap_b32_e32 v157, v149
	v_permlane32_swap_b32_e32 v158, v150
	v_permlane32_swap_b32_e32 v159, v151
	v_permlane32_swap_b32_e32 v154, v146
	v_permlane32_swap_b32_e32 v155, v147
	v_permlane32_swap_b32_e32 v152, v144
	v_permlane32_swap_b32_e32 v153, v145
	v_mov_b64_e32 v[16:17], s[22:23]
	v_pk_mul_f32 v[0:1], v[192:193], v[156:157]
	v_pk_mul_f32 v[2:3], v[194:195], v[158:159]
	v_and_b32_e32 v19, 0x7fffffff, v1
	v_and_b32_e32 v18, 0x7fffffff, v0
	v_pk_mul_f32 v[6:7], v[198:199], v[154:155]
	v_and_b32_e32 v23, 0x7fffffff, v3
	v_and_b32_e32 v22, 0x7fffffff, v2
	v_pk_fma_f32 v[36:37], v[18:19], s[20:21], 1.0 op_sel_hi:[1,0,0]
	v_pk_mul_f32 v[4:5], v[196:197], v[152:153]
	v_and_b32_e32 v31, 0x7fffffff, v7
	v_and_b32_e32 v30, 0x7fffffff, v6
	v_pk_fma_f32 v[38:39], v[22:23], s[20:21], 1.0 op_sel_hi:[1,0,0]
	v_rcp_f32_e32 v36, v36
	v_rcp_f32_e32 v37, v37
	v_and_b32_e32 v27, 0x7fffffff, v5
	v_and_b32_e32 v26, 0x7fffffff, v4
	v_pk_fma_f32 v[42:43], v[30:31], s[20:21], 1.0 op_sel_hi:[1,0,0]
	v_rcp_f32_e32 v38, v38
	v_rcp_f32_e32 v39, v39
	v_pk_fma_f32 v[40:41], v[26:27], s[20:21], 1.0 op_sel_hi:[1,0,0]
	v_rcp_f32_e32 v42, v42
	v_rcp_f32_e32 v43, v43
	v_pk_mul_f32 v[20:21], v[0:1], v[0:1]
	v_rcp_f32_e32 v40, v40
	v_rcp_f32_e32 v41, v41
	v_pk_mul_f32 v[24:25], v[2:3], v[2:3]
	v_pk_mul_f32 v[20:21], v[20:21], s[14:15] op_sel_hi:[1,0]
	v_pk_fma_f32 v[46:47], v[36:37], s[16:17], v[16:17] op_sel_hi:[1,0,0]
	v_pk_mul_f32 v[8:9], v[200:201], v[148:149]
	v_pk_mul_f32 v[32:33], v[6:7], v[6:7]
	v_pk_mul_f32 v[24:25], v[24:25], s[14:15] op_sel_hi:[1,0]
	v_exp_f32_e32 v20, v20
	v_exp_f32_e32 v21, v21
	v_pk_fma_f32 v[148:149], v[38:39], s[16:17], v[16:17] op_sel_hi:[1,0,0]
	v_pk_fma_f32 v[46:47], v[36:37], v[46:47], s[18:19] op_sel_hi:[1,1,0]
	v_pk_mul_f32 v[28:29], v[4:5], v[4:5]
	v_pk_mul_f32 v[32:33], v[32:33], s[14:15] op_sel_hi:[1,0]
	v_exp_f32_e32 v24, v24
	v_exp_f32_e32 v25, v25
	v_pk_fma_f32 v[154:155], v[42:43], s[16:17], v[16:17] op_sel_hi:[1,0,0]
	v_pk_fma_f32 v[148:149], v[38:39], v[148:149], s[18:19] op_sel_hi:[1,1,0]
	v_pk_fma_f32 v[46:47], v[36:37], v[46:47], s[10:11] op_sel_hi:[1,1,0]
	v_and_b32_e32 v35, 0x7fffffff, v9
	v_and_b32_e32 v34, 0x7fffffff, v8
	v_pk_mul_f32 v[28:29], v[28:29], s[14:15] op_sel_hi:[1,0]
	v_exp_f32_e32 v32, v32
	v_exp_f32_e32 v33, v33
	v_pk_fma_f32 v[152:153], v[40:41], s[16:17], v[16:17] op_sel_hi:[1,0,0]
	v_pk_fma_f32 v[154:155], v[42:43], v[154:155], s[18:19] op_sel_hi:[1,1,0]
	v_pk_fma_f32 v[148:149], v[38:39], v[148:149], s[10:11] op_sel_hi:[1,1,0]
	v_pk_fma_f32 v[46:47], v[36:37], v[46:47], s[12:13] op_sel_hi:[1,1,0]
	v_pk_fma_f32 v[44:45], v[34:35], s[20:21], 1.0 op_sel_hi:[1,0,0]
	v_exp_f32_e32 v28, v28
	v_exp_f32_e32 v29, v29
	v_pk_fma_f32 v[152:153], v[40:41], v[152:153], s[18:19] op_sel_hi:[1,1,0]
	v_pk_fma_f32 v[154:155], v[42:43], v[154:155], s[10:11] op_sel_hi:[1,1,0]
	v_pk_fma_f32 v[148:149], v[38:39], v[148:149], s[12:13] op_sel_hi:[1,1,0]
	v_pk_mul_f32 v[36:37], v[36:37], v[46:47]
	v_rcp_f32_e32 v44, v44
	v_pk_fma_f32 v[152:153], v[40:41], v[152:153], s[10:11] op_sel_hi:[1,1,0]
	v_pk_fma_f32 v[154:155], v[42:43], v[154:155], s[12:13] op_sel_hi:[1,1,0]
	v_pk_mul_f32 v[38:39], v[38:39], v[148:149]
	v_pk_fma_f32 v[20:21], v[20:21], v[36:37], 0.5 op_sel_hi:[1,1,0] neg_lo:[1,0,0] neg_hi:[1,0,0]
	v_rcp_f32_e32 v45, v45
	v_pk_fma_f32 v[152:153], v[40:41], v[152:153], s[12:13] op_sel_hi:[1,1,0]
	v_pk_mul_f32 v[42:43], v[42:43], v[154:155]
	v_pk_fma_f32 v[24:25], v[24:25], v[38:39], 0.5 op_sel_hi:[1,1,0] neg_lo:[1,0,0] neg_hi:[1,0,0]
	v_pk_mul_f32 v[18:19], v[18:19], v[20:21]
	v_pk_mul_f32 v[40:41], v[40:41], v[152:153]
	v_pk_mul_f32 v[20:21], v[22:23], v[24:25]
	v_pk_fma_f32 v[0:1], v[0:1], 0.5, v[18:19] op_sel_hi:[1,0,1]
	v_pk_fma_f32 v[18:19], v[32:33], v[42:43], 0.5 op_sel_hi:[1,1,0] neg_lo:[1,0,0] neg_hi:[1,0,0]
	v_pk_fma_f32 v[28:29], v[28:29], v[40:41], 0.5 op_sel_hi:[1,1,0] neg_lo:[1,0,0] neg_hi:[1,0,0]
	v_pk_fma_f32 v[2:3], v[2:3], 0.5, v[20:21] op_sel_hi:[1,0,1]
	v_pk_mul_f32 v[18:19], v[30:31], v[18:19]
	v_pk_mul_f32 v[20:21], v[8:9], v[8:9]
	v_pk_mul_f32 v[22:23], v[26:27], v[28:29]
	v_pk_fma_f32 v[6:7], v[6:7], 0.5, v[18:19] op_sel_hi:[1,0,1]
	v_pk_fma_f32 v[18:19], v[44:45], s[16:17], v[16:17] op_sel_hi:[1,0,0]
	v_pk_mul_f32 v[20:21], v[20:21], s[14:15] op_sel_hi:[1,0]
	v_pk_mul_f32 v[10:11], v[202:203], v[150:151]
	v_pk_fma_f32 v[4:5], v[4:5], 0.5, v[22:23] op_sel_hi:[1,0,1]
	v_pk_fma_f32 v[18:19], v[44:45], v[18:19], s[18:19] op_sel_hi:[1,1,0]
	v_exp_f32_e32 v20, v20
	v_exp_f32_e32 v21, v21
	v_and_b32_e32 v23, 0x7fffffff, v11
	v_and_b32_e32 v22, 0x7fffffff, v10
	v_pk_fma_f32 v[18:19], v[44:45], v[18:19], s[10:11] op_sel_hi:[1,1,0]
	v_pk_fma_f32 v[24:25], v[22:23], s[20:21], 1.0 op_sel_hi:[1,0,0]
	v_pk_fma_f32 v[18:19], v[44:45], v[18:19], s[12:13] op_sel_hi:[1,1,0]
	v_rcp_f32_e32 v24, v24
	v_rcp_f32_e32 v25, v25
	v_pk_mul_f32 v[18:19], v[44:45], v[18:19]
	v_pk_mul_f32 v[12:13], v[204:205], v[144:145]
	v_pk_fma_f32 v[18:19], v[20:21], v[18:19], 0.5 op_sel_hi:[1,1,0] neg_lo:[1,0,0] neg_hi:[1,0,0]
	v_pk_mul_f32 v[20:21], v[10:11], v[10:11]
	v_pk_mul_f32 v[18:19], v[34:35], v[18:19]
	v_pk_mul_f32 v[20:21], v[20:21], s[14:15] op_sel_hi:[1,0]
	v_pk_fma_f32 v[8:9], v[8:9], 0.5, v[18:19] op_sel_hi:[1,0,1]
	v_pk_fma_f32 v[18:19], v[24:25], s[16:17], v[16:17] op_sel_hi:[1,0,0]
	v_exp_f32_e32 v20, v20
	v_pk_fma_f32 v[18:19], v[24:25], v[18:19], s[18:19] op_sel_hi:[1,1,0]
	v_exp_f32_e32 v21, v21
	v_pk_fma_f32 v[18:19], v[24:25], v[18:19], s[10:11] op_sel_hi:[1,1,0]
	v_pk_mul_f32 v[14:15], v[206:207], v[146:147]
	v_pk_fma_f32 v[18:19], v[24:25], v[18:19], s[12:13] op_sel_hi:[1,1,0]
	v_mov_b32_e32 v147, v161
	v_pk_mul_f32 v[18:19], v[24:25], v[18:19]
	v_and_b32_e32 v25, 0x7fffffff, v13
	v_and_b32_e32 v24, 0x7fffffff, v12
	v_pk_fma_f32 v[26:27], v[24:25], s[20:21], 1.0 op_sel_hi:[1,0,0]
	v_pk_fma_f32 v[18:19], v[20:21], v[18:19], 0.5 op_sel_hi:[1,1,0] neg_lo:[1,0,0] neg_hi:[1,0,0]
	v_rcp_f32_e32 v26, v26
	v_rcp_f32_e32 v27, v27
	v_pk_mul_f32 v[18:19], v[22:23], v[18:19]
	v_pk_mul_f32 v[20:21], v[12:13], v[12:13]
	v_pk_fma_f32 v[10:11], v[10:11], 0.5, v[18:19] op_sel_hi:[1,0,1]
	v_pk_fma_f32 v[18:19], v[26:27], s[16:17], v[16:17] op_sel_hi:[1,0,0]
	v_pk_mul_f32 v[20:21], v[20:21], s[14:15] op_sel_hi:[1,0]
	v_pk_fma_f32 v[18:19], v[26:27], v[18:19], s[18:19] op_sel_hi:[1,1,0]
	v_exp_f32_e32 v20, v20
	v_pk_fma_f32 v[18:19], v[26:27], v[18:19], s[10:11] op_sel_hi:[1,1,0]
	v_exp_f32_e32 v21, v21
	v_pk_fma_f32 v[18:19], v[26:27], v[18:19], s[12:13] op_sel_hi:[1,1,0]
	v_and_b32_e32 v23, 0x7fffffff, v15
	v_and_b32_e32 v22, 0x7fffffff, v14
	v_pk_mul_f32 v[18:19], v[26:27], v[18:19]
	v_pk_fma_f32 v[26:27], v[22:23], s[20:21], 1.0 op_sel_hi:[1,0,0]
	v_pk_fma_f32 v[18:19], v[20:21], v[18:19], 0.5 op_sel_hi:[1,1,0] neg_lo:[1,0,0] neg_hi:[1,0,0]
	v_rcp_f32_e32 v26, v26
	v_rcp_f32_e32 v27, v27
	v_pk_mul_f32 v[18:19], v[24:25], v[18:19]
	v_pk_fma_f32 v[16:17], v[26:27], s[16:17], v[16:17] op_sel_hi:[1,0,0]
	v_pk_fma_f32 v[12:13], v[12:13], 0.5, v[18:19] op_sel_hi:[1,0,1]
	v_pk_mul_f32 v[18:19], v[14:15], v[14:15]
	v_pk_fma_f32 v[16:17], v[26:27], v[16:17], s[18:19] op_sel_hi:[1,1,0]
	v_pk_mul_f32 v[18:19], v[18:19], s[14:15] op_sel_hi:[1,0]
	v_pk_fma_f32 v[16:17], v[26:27], v[16:17], s[10:11] op_sel_hi:[1,1,0]
	v_exp_f32_e32 v18, v18
	v_exp_f32_e32 v19, v19
	v_pk_fma_f32 v[16:17], v[26:27], v[16:17], s[12:13] op_sel_hi:[1,1,0]
	s_nop 0
	v_pk_mul_f32 v[16:17], v[26:27], v[16:17]
	s_nop 0
	v_pk_fma_f32 v[16:17], v[18:19], v[16:17], 0.5 op_sel_hi:[1,1,0] neg_lo:[1,0,0] neg_hi:[1,0,0]
	v_max_f32_e64 v18, |v6|, |v7|
	v_pk_mul_f32 v[16:17], v[22:23], v[16:17]
	s_nop 0
	v_pk_fma_f32 v[14:15], v[14:15], 0.5, v[16:17] op_sel_hi:[1,0,1]
	v_max_f32_e64 v16, |v0|, |v1|
	v_max_f32_e64 v17, |v2|, |v3|
	v_max3_f32 v16, v16, 0, v17
	v_max_f32_e64 v17, |v4|, |v5|
	v_max3_f32 v16, v16, v17, v18
	v_max_f32_e64 v17, |v8|, |v9|
	v_max_f32_e64 v18, |v10|, |v11|
	v_max3_f32 v16, v16, v17, v18
	v_max_f32_e64 v17, |v12|, |v13|
	v_max_f32_e64 v18, |v14|, |v15|
	v_max3_f32 v16, v16, v17, v18
	v_mov_b32_e32 v17, v16
	s_nop 1
	v_permlane16_swap_b32_e32 v16, v17
	v_max_f32_e32 v17, v17, v17
	v_max_f32_e32 v16, v16, v16
	v_max_f32_e32 v16, v16, v17
	v_lshrrev_b32_e32 v17, 23, v16
	v_and_b32_e32 v16, 0x7fffff, v16
	v_cmp_lt_u32_e32 vcc, s9, v16
	s_nop 1
	v_addc_co_u32_e32 v16, vcc, v17, v182, vcc
	v_med3_i32 v145, v16, s13, v183
	v_lshlrev_b32_e32 v16, 23, v145
	v_sub_u32_e32 v16, 1.0, v16
	v_pk_mul_f32 v[40:41], v[16:17], v[8:9] op_sel_hi:[0,1]
	v_pk_mul_f32 v[42:43], v[16:17], v[10:11] op_sel_hi:[0,1]
	v_pk_mul_f32 v[44:45], v[16:17], v[12:13] op_sel_hi:[0,1]
	v_pk_mul_f32 v[46:47], v[16:17], v[14:15] op_sel_hi:[0,1]
	v_pk_mul_f32 v[32:33], v[16:17], v[0:1] op_sel_hi:[0,1]
	v_pk_mul_f32 v[34:35], v[16:17], v[2:3] op_sel_hi:[0,1]
	v_pk_mul_f32 v[36:37], v[16:17], v[4:5] op_sel_hi:[0,1]
	v_pk_mul_f32 v[38:39], v[16:17], v[6:7] op_sel_hi:[0,1]
	v_cvt_scalef32_2xpk16_fp6_f32 v[148:153], v[32:47], v[40:55], 1.0
	v_cvt_scalef32_pk32_f32_fp6 v[0:31], v[148:153], s15
	v_fma_f32 v16, v32, s8, v0
	v_fma_f32 v17, v33, s8, v2
	v_fma_f32 v18, v34, s8, v4
	v_fma_f32 v19, v35, s8, v6
	v_fma_f32 v20, v36, s8, v8
	v_fma_f32 v21, v37, s8, v10
	v_fma_f32 v22, v38, s8, v12
	v_fma_f32 v23, v39, s8, v14
	v_fma_f32 v24, v40, s8, v1
	v_fma_f32 v25, v41, s8, v3
	v_fma_f32 v26, v42, s8, v5
	v_fma_f32 v27, v43, s8, v7
	v_fma_f32 v28, v44, s8, v9
	v_fma_f32 v29, v45, s8, v11
	v_fma_f32 v30, v46, s8, v13
	v_fma_f32 v31, v47, s8, v15
	v_cvt_scalef32_2xpk16_fp6_f32 v[0:5], v[16:31], v[24:39], 1.0
	v_or_b32_e32 v3, 16, v181
	v_or_b32_e32 v4, v3, v180
	v_mul_u32_u24_e32 v146, 24, v4
	v_lshl_add_u64 v[4:5], v[168:169], 0, v[146:147]
	v_lshl_add_u64 v[4:5], v[4:5], 0, v[160:161]
	global_store_dwordx3 v[4:5], v[148:150], off nt
	v_add_co_u32_e32 v4, vcc, 0x1000, v4
	v_xor_b32_e32 v0, 0x20820820, v0
	v_xor_b32_e32 v1, 0x8208208, v1
	v_xor_b32_e32 v2, 0x82082082, v2
	v_addc_co_u32_e32 v5, vcc, 0, v5, vcc
	v_lshl_or_b32 v144, v3, 1, v180
	global_store_dwordx3 v[4:5], v[0:2], off offset:2048 nt
	s_and_saveexec_b64 s[8:9], s[0:1]
	s_cbranch_execz .LBB3_10
	v_mov_b32_e32 v1, 0x7a00
	v_add_u32_e32 v0, 0x7f, v145
	v_lshl_add_u32 v1, v145, 8, v1
	v_mov_b32_e32 v145, 0
	v_or_b32_e32 v2, v1, v0
	v_lshl_add_u64 v[0:1], v[166:167], 0, v[144:145]
	global_store_short v[0:1], v2, off
.LBB3_10:
	s_or_b64 exec, exec, s[8:9]
	v_permlane32_swap_b32_e32 v140, v132
	v_permlane32_swap_b32_e32 v141, v133
	v_permlane32_swap_b32_e32 v142, v134
	v_permlane32_swap_b32_e32 v143, v135
	v_permlane32_swap_b32_e32 v136, v128
	v_permlane32_swap_b32_e32 v137, v129
	s_mov_b32 s18, 0x3e6d3388
	v_permlane32_swap_b32_e32 v138, v130
	v_permlane32_swap_b32_e32 v139, v131
	s_mov_b32 s14, 0x3f07dc22
	s_mov_b32 s12, 0xbf38aa3b
	v_mov_b64_e32 v[16:17], s[22:23]
	s_mov_b32 s16, 0x3f35f0e3
	s_mov_b32 s8, 0xbe11a98e
	s_mov_b32 s10, 0x3e027906
	s_mov_b32 s20, 0xc2000000
	v_pk_mul_f32 v[0:1], v[192:193], v[140:141]
	v_pk_mul_f32 v[2:3], v[194:195], v[142:143]
	v_pk_mul_f32 v[4:5], v[196:197], v[136:137]
	v_and_b32_e32 v19, 0x7fffffff, v1
	v_and_b32_e32 v18, 0x7fffffff, v0
	v_and_b32_e32 v23, 0x7fffffff, v3
	v_and_b32_e32 v22, 0x7fffffff, v2
	v_and_b32_e32 v27, 0x7fffffff, v5
	v_and_b32_e32 v26, 0x7fffffff, v4
	v_pk_fma_f32 v[34:35], v[18:19], s[18:19], 1.0 op_sel_hi:[1,0,0]
	v_pk_fma_f32 v[36:37], v[22:23], s[18:19], 1.0 op_sel_hi:[1,0,0]
	v_pk_fma_f32 v[38:39], v[26:27], s[18:19], 1.0 op_sel_hi:[1,0,0]
	v_rcp_f32_e32 v34, v34
	v_rcp_f32_e32 v35, v35
	v_rcp_f32_e32 v36, v36
	v_rcp_f32_e32 v37, v37
	v_rcp_f32_e32 v38, v38
	v_rcp_f32_e32 v39, v39
	v_pk_mul_f32 v[6:7], v[198:199], v[138:139]
	v_pk_mul_f32 v[20:21], v[0:1], v[0:1]
	v_pk_mul_f32 v[24:25], v[2:3], v[2:3]
	v_pk_mul_f32 v[28:29], v[4:5], v[4:5]
	v_and_b32_e32 v31, 0x7fffffff, v7
	v_and_b32_e32 v30, 0x7fffffff, v6
	v_pk_mul_f32 v[20:21], v[20:21], s[12:13] op_sel_hi:[1,0]
	v_pk_mul_f32 v[24:25], v[24:25], s[12:13] op_sel_hi:[1,0]
	v_pk_fma_f32 v[42:43], v[34:35], s[14:15], v[16:17] op_sel_hi:[1,0,0]
	v_pk_fma_f32 v[44:45], v[36:37], s[14:15], v[16:17] op_sel_hi:[1,0,0]
	v_pk_mul_f32 v[28:29], v[28:29], s[12:13] op_sel_hi:[1,0]
	v_pk_fma_f32 v[40:41], v[30:31], s[18:19], 1.0 op_sel_hi:[1,0,0]
	v_exp_f32_e32 v20, v20
	v_exp_f32_e32 v21, v21
	v_exp_f32_e32 v24, v24
	v_exp_f32_e32 v25, v25
	v_pk_fma_f32 v[46:47], v[38:39], s[14:15], v[16:17] op_sel_hi:[1,0,0]
	v_pk_fma_f32 v[42:43], v[34:35], v[42:43], s[16:17] op_sel_hi:[1,1,0]
	v_pk_fma_f32 v[44:45], v[36:37], v[44:45], s[16:17] op_sel_hi:[1,1,0]
	v_exp_f32_e32 v28, v28
	v_exp_f32_e32 v29, v29
	v_rcp_f32_e32 v40, v40
	v_rcp_f32_e32 v41, v41
	v_pk_fma_f32 v[46:47], v[38:39], v[46:47], s[16:17] op_sel_hi:[1,1,0]
	v_pk_fma_f32 v[42:43], v[34:35], v[42:43], s[8:9] op_sel_hi:[1,1,0]
	v_pk_fma_f32 v[44:45], v[36:37], v[44:45], s[8:9] op_sel_hi:[1,1,0]
	v_pk_fma_f32 v[46:47], v[38:39], v[46:47], s[8:9] op_sel_hi:[1,1,0]
	v_pk_fma_f32 v[42:43], v[34:35], v[42:43], s[10:11] op_sel_hi:[1,1,0]
	v_pk_fma_f32 v[44:45], v[36:37], v[44:45], s[10:11] op_sel_hi:[1,1,0]
	v_pk_fma_f32 v[46:47], v[38:39], v[46:47], s[10:11] op_sel_hi:[1,1,0]
	v_pk_mul_f32 v[34:35], v[34:35], v[42:43]
	v_pk_mul_f32 v[36:37], v[36:37], v[44:45]
	v_pk_mul_f32 v[32:33], v[6:7], v[6:7]
	v_pk_mul_f32 v[38:39], v[38:39], v[46:47]
	v_pk_fma_f32 v[20:21], v[20:21], v[34:35], 0.5 op_sel_hi:[1,1,0] neg_lo:[1,0,0] neg_hi:[1,0,0]
	v_pk_fma_f32 v[24:25], v[24:25], v[36:37], 0.5 op_sel_hi:[1,1,0] neg_lo:[1,0,0] neg_hi:[1,0,0]
	v_pk_mul_f32 v[32:33], v[32:33], s[12:13] op_sel_hi:[1,0]
	v_pk_fma_f32 v[136:137], v[40:41], s[14:15], v[16:17] op_sel_hi:[1,0,0]
	v_pk_fma_f32 v[28:29], v[28:29], v[38:39], 0.5 op_sel_hi:[1,1,0] neg_lo:[1,0,0] neg_hi:[1,0,0]
	v_pk_mul_f32 v[18:19], v[18:19], v[20:21]
	v_pk_mul_f32 v[20:21], v[22:23], v[24:25]
	v_pk_mul_f32 v[8:9], v[200:201], v[132:133]
	v_pk_fma_f32 v[136:137], v[40:41], v[136:137], s[16:17] op_sel_hi:[1,1,0]
	v_pk_mul_f32 v[22:23], v[26:27], v[28:29]
	v_pk_fma_f32 v[0:1], v[0:1], 0.5, v[18:19] op_sel_hi:[1,0,1]
	v_pk_fma_f32 v[2:3], v[2:3], 0.5, v[20:21] op_sel_hi:[1,0,1]
	v_exp_f32_e32 v18, v32
	v_exp_f32_e32 v19, v33
	v_and_b32_e32 v21, 0x7fffffff, v9
	v_and_b32_e32 v20, 0x7fffffff, v8
	v_pk_fma_f32 v[136:137], v[40:41], v[136:137], s[8:9] op_sel_hi:[1,1,0]
	v_pk_fma_f32 v[4:5], v[4:5], 0.5, v[22:23] op_sel_hi:[1,0,1]
	v_pk_fma_f32 v[22:23], v[20:21], s[18:19], 1.0 op_sel_hi:[1,0,0]
	v_pk_fma_f32 v[136:137], v[40:41], v[136:137], s[10:11] op_sel_hi:[1,1,0]
	v_rcp_f32_e32 v22, v22
	v_rcp_f32_e32 v23, v23
	v_pk_mul_f32 v[40:41], v[40:41], v[136:137]
	v_pk_mul_f32 v[10:11], v[202:203], v[134:135]
	v_pk_fma_f32 v[18:19], v[18:19], v[40:41], 0.5 op_sel_hi:[1,1,0] neg_lo:[1,0,0] neg_hi:[1,0,0]
	v_and_b32_e32 v25, 0x7fffffff, v11
	v_pk_mul_f32 v[18:19], v[30:31], v[18:19]
	v_and_b32_e32 v24, 0x7fffffff, v10
	v_pk_fma_f32 v[6:7], v[6:7], 0.5, v[18:19] op_sel_hi:[1,0,1]
	v_pk_fma_f32 v[18:19], v[22:23], s[14:15], v[16:17] op_sel_hi:[1,0,0]
	v_pk_fma_f32 v[26:27], v[24:25], s[18:19], 1.0 op_sel_hi:[1,0,0]
	v_pk_fma_f32 v[18:19], v[22:23], v[18:19], s[16:17] op_sel_hi:[1,1,0]
	v_rcp_f32_e32 v26, v26
	v_pk_fma_f32 v[18:19], v[22:23], v[18:19], s[8:9] op_sel_hi:[1,1,0]
	v_rcp_f32_e32 v27, v27
	v_pk_fma_f32 v[18:19], v[22:23], v[18:19], s[10:11] op_sel_hi:[1,1,0]
	v_pk_mul_f32 v[12:13], v[204:205], v[128:129]
	v_pk_mul_f32 v[18:19], v[22:23], v[18:19]
	v_pk_mul_f32 v[22:23], v[8:9], v[8:9]
	v_pk_mul_f32 v[14:15], v[206:207], v[130:131]
	v_pk_mul_f32 v[22:23], v[22:23], s[12:13] op_sel_hi:[1,0]
	v_mov_b32_e32 v132, 0xffffff7f
	v_exp_f32_e32 v22, v22
	v_exp_f32_e32 v23, v23
	v_mov_b32_e32 v133, 0x64
	v_mov_b32_e32 v131, 0
	v_pk_fma_f32 v[18:19], v[22:23], v[18:19], 0.5 op_sel_hi:[1,1,0] neg_lo:[1,0,0] neg_hi:[1,0,0]
	s_nop 0
	v_pk_mul_f32 v[18:19], v[20:21], v[18:19]
	v_pk_mul_f32 v[20:21], v[10:11], v[10:11]
	v_pk_fma_f32 v[8:9], v[8:9], 0.5, v[18:19] op_sel_hi:[1,0,1]
	v_pk_fma_f32 v[18:19], v[26:27], s[14:15], v[16:17] op_sel_hi:[1,0,0]
	v_pk_mul_f32 v[20:21], v[20:21], s[12:13] op_sel_hi:[1,0]
	v_pk_fma_f32 v[18:19], v[26:27], v[18:19], s[16:17] op_sel_hi:[1,1,0]
	v_exp_f32_e32 v20, v20
	v_pk_fma_f32 v[18:19], v[26:27], v[18:19], s[8:9] op_sel_hi:[1,1,0]
	v_exp_f32_e32 v21, v21
	v_pk_fma_f32 v[18:19], v[26:27], v[18:19], s[10:11] op_sel_hi:[1,1,0]
	v_and_b32_e32 v23, 0x7fffffff, v13
	v_and_b32_e32 v22, 0x7fffffff, v12
	v_pk_mul_f32 v[18:19], v[26:27], v[18:19]
	v_pk_fma_f32 v[26:27], v[22:23], s[18:19], 1.0 op_sel_hi:[1,0,0]
	v_pk_fma_f32 v[18:19], v[20:21], v[18:19], 0.5 op_sel_hi:[1,1,0] neg_lo:[1,0,0] neg_hi:[1,0,0]
	v_rcp_f32_e32 v26, v26
	v_rcp_f32_e32 v27, v27
	v_pk_mul_f32 v[18:19], v[24:25], v[18:19]
	v_pk_mul_f32 v[20:21], v[12:13], v[12:13]
	v_pk_fma_f32 v[10:11], v[10:11], 0.5, v[18:19] op_sel_hi:[1,0,1]
	v_pk_fma_f32 v[18:19], v[26:27], s[14:15], v[16:17] op_sel_hi:[1,0,0]
	v_pk_mul_f32 v[20:21], v[20:21], s[12:13] op_sel_hi:[1,0]
	v_pk_fma_f32 v[18:19], v[26:27], v[18:19], s[16:17] op_sel_hi:[1,1,0]
	v_exp_f32_e32 v20, v20
	v_pk_fma_f32 v[18:19], v[26:27], v[18:19], s[8:9] op_sel_hi:[1,1,0]
	v_exp_f32_e32 v21, v21
	v_pk_fma_f32 v[18:19], v[26:27], v[18:19], s[10:11] op_sel_hi:[1,1,0]
	v_and_b32_e32 v25, 0x7fffffff, v15
	v_and_b32_e32 v24, 0x7fffffff, v14
	v_pk_mul_f32 v[18:19], v[26:27], v[18:19]
	v_pk_fma_f32 v[26:27], v[24:25], s[18:19], 1.0 op_sel_hi:[1,0,0]
	v_pk_fma_f32 v[18:19], v[20:21], v[18:19], 0.5 op_sel_hi:[1,1,0] neg_lo:[1,0,0] neg_hi:[1,0,0]
	v_rcp_f32_e32 v26, v26
	v_rcp_f32_e32 v27, v27
	v_pk_mul_f32 v[18:19], v[22:23], v[18:19]
	v_pk_fma_f32 v[16:17], v[26:27], s[14:15], v[16:17] op_sel_hi:[1,0,0]
	v_pk_fma_f32 v[12:13], v[12:13], 0.5, v[18:19] op_sel_hi:[1,0,1]
	v_pk_mul_f32 v[18:19], v[14:15], v[14:15]
	v_pk_fma_f32 v[16:17], v[26:27], v[16:17], s[16:17] op_sel_hi:[1,1,0]
	v_pk_mul_f32 v[18:19], v[18:19], s[12:13] op_sel_hi:[1,0]
	v_pk_fma_f32 v[16:17], v[26:27], v[16:17], s[8:9] op_sel_hi:[1,1,0]
	v_exp_f32_e32 v18, v18
	v_exp_f32_e32 v19, v19
	v_pk_fma_f32 v[16:17], v[26:27], v[16:17], s[10:11] op_sel_hi:[1,1,0]
	s_mov_b32 s9, 0x700000
	v_pk_mul_f32 v[16:17], v[26:27], v[16:17]
	s_nop 0
	v_pk_fma_f32 v[16:17], v[18:19], v[16:17], 0.5 op_sel_hi:[1,1,0] neg_lo:[1,0,0] neg_hi:[1,0,0]
	v_max_f32_e64 v18, |v6|, |v7|
	v_pk_mul_f32 v[16:17], v[24:25], v[16:17]
	s_nop 0
	v_pk_fma_f32 v[14:15], v[14:15], 0.5, v[16:17] op_sel_hi:[1,0,1]
	v_max_f32_e64 v16, |v0|, |v1|
	v_max_f32_e64 v17, |v2|, |v3|
	v_max3_f32 v16, v16, 0, v17
	v_max_f32_e64 v17, |v4|, |v5|
	v_max3_f32 v16, v16, v17, v18
	v_max_f32_e64 v17, |v8|, |v9|
	v_max_f32_e64 v18, |v10|, |v11|
	v_max3_f32 v16, v16, v17, v18
	v_max_f32_e64 v17, |v12|, |v13|
	v_max_f32_e64 v18, |v14|, |v15|
	v_max3_f32 v16, v16, v17, v18
	v_mov_b32_e32 v17, v16
	s_nop 1
	v_permlane16_swap_b32_e32 v16, v17
	v_max_f32_e32 v17, v17, v17
	v_max_f32_e32 v16, v16, v16
	v_max_f32_e32 v16, v16, v17
	v_lshrrev_b32_e32 v17, 23, v16
	v_and_b32_e32 v16, 0x7fffff, v16
	v_cmp_lt_u32_e32 vcc, s9, v16
	s_nop 1
	v_addc_co_u32_e32 v16, vcc, v17, v132, vcc
	v_med3_i32 v129, v16, s13, v133
	v_lshlrev_b32_e32 v16, 23, v129
	v_sub_u32_e32 v16, 1.0, v16
	v_pk_mul_f32 v[40:41], v[16:17], v[8:9] op_sel_hi:[0,1]
	v_pk_mul_f32 v[42:43], v[16:17], v[10:11] op_sel_hi:[0,1]
	v_pk_mul_f32 v[44:45], v[16:17], v[12:13] op_sel_hi:[0,1]
	v_pk_mul_f32 v[46:47], v[16:17], v[14:15] op_sel_hi:[0,1]
	v_pk_mul_f32 v[32:33], v[16:17], v[0:1] op_sel_hi:[0,1]
	v_pk_mul_f32 v[34:35], v[16:17], v[2:3] op_sel_hi:[0,1]
	v_pk_mul_f32 v[36:37], v[16:17], v[4:5] op_sel_hi:[0,1]
	v_pk_mul_f32 v[38:39], v[16:17], v[6:7] op_sel_hi:[0,1]
	v_cvt_scalef32_2xpk16_fp6_f32 v[134:139], v[32:47], v[40:55], 1.0
	v_cvt_scalef32_pk32_f32_fp6 v[0:31], v[134:139], s15
	v_fma_f32 v16, v32, s20, v0
	v_fma_f32 v17, v33, s20, v2
	v_fma_f32 v18, v34, s20, v4
	v_fma_f32 v19, v35, s20, v6
	v_fma_f32 v20, v36, s20, v8
	v_fma_f32 v21, v37, s20, v10
	v_fma_f32 v22, v38, s20, v12
	v_fma_f32 v23, v39, s20, v14
	v_fma_f32 v24, v40, s20, v1
	v_fma_f32 v25, v41, s20, v3
	v_fma_f32 v26, v42, s20, v5
	v_fma_f32 v27, v43, s20, v7
	v_fma_f32 v28, v44, s20, v9
	v_fma_f32 v29, v45, s20, v11
	v_fma_f32 v30, v46, s20, v13
	v_fma_f32 v31, v47, s20, v15
	v_cvt_scalef32_2xpk16_fp6_f32 v[0:5], v[16:31], v[24:39], 1.0
	v_or_b32_e32 v3, 32, v181
	v_or_b32_e32 v4, v3, v180
	v_mul_u32_u24_e32 v130, 24, v4
	v_lshl_add_u64 v[4:5], v[168:169], 0, v[130:131]
	v_lshl_add_u64 v[4:5], v[4:5], 0, v[160:161]
	global_store_dwordx3 v[4:5], v[134:136], off nt
	v_add_co_u32_e32 v4, vcc, 0x1000, v4
	v_xor_b32_e32 v0, 0x20820820, v0
	v_xor_b32_e32 v1, 0x8208208, v1
	v_xor_b32_e32 v2, 0x82082082, v2
	v_addc_co_u32_e32 v5, vcc, 0, v5, vcc
	v_lshl_or_b32 v128, v3, 1, v180
	global_store_dwordx3 v[4:5], v[0:2], off offset:2048 nt
	s_and_saveexec_b64 s[24:25], s[0:1]
	s_cbranch_execz .LBB3_12
	v_mov_b32_e32 v1, 0x7a00
	v_add_u32_e32 v0, 0x7f, v129
	v_lshl_add_u32 v1, v129, 8, v1
	v_mov_b32_e32 v129, v131
	v_or_b32_e32 v2, v1, v0
	v_lshl_add_u64 v[0:1], v[166:167], 0, v[128:129]
	global_store_short v[0:1], v2, off
.LBB3_12:
	s_or_b64 exec, exec, s[24:25]
	v_permlane32_swap_b32_e32 v124, v116
	v_permlane32_swap_b32_e32 v125, v117
	v_permlane32_swap_b32_e32 v126, v118
	v_permlane32_swap_b32_e32 v127, v119
	v_permlane32_swap_b32_e32 v122, v114
	v_permlane32_swap_b32_e32 v123, v115
	v_permlane32_swap_b32_e32 v120, v112
	v_permlane32_swap_b32_e32 v121, v113
	v_mov_b64_e32 v[16:17], s[22:23]
	v_pk_mul_f32 v[0:1], v[192:193], v[124:125]
	v_pk_mul_f32 v[2:3], v[194:195], v[126:127]
	v_and_b32_e32 v19, 0x7fffffff, v1
	v_and_b32_e32 v18, 0x7fffffff, v0
	v_pk_mul_f32 v[6:7], v[198:199], v[122:123]
	v_and_b32_e32 v23, 0x7fffffff, v3
	v_and_b32_e32 v22, 0x7fffffff, v2
	v_pk_fma_f32 v[36:37], v[18:19], s[18:19], 1.0 op_sel_hi:[1,0,0]
	v_pk_mul_f32 v[4:5], v[196:197], v[120:121]
	v_and_b32_e32 v31, 0x7fffffff, v7
	v_and_b32_e32 v30, 0x7fffffff, v6
	v_pk_fma_f32 v[38:39], v[22:23], s[18:19], 1.0 op_sel_hi:[1,0,0]
	v_rcp_f32_e32 v36, v36
	v_rcp_f32_e32 v37, v37
	v_and_b32_e32 v27, 0x7fffffff, v5
	v_and_b32_e32 v26, 0x7fffffff, v4
	v_pk_fma_f32 v[42:43], v[30:31], s[18:19], 1.0 op_sel_hi:[1,0,0]
	v_rcp_f32_e32 v38, v38
	v_rcp_f32_e32 v39, v39
	v_pk_fma_f32 v[40:41], v[26:27], s[18:19], 1.0 op_sel_hi:[1,0,0]
	v_rcp_f32_e32 v42, v42
	v_rcp_f32_e32 v43, v43
	v_pk_mul_f32 v[20:21], v[0:1], v[0:1]
	v_rcp_f32_e32 v40, v40
	v_rcp_f32_e32 v41, v41
	v_pk_mul_f32 v[24:25], v[2:3], v[2:3]
	v_pk_mul_f32 v[20:21], v[20:21], s[12:13] op_sel_hi:[1,0]
	v_pk_fma_f32 v[46:47], v[36:37], s[14:15], v[16:17] op_sel_hi:[1,0,0]
	v_pk_mul_f32 v[8:9], v[200:201], v[116:117]
	v_pk_mul_f32 v[32:33], v[6:7], v[6:7]
	v_pk_mul_f32 v[24:25], v[24:25], s[12:13] op_sel_hi:[1,0]
	v_exp_f32_e32 v20, v20
	v_exp_f32_e32 v21, v21
	v_pk_fma_f32 v[116:117], v[38:39], s[14:15], v[16:17] op_sel_hi:[1,0,0]
	v_pk_fma_f32 v[46:47], v[36:37], v[46:47], s[16:17] op_sel_hi:[1,1,0]
	v_pk_mul_f32 v[28:29], v[4:5], v[4:5]
	v_pk_mul_f32 v[32:33], v[32:33], s[12:13] op_sel_hi:[1,0]
	v_exp_f32_e32 v24, v24
	v_exp_f32_e32 v25, v25
	v_pk_fma_f32 v[122:123], v[42:43], s[14:15], v[16:17] op_sel_hi:[1,0,0]
	v_pk_fma_f32 v[116:117], v[38:39], v[116:117], s[16:17] op_sel_hi:[1,1,0]
	v_pk_fma_f32 v[46:47], v[36:37], v[46:47], s[8:9] op_sel_hi:[1,1,0]
	v_and_b32_e32 v35, 0x7fffffff, v9
	v_and_b32_e32 v34, 0x7fffffff, v8
	v_pk_mul_f32 v[28:29], v[28:29], s[12:13] op_sel_hi:[1,0]
	v_exp_f32_e32 v32, v32
	v_exp_f32_e32 v33, v33
	v_pk_fma_f32 v[120:121], v[40:41], s[14:15], v[16:17] op_sel_hi:[1,0,0]
	v_pk_fma_f32 v[122:123], v[42:43], v[122:123], s[16:17] op_sel_hi:[1,1,0]
	v_pk_fma_f32 v[116:117], v[38:39], v[116:117], s[8:9] op_sel_hi:[1,1,0]
	v_pk_fma_f32 v[46:47], v[36:37], v[46:47], s[10:11] op_sel_hi:[1,1,0]
	v_pk_fma_f32 v[44:45], v[34:35], s[18:19], 1.0 op_sel_hi:[1,0,0]
	v_exp_f32_e32 v28, v28
	v_exp_f32_e32 v29, v29
	v_pk_fma_f32 v[120:121], v[40:41], v[120:121], s[16:17] op_sel_hi:[1,1,0]
	v_pk_fma_f32 v[122:123], v[42:43], v[122:123], s[8:9] op_sel_hi:[1,1,0]
	v_pk_fma_f32 v[116:117], v[38:39], v[116:117], s[10:11] op_sel_hi:[1,1,0]
	v_pk_mul_f32 v[36:37], v[36:37], v[46:47]
	v_rcp_f32_e32 v44, v44
	v_pk_fma_f32 v[120:121], v[40:41], v[120:121], s[8:9] op_sel_hi:[1,1,0]
	v_pk_fma_f32 v[122:123], v[42:43], v[122:123], s[10:11] op_sel_hi:[1,1,0]
	v_pk_mul_f32 v[38:39], v[38:39], v[116:117]
	v_pk_fma_f32 v[20:21], v[20:21], v[36:37], 0.5 op_sel_hi:[1,1,0] neg_lo:[1,0,0] neg_hi:[1,0,0]
	v_rcp_f32_e32 v45, v45
	v_pk_fma_f32 v[120:121], v[40:41], v[120:121], s[10:11] op_sel_hi:[1,1,0]
	v_pk_mul_f32 v[42:43], v[42:43], v[122:123]
	v_pk_fma_f32 v[24:25], v[24:25], v[38:39], 0.5 op_sel_hi:[1,1,0] neg_lo:[1,0,0] neg_hi:[1,0,0]
	v_pk_mul_f32 v[18:19], v[18:19], v[20:21]
	v_pk_mul_f32 v[40:41], v[40:41], v[120:121]
	v_pk_mul_f32 v[20:21], v[22:23], v[24:25]
	v_pk_fma_f32 v[0:1], v[0:1], 0.5, v[18:19] op_sel_hi:[1,0,1]
	v_pk_fma_f32 v[18:19], v[32:33], v[42:43], 0.5 op_sel_hi:[1,1,0] neg_lo:[1,0,0] neg_hi:[1,0,0]
	v_pk_fma_f32 v[28:29], v[28:29], v[40:41], 0.5 op_sel_hi:[1,1,0] neg_lo:[1,0,0] neg_hi:[1,0,0]
	v_pk_fma_f32 v[2:3], v[2:3], 0.5, v[20:21] op_sel_hi:[1,0,1]
	v_pk_mul_f32 v[18:19], v[30:31], v[18:19]
	v_pk_mul_f32 v[20:21], v[8:9], v[8:9]
	v_pk_mul_f32 v[22:23], v[26:27], v[28:29]
	v_pk_fma_f32 v[6:7], v[6:7], 0.5, v[18:19] op_sel_hi:[1,0,1]
	v_pk_fma_f32 v[18:19], v[44:45], s[14:15], v[16:17] op_sel_hi:[1,0,0]
	v_pk_mul_f32 v[20:21], v[20:21], s[12:13] op_sel_hi:[1,0]
	v_pk_mul_f32 v[10:11], v[202:203], v[118:119]
	v_pk_fma_f32 v[4:5], v[4:5], 0.5, v[22:23] op_sel_hi:[1,0,1]
	v_pk_fma_f32 v[18:19], v[44:45], v[18:19], s[16:17] op_sel_hi:[1,1,0]
	v_exp_f32_e32 v20, v20
	v_exp_f32_e32 v21, v21
	v_and_b32_e32 v23, 0x7fffffff, v11
	v_and_b32_e32 v22, 0x7fffffff, v10
	v_pk_fma_f32 v[18:19], v[44:45], v[18:19], s[8:9] op_sel_hi:[1,1,0]
	v_pk_fma_f32 v[24:25], v[22:23], s[18:19], 1.0 op_sel_hi:[1,0,0]
	v_pk_fma_f32 v[18:19], v[44:45], v[18:19], s[10:11] op_sel_hi:[1,1,0]
	v_rcp_f32_e32 v24, v24
	v_rcp_f32_e32 v25, v25
	v_pk_mul_f32 v[18:19], v[44:45], v[18:19]
	v_pk_mul_f32 v[12:13], v[204:205], v[112:113]
	v_pk_fma_f32 v[18:19], v[20:21], v[18:19], 0.5 op_sel_hi:[1,1,0] neg_lo:[1,0,0] neg_hi:[1,0,0]
	v_pk_mul_f32 v[20:21], v[10:11], v[10:11]
	v_pk_mul_f32 v[18:19], v[34:35], v[18:19]
	v_pk_mul_f32 v[20:21], v[20:21], s[12:13] op_sel_hi:[1,0]
	v_pk_fma_f32 v[8:9], v[8:9], 0.5, v[18:19] op_sel_hi:[1,0,1]
	v_pk_fma_f32 v[18:19], v[24:25], s[14:15], v[16:17] op_sel_hi:[1,0,0]
	v_exp_f32_e32 v20, v20
	v_pk_fma_f32 v[18:19], v[24:25], v[18:19], s[16:17] op_sel_hi:[1,1,0]
	v_exp_f32_e32 v21, v21
	v_pk_fma_f32 v[18:19], v[24:25], v[18:19], s[8:9] op_sel_hi:[1,1,0]
	v_pk_mul_f32 v[14:15], v[206:207], v[114:115]
	v_pk_fma_f32 v[18:19], v[24:25], v[18:19], s[10:11] op_sel_hi:[1,1,0]
	v_mov_b32_e32 v115, v131
	v_pk_mul_f32 v[18:19], v[24:25], v[18:19]
	v_and_b32_e32 v25, 0x7fffffff, v13
	v_and_b32_e32 v24, 0x7fffffff, v12
	v_pk_fma_f32 v[26:27], v[24:25], s[18:19], 1.0 op_sel_hi:[1,0,0]
	v_pk_fma_f32 v[18:19], v[20:21], v[18:19], 0.5 op_sel_hi:[1,1,0] neg_lo:[1,0,0] neg_hi:[1,0,0]
	v_rcp_f32_e32 v26, v26
	v_rcp_f32_e32 v27, v27
	v_pk_mul_f32 v[18:19], v[22:23], v[18:19]
	v_pk_mul_f32 v[20:21], v[12:13], v[12:13]
	v_pk_fma_f32 v[10:11], v[10:11], 0.5, v[18:19] op_sel_hi:[1,0,1]
	v_pk_fma_f32 v[18:19], v[26:27], s[14:15], v[16:17] op_sel_hi:[1,0,0]
	v_pk_mul_f32 v[20:21], v[20:21], s[12:13] op_sel_hi:[1,0]
	v_pk_fma_f32 v[18:19], v[26:27], v[18:19], s[16:17] op_sel_hi:[1,1,0]
	v_exp_f32_e32 v20, v20
	v_pk_fma_f32 v[18:19], v[26:27], v[18:19], s[8:9] op_sel_hi:[1,1,0]
	v_exp_f32_e32 v21, v21
	v_pk_fma_f32 v[18:19], v[26:27], v[18:19], s[10:11] op_sel_hi:[1,1,0]
	v_and_b32_e32 v23, 0x7fffffff, v15
	v_and_b32_e32 v22, 0x7fffffff, v14
	v_pk_mul_f32 v[18:19], v[26:27], v[18:19]
	v_pk_fma_f32 v[26:27], v[22:23], s[18:19], 1.0 op_sel_hi:[1,0,0]
	v_pk_fma_f32 v[18:19], v[20:21], v[18:19], 0.5 op_sel_hi:[1,1,0] neg_lo:[1,0,0] neg_hi:[1,0,0]
	v_rcp_f32_e32 v26, v26
	v_rcp_f32_e32 v27, v27
	v_pk_mul_f32 v[18:19], v[24:25], v[18:19]
	v_pk_fma_f32 v[16:17], v[26:27], s[14:15], v[16:17] op_sel_hi:[1,0,0]
	v_pk_fma_f32 v[12:13], v[12:13], 0.5, v[18:19] op_sel_hi:[1,0,1]
	v_pk_mul_f32 v[18:19], v[14:15], v[14:15]
	v_pk_fma_f32 v[16:17], v[26:27], v[16:17], s[16:17] op_sel_hi:[1,1,0]
	v_pk_mul_f32 v[18:19], v[18:19], s[12:13] op_sel_hi:[1,0]
	v_pk_fma_f32 v[16:17], v[26:27], v[16:17], s[8:9] op_sel_hi:[1,1,0]
	v_exp_f32_e32 v18, v18
	v_exp_f32_e32 v19, v19
	v_pk_fma_f32 v[16:17], v[26:27], v[16:17], s[10:11] op_sel_hi:[1,1,0]
	s_nop 0
	v_pk_mul_f32 v[16:17], v[26:27], v[16:17]
	s_nop 0
	v_pk_fma_f32 v[16:17], v[18:19], v[16:17], 0.5 op_sel_hi:[1,1,0] neg_lo:[1,0,0] neg_hi:[1,0,0]
	v_max_f32_e64 v18, |v6|, |v7|
	v_pk_mul_f32 v[16:17], v[22:23], v[16:17]
	s_nop 0
	v_pk_fma_f32 v[14:15], v[14:15], 0.5, v[16:17] op_sel_hi:[1,0,1]
	v_max_f32_e64 v16, |v0|, |v1|
	v_max_f32_e64 v17, |v2|, |v3|
	v_max3_f32 v16, v16, 0, v17
	v_max_f32_e64 v17, |v4|, |v5|
	v_max3_f32 v16, v16, v17, v18
	v_max_f32_e64 v17, |v8|, |v9|
	v_max_f32_e64 v18, |v10|, |v11|
	v_max3_f32 v16, v16, v17, v18
	v_max_f32_e64 v17, |v12|, |v13|
	v_max_f32_e64 v18, |v14|, |v15|
	v_max3_f32 v16, v16, v17, v18
	v_mov_b32_e32 v17, v16
	s_nop 1
	v_permlane16_swap_b32_e32 v16, v17
	v_max_f32_e32 v17, v17, v17
	v_max_f32_e32 v16, v16, v16
	v_max_f32_e32 v16, v16, v17
	v_lshrrev_b32_e32 v17, 23, v16
	v_and_b32_e32 v16, 0x7fffff, v16
	v_cmp_lt_u32_e32 vcc, s9, v16
	s_nop 1
	v_addc_co_u32_e32 v16, vcc, v17, v132, vcc
	v_med3_i32 v113, v16, s13, v133
	v_lshlrev_b32_e32 v16, 23, v113
	v_sub_u32_e32 v16, 1.0, v16
	v_pk_mul_f32 v[40:41], v[16:17], v[8:9] op_sel_hi:[0,1]
	v_pk_mul_f32 v[42:43], v[16:17], v[10:11] op_sel_hi:[0,1]
	v_pk_mul_f32 v[44:45], v[16:17], v[12:13] op_sel_hi:[0,1]
	v_pk_mul_f32 v[46:47], v[16:17], v[14:15] op_sel_hi:[0,1]
	v_pk_mul_f32 v[32:33], v[16:17], v[0:1] op_sel_hi:[0,1]
	v_pk_mul_f32 v[34:35], v[16:17], v[2:3] op_sel_hi:[0,1]
	v_pk_mul_f32 v[36:37], v[16:17], v[4:5] op_sel_hi:[0,1]
	v_pk_mul_f32 v[38:39], v[16:17], v[6:7] op_sel_hi:[0,1]
	v_cvt_scalef32_2xpk16_fp6_f32 v[116:121], v[32:47], v[40:55], 1.0
	v_cvt_scalef32_pk32_f32_fp6 v[0:31], v[116:121], s15
	v_fma_f32 v16, v32, s20, v0
	v_fma_f32 v17, v33, s20, v2
	v_fma_f32 v18, v34, s20, v4
	v_fma_f32 v19, v35, s20, v6
	v_fma_f32 v20, v36, s20, v8
	v_fma_f32 v21, v37, s20, v10
	v_fma_f32 v22, v38, s20, v12
	v_fma_f32 v23, v39, s20, v14
	v_fma_f32 v24, v40, s20, v1
	v_fma_f32 v25, v41, s20, v3
	v_fma_f32 v26, v42, s20, v5
	v_fma_f32 v27, v43, s20, v7
	v_fma_f32 v28, v44, s20, v9
	v_fma_f32 v29, v45, s20, v11
	v_fma_f32 v30, v46, s20, v13
	v_fma_f32 v31, v47, s20, v15
	v_cvt_scalef32_2xpk16_fp6_f32 v[0:5], v[16:31], v[24:39], 1.0
	v_or_b32_e32 v3, 48, v181
	v_or_b32_e32 v4, v3, v180
	v_mul_u32_u24_e32 v114, 24, v4
	v_lshl_add_u64 v[4:5], v[168:169], 0, v[114:115]
	v_lshl_add_u64 v[4:5], v[4:5], 0, v[160:161]
	global_store_dwordx3 v[4:5], v[116:118], off nt
	v_add_co_u32_e32 v4, vcc, 0x1000, v4
	v_xor_b32_e32 v0, 0x20820820, v0
	v_xor_b32_e32 v1, 0x8208208, v1
	v_xor_b32_e32 v2, 0x82082082, v2
	v_addc_co_u32_e32 v5, vcc, 0, v5, vcc
	v_lshl_or_b32 v112, v3, 1, v180
	global_store_dwordx3 v[4:5], v[0:2], off offset:2048 nt
	s_and_saveexec_b64 s[8:9], s[0:1]
	s_cbranch_execz .LBB3_14
	v_mov_b32_e32 v1, 0x7a00
	v_add_u32_e32 v0, 0x7f, v113
	v_lshl_add_u32 v1, v113, 8, v1
	v_mov_b32_e32 v113, 0
	v_or_b32_e32 v2, v1, v0
	v_lshl_add_u64 v[0:1], v[166:167], 0, v[112:113]
	global_store_short v[0:1], v2, off
.LBB3_14:
	s_or_b64 exec, exec, s[8:9]
	v_or_b32_e32 v8, 2, v178
	v_or_b32_e32 v0, v8, v177
	v_lshlrev_b32_e32 v20, 5, v0
	v_or_b32_e32 v12, v20, v179
	v_ashrrev_i32_e32 v13, 31, v12
	v_lshl_add_u64 v[120:121], v[12:13], 2, s[4:5]
	v_ashrrev_i32_e32 v13, 31, v20
	v_lshl_add_u64 v[122:123], v[12:13], 2, s[4:5]
	v_ashrrev_i32_e32 v12, 1, v8
	v_add_u32_e32 v18, s11, v12
	s_movk_i32 s9, 0x6000
	v_mov_b64_e32 v[14:15], s[2:3]
	v_ashrrev_i32_e32 v19, 31, v18
	v_or_b32_e32 v12, v20, v176
	v_mad_i64_i32 v[118:119], s[20:21], v18, s9, v[14:15]
	v_lshlrev_b64 v[14:15], 10, v[18:19]
	v_lshl_add_u64 v[124:125], v[12:13], 2, s[4:5]
	v_lshl_add_u64 v[116:117], s[6:7], 0, v[14:15]
	v_permlane32_swap_b32_e32 v108, v100
	v_permlane32_swap_b32_e32 v109, v101
	s_mov_b32 s16, 0x3e6d3388
	v_permlane32_swap_b32_e32 v110, v102
	v_permlane32_swap_b32_e32 v111, v103
	v_permlane32_swap_b32_e32 v104, v96
	v_permlane32_swap_b32_e32 v105, v97
	s_mov_b32 s18, 0xbf3a00e3
	s_mov_b32 s12, 0x3f07dc22
	s_mov_b32 s10, 0xbf38aa3b
	v_mov_b64_e32 v[16:17], s[18:19]
	s_mov_b32 s14, 0x3f35f0e3
	s_mov_b32 s2, 0xbe11a98e
	s_mov_b32 s8, 0x3e027906
	v_permlane32_swap_b32_e32 v106, v98
	v_permlane32_swap_b32_e32 v107, v99
	s_movk_i32 s5, 0xff9c
	s_mov_b32 s4, 0xc2000000
	s_waitcnt vmcnt(8)
	v_pk_mul_f32 v[0:1], v[208:209], v[108:109]
	s_nop 0
	v_and_b32_e32 v19, 0x7fffffff, v1
	v_and_b32_e32 v18, 0x7fffffff, v0
	v_pk_fma_f32 v[26:27], v[18:19], s[16:17], 1.0 op_sel_hi:[1,0,0]
	v_pk_mul_f32 v[2:3], v[210:211], v[110:111]
	v_rcp_f32_e32 v26, v26
	v_rcp_f32_e32 v27, v27
	v_and_b32_e32 v23, 0x7fffffff, v3
	v_and_b32_e32 v22, 0x7fffffff, v2
	v_pk_mul_f32 v[4:5], v[212:213], v[104:105]
	v_pk_fma_f32 v[28:29], v[22:23], s[16:17], 1.0 op_sel_hi:[1,0,0]
	v_pk_mul_f32 v[20:21], v[0:1], v[0:1]
	v_and_b32_e32 v31, 0x7fffffff, v5
	v_and_b32_e32 v30, 0x7fffffff, v4
	v_rcp_f32_e32 v28, v28
	v_rcp_f32_e32 v29, v29
	v_pk_mul_f32 v[20:21], v[20:21], s[10:11] op_sel_hi:[1,0]
	v_pk_fma_f32 v[36:37], v[30:31], s[16:17], 1.0 op_sel_hi:[1,0,0]
	v_pk_fma_f32 v[38:39], v[26:27], s[12:13], v[16:17] op_sel_hi:[1,0,0]
	v_exp_f32_e32 v20, v20
	v_exp_f32_e32 v21, v21
	v_rcp_f32_e32 v36, v36
	v_rcp_f32_e32 v37, v37
	v_pk_fma_f32 v[38:39], v[26:27], v[38:39], s[14:15] op_sel_hi:[1,1,0]
	v_pk_mul_f32 v[24:25], v[2:3], v[2:3]
	v_pk_fma_f32 v[38:39], v[26:27], v[38:39], s[2:3] op_sel_hi:[1,1,0]
	v_pk_mul_f32 v[24:25], v[24:25], s[10:11] op_sel_hi:[1,0]
	v_pk_fma_f32 v[40:41], v[28:29], s[12:13], v[16:17] op_sel_hi:[1,0,0]
	v_pk_fma_f32 v[38:39], v[26:27], v[38:39], s[8:9] op_sel_hi:[1,1,0]
	v_pk_mul_f32 v[32:33], v[4:5], v[4:5]
	v_exp_f32_e32 v24, v24
	v_exp_f32_e32 v25, v25
	v_pk_fma_f32 v[40:41], v[28:29], v[40:41], s[14:15] op_sel_hi:[1,1,0]
	v_pk_mul_f32 v[26:27], v[26:27], v[38:39]
	v_pk_mul_f32 v[6:7], v[214:215], v[106:107]
	v_pk_mul_f32 v[32:33], v[32:33], s[10:11] op_sel_hi:[1,0]
	v_pk_fma_f32 v[42:43], v[36:37], s[12:13], v[16:17] op_sel_hi:[1,0,0]
	v_pk_fma_f32 v[40:41], v[28:29], v[40:41], s[2:3] op_sel_hi:[1,1,0]
	v_pk_fma_f32 v[20:21], v[20:21], v[26:27], 0.5 op_sel_hi:[1,1,0] neg_lo:[1,0,0] neg_hi:[1,0,0]
	v_and_b32_e32 v35, 0x7fffffff, v7
	v_and_b32_e32 v34, 0x7fffffff, v6
	v_exp_f32_e32 v32, v32
	v_exp_f32_e32 v33, v33
	v_pk_fma_f32 v[42:43], v[36:37], v[42:43], s[14:15] op_sel_hi:[1,1,0]
	v_pk_fma_f32 v[40:41], v[28:29], v[40:41], s[8:9] op_sel_hi:[1,1,0]
	v_pk_mul_f32 v[18:19], v[18:19], v[20:21]
	v_pk_fma_f32 v[42:43], v[36:37], v[42:43], s[2:3] op_sel_hi:[1,1,0]
	v_pk_mul_f32 v[28:29], v[28:29], v[40:41]
	v_pk_fma_f32 v[0:1], v[0:1], 0.5, v[18:19] op_sel_hi:[1,0,1]
	v_pk_fma_f32 v[18:19], v[34:35], s[16:17], 1.0 op_sel_hi:[1,0,0]
	v_pk_fma_f32 v[38:39], v[36:37], v[42:43], s[8:9] op_sel_hi:[1,1,0]
	v_pk_fma_f32 v[24:25], v[24:25], v[28:29], 0.5 op_sel_hi:[1,1,0] neg_lo:[1,0,0] neg_hi:[1,0,0]
	v_rcp_f32_e32 v18, v18
	v_rcp_f32_e32 v19, v19
	v_pk_mul_f32 v[26:27], v[36:37], v[38:39]
	v_pk_mul_f32 v[20:21], v[22:23], v[24:25]
	v_pk_mul_f32 v[8:9], v[216:217], v[100:101]
	v_pk_fma_f32 v[2:3], v[2:3], 0.5, v[20:21] op_sel_hi:[1,0,1]
	v_pk_fma_f32 v[20:21], v[32:33], v[26:27], 0.5 op_sel_hi:[1,1,0] neg_lo:[1,0,0] neg_hi:[1,0,0]
	v_and_b32_e32 v23, 0x7fffffff, v9
	v_pk_mul_f32 v[20:21], v[30:31], v[20:21]
	v_and_b32_e32 v22, 0x7fffffff, v8
	v_pk_fma_f32 v[4:5], v[4:5], 0.5, v[20:21] op_sel_hi:[1,0,1]
	v_pk_fma_f32 v[20:21], v[18:19], s[12:13], v[16:17] op_sel_hi:[1,0,0]
	v_pk_fma_f32 v[24:25], v[22:23], s[16:17], 1.0 op_sel_hi:[1,0,0]
	v_pk_fma_f32 v[20:21], v[18:19], v[20:21], s[14:15] op_sel_hi:[1,1,0]
	v_rcp_f32_e32 v24, v24
	v_pk_fma_f32 v[20:21], v[18:19], v[20:21], s[2:3] op_sel_hi:[1,1,0]
	v_rcp_f32_e32 v25, v25
	v_pk_fma_f32 v[20:21], v[18:19], v[20:21], s[8:9] op_sel_hi:[1,1,0]
	v_pk_mul_f32 v[10:11], v[218:219], v[102:103]
	v_pk_mul_f32 v[18:19], v[18:19], v[20:21]
	v_pk_mul_f32 v[20:21], v[6:7], v[6:7]
	v_pk_mul_f32 v[12:13], v[220:221], v[96:97]
	v_pk_mul_f32 v[20:21], v[20:21], s[10:11] op_sel_hi:[1,0]
	v_pk_mul_f32 v[14:15], v[222:223], v[98:99]
	v_exp_f32_e32 v20, v20
	v_exp_f32_e32 v21, v21
	v_mov_b32_e32 v96, 0xffffff7f
	v_mov_b32_e32 v97, 0x64
	v_pk_fma_f32 v[18:19], v[20:21], v[18:19], 0.5 op_sel_hi:[1,1,0] neg_lo:[1,0,0] neg_hi:[1,0,0]
	s_nop 0
	v_pk_mul_f32 v[18:19], v[34:35], v[18:19]
	v_pk_mul_f32 v[20:21], v[8:9], v[8:9]
	v_pk_fma_f32 v[6:7], v[6:7], 0.5, v[18:19] op_sel_hi:[1,0,1]
	v_pk_fma_f32 v[18:19], v[24:25], s[12:13], v[16:17] op_sel_hi:[1,0,0]
	v_pk_mul_f32 v[20:21], v[20:21], s[10:11] op_sel_hi:[1,0]
	v_pk_fma_f32 v[18:19], v[24:25], v[18:19], s[14:15] op_sel_hi:[1,1,0]
	v_exp_f32_e32 v20, v20
	v_pk_fma_f32 v[18:19], v[24:25], v[18:19], s[2:3] op_sel_hi:[1,1,0]
	v_exp_f32_e32 v21, v21
	v_pk_fma_f32 v[18:19], v[24:25], v[18:19], s[8:9] op_sel_hi:[1,1,0]
	s_nop 0
	v_pk_mul_f32 v[18:19], v[24:25], v[18:19]
	v_and_b32_e32 v25, 0x7fffffff, v11
	v_and_b32_e32 v24, 0x7fffffff, v10
	v_pk_fma_f32 v[26:27], v[24:25], s[16:17], 1.0 op_sel_hi:[1,0,0]
	v_pk_fma_f32 v[18:19], v[20:21], v[18:19], 0.5 op_sel_hi:[1,1,0] neg_lo:[1,0,0] neg_hi:[1,0,0]
	v_rcp_f32_e32 v26, v26
	v_rcp_f32_e32 v27, v27
	v_pk_mul_f32 v[18:19], v[22:23], v[18:19]
	v_pk_mul_f32 v[20:21], v[10:11], v[10:11]
	v_pk_fma_f32 v[8:9], v[8:9], 0.5, v[18:19] op_sel_hi:[1,0,1]
	v_pk_fma_f32 v[18:19], v[26:27], s[12:13], v[16:17] op_sel_hi:[1,0,0]
	v_pk_mul_f32 v[20:21], v[20:21], s[10:11] op_sel_hi:[1,0]
	v_pk_fma_f32 v[18:19], v[26:27], v[18:19], s[14:15] op_sel_hi:[1,1,0]
	v_exp_f32_e32 v20, v20
	v_pk_fma_f32 v[18:19], v[26:27], v[18:19], s[2:3] op_sel_hi:[1,1,0]
	v_exp_f32_e32 v21, v21
	v_pk_fma_f32 v[18:19], v[26:27], v[18:19], s[8:9] op_sel_hi:[1,1,0]
	v_and_b32_e32 v23, 0x7fffffff, v13
	v_and_b32_e32 v22, 0x7fffffff, v12
	v_pk_mul_f32 v[18:19], v[26:27], v[18:19]
	v_pk_fma_f32 v[26:27], v[22:23], s[16:17], 1.0 op_sel_hi:[1,0,0]
	v_pk_fma_f32 v[18:19], v[20:21], v[18:19], 0.5 op_sel_hi:[1,1,0] neg_lo:[1,0,0] neg_hi:[1,0,0]
	v_rcp_f32_e32 v26, v26
	v_rcp_f32_e32 v27, v27
	v_pk_mul_f32 v[18:19], v[24:25], v[18:19]
	v_pk_mul_f32 v[20:21], v[12:13], v[12:13]
	v_pk_fma_f32 v[10:11], v[10:11], 0.5, v[18:19] op_sel_hi:[1,0,1]
	v_pk_fma_f32 v[18:19], v[26:27], s[12:13], v[16:17] op_sel_hi:[1,0,0]
	v_pk_mul_f32 v[20:21], v[20:21], s[10:11] op_sel_hi:[1,0]
	v_pk_fma_f32 v[18:19], v[26:27], v[18:19], s[14:15] op_sel_hi:[1,1,0]
	v_exp_f32_e32 v20, v20
	v_pk_fma_f32 v[18:19], v[26:27], v[18:19], s[2:3] op_sel_hi:[1,1,0]
	v_exp_f32_e32 v21, v21
	v_pk_fma_f32 v[18:19], v[26:27], v[18:19], s[8:9] op_sel_hi:[1,1,0]
	v_and_b32_e32 v25, 0x7fffffff, v15
	v_and_b32_e32 v24, 0x7fffffff, v14
	v_pk_mul_f32 v[18:19], v[26:27], v[18:19]
	v_pk_fma_f32 v[26:27], v[24:25], s[16:17], 1.0 op_sel_hi:[1,0,0]
	v_pk_fma_f32 v[18:19], v[20:21], v[18:19], 0.5 op_sel_hi:[1,1,0] neg_lo:[1,0,0] neg_hi:[1,0,0]
	v_rcp_f32_e32 v26, v26
	v_rcp_f32_e32 v27, v27
	v_pk_mul_f32 v[18:19], v[22:23], v[18:19]
	v_pk_fma_f32 v[16:17], v[26:27], s[12:13], v[16:17] op_sel_hi:[1,0,0]
	v_pk_fma_f32 v[12:13], v[12:13], 0.5, v[18:19] op_sel_hi:[1,0,1]
	v_pk_mul_f32 v[18:19], v[14:15], v[14:15]
	v_pk_fma_f32 v[16:17], v[26:27], v[16:17], s[14:15] op_sel_hi:[1,1,0]
	v_pk_mul_f32 v[18:19], v[18:19], s[10:11] op_sel_hi:[1,0]
	v_pk_fma_f32 v[16:17], v[26:27], v[16:17], s[2:3] op_sel_hi:[1,1,0]
	v_exp_f32_e32 v18, v18
	v_exp_f32_e32 v19, v19
	v_pk_fma_f32 v[16:17], v[26:27], v[16:17], s[8:9] op_sel_hi:[1,1,0]
	s_mov_b32 s3, 0x700000
	v_pk_mul_f32 v[16:17], v[26:27], v[16:17]
	s_mov_b32 s9, 0x42000000
	v_pk_fma_f32 v[16:17], v[18:19], v[16:17], 0.5 op_sel_hi:[1,1,0] neg_lo:[1,0,0] neg_hi:[1,0,0]
	v_max_f32_e64 v18, |v6|, |v7|
	v_pk_mul_f32 v[16:17], v[24:25], v[16:17]
	s_nop 0
	v_pk_fma_f32 v[14:15], v[14:15], 0.5, v[16:17] op_sel_hi:[1,0,1]
	v_max_f32_e64 v16, |v0|, |v1|
	v_max_f32_e64 v17, |v2|, |v3|
	v_max3_f32 v16, v16, 0, v17
	v_max_f32_e64 v17, |v4|, |v5|
	v_max3_f32 v16, v16, v17, v18
	v_max_f32_e64 v17, |v8|, |v9|
	v_max_f32_e64 v18, |v10|, |v11|
	v_max3_f32 v16, v16, v17, v18
	v_max_f32_e64 v17, |v12|, |v13|
	v_max_f32_e64 v18, |v14|, |v15|
	v_max3_f32 v16, v16, v17, v18
	v_mov_b32_e32 v17, v16
	s_nop 1
	v_permlane16_swap_b32_e32 v16, v17
	v_max_f32_e32 v17, v17, v17
	v_max_f32_e32 v16, v16, v16
	v_max_f32_e32 v16, v16, v17
	v_lshrrev_b32_e32 v17, 23, v16
	v_and_b32_e32 v16, 0x7fffff, v16
	v_cmp_lt_u32_e32 vcc, s3, v16
	s_nop 1
	v_addc_co_u32_e32 v16, vcc, v17, v96, vcc
	v_med3_i32 v98, v16, s5, v97
	v_lshlrev_b32_e32 v16, 23, v98
	v_sub_u32_e32 v16, 1.0, v16
	v_pk_mul_f32 v[40:41], v[16:17], v[8:9] op_sel_hi:[0,1]
	v_pk_mul_f32 v[42:43], v[16:17], v[10:11] op_sel_hi:[0,1]
	v_pk_mul_f32 v[44:45], v[16:17], v[12:13] op_sel_hi:[0,1]
	v_pk_mul_f32 v[46:47], v[16:17], v[14:15] op_sel_hi:[0,1]
	v_pk_mul_f32 v[32:33], v[16:17], v[0:1] op_sel_hi:[0,1]
	v_pk_mul_f32 v[34:35], v[16:17], v[2:3] op_sel_hi:[0,1]
	v_pk_mul_f32 v[36:37], v[16:17], v[4:5] op_sel_hi:[0,1]
	v_pk_mul_f32 v[38:39], v[16:17], v[6:7] op_sel_hi:[0,1]
	v_cvt_scalef32_2xpk16_fp6_f32 v[100:105], v[32:47], v[40:55], 1.0
	v_cvt_scalef32_pk32_f32_fp6 v[0:31], v[100:105], s9
	v_fma_f32 v16, v32, s4, v0
	v_fma_f32 v17, v33, s4, v2
	v_fma_f32 v18, v34, s4, v4
	v_fma_f32 v19, v35, s4, v6
	v_fma_f32 v20, v36, s4, v8
	v_fma_f32 v21, v37, s4, v10
	v_fma_f32 v22, v38, s4, v12
	v_fma_f32 v23, v39, s4, v14
	v_fma_f32 v24, v40, s4, v1
	v_fma_f32 v25, v41, s4, v3
	v_fma_f32 v26, v42, s4, v5
	v_fma_f32 v27, v43, s4, v7
	v_fma_f32 v28, v44, s4, v9
	v_fma_f32 v29, v45, s4, v11
	v_fma_f32 v30, v46, s4, v13
	v_fma_f32 v31, v47, s4, v15
	v_cvt_scalef32_2xpk16_fp6_f32 v[0:5], v[16:31], v[24:39], 1.0
	v_lshl_add_u64 v[4:5], v[118:119], 0, v[164:165]
	v_lshl_add_u64 v[4:5], v[4:5], 0, v[160:161]
	global_store_dwordx3 v[4:5], v[100:102], off nt
	v_add_co_u32_e32 v4, vcc, 0x1000, v4
	v_xor_b32_e32 v0, 0x20820820, v0
	v_xor_b32_e32 v1, 0x8208208, v1
	v_xor_b32_e32 v2, 0x82082082, v2
	v_addc_co_u32_e32 v5, vcc, 0, v5, vcc
	global_store_dwordx3 v[4:5], v[0:2], off offset:2048 nt
	s_and_saveexec_b64 s[6:7], s[0:1]
	s_cbranch_execz .LBB3_16
	v_mov_b32_e32 v1, 0x7a00
	v_add_u32_e32 v0, 0x7f, v98
	v_lshl_add_u32 v1, v98, 8, v1
	v_mov_b32_e32 v163, 0
	v_or_b32_e32 v2, v1, v0
	v_lshl_add_u64 v[0:1], v[116:117], 0, v[162:163]
	global_store_short v[0:1], v2, off
.LBB3_16:
	s_or_b64 exec, exec, s[6:7]
	v_permlane32_swap_b32_e32 v92, v84
	v_permlane32_swap_b32_e32 v93, v85
	v_permlane32_swap_b32_e32 v94, v86
	v_permlane32_swap_b32_e32 v95, v87
	v_permlane32_swap_b32_e32 v90, v82
	v_permlane32_swap_b32_e32 v91, v83
	v_permlane32_swap_b32_e32 v88, v80
	v_permlane32_swap_b32_e32 v89, v81
	v_mov_b64_e32 v[16:17], s[18:19]
	v_pk_mul_f32 v[0:1], v[208:209], v[92:93]
	v_pk_mul_f32 v[2:3], v[210:211], v[94:95]
	v_and_b32_e32 v19, 0x7fffffff, v1
	v_and_b32_e32 v18, 0x7fffffff, v0
	v_pk_mul_f32 v[6:7], v[214:215], v[90:91]
	v_and_b32_e32 v23, 0x7fffffff, v3
	v_and_b32_e32 v22, 0x7fffffff, v2
	v_pk_fma_f32 v[36:37], v[18:19], s[16:17], 1.0 op_sel_hi:[1,0,0]
	v_pk_mul_f32 v[4:5], v[212:213], v[88:89]
	v_and_b32_e32 v31, 0x7fffffff, v7
	v_and_b32_e32 v30, 0x7fffffff, v6
	v_pk_fma_f32 v[38:39], v[22:23], s[16:17], 1.0 op_sel_hi:[1,0,0]
	v_rcp_f32_e32 v36, v36
	v_rcp_f32_e32 v37, v37
	v_and_b32_e32 v27, 0x7fffffff, v5
	v_and_b32_e32 v26, 0x7fffffff, v4
	v_pk_fma_f32 v[42:43], v[30:31], s[16:17], 1.0 op_sel_hi:[1,0,0]
	v_rcp_f32_e32 v38, v38
	v_rcp_f32_e32 v39, v39
	v_pk_fma_f32 v[40:41], v[26:27], s[16:17], 1.0 op_sel_hi:[1,0,0]
	v_rcp_f32_e32 v42, v42
	v_rcp_f32_e32 v43, v43
	v_pk_mul_f32 v[20:21], v[0:1], v[0:1]
	v_rcp_f32_e32 v40, v40
	v_rcp_f32_e32 v41, v41
	v_pk_mul_f32 v[24:25], v[2:3], v[2:3]
	v_pk_mul_f32 v[20:21], v[20:21], s[10:11] op_sel_hi:[1,0]
	v_pk_fma_f32 v[46:47], v[36:37], s[12:13], v[16:17] op_sel_hi:[1,0,0]
	v_pk_mul_f32 v[8:9], v[216:217], v[84:85]
	v_pk_mul_f32 v[32:33], v[6:7], v[6:7]
	v_pk_mul_f32 v[24:25], v[24:25], s[10:11] op_sel_hi:[1,0]
	v_exp_f32_e32 v20, v20
	v_exp_f32_e32 v21, v21
	v_pk_fma_f32 v[84:85], v[38:39], s[12:13], v[16:17] op_sel_hi:[1,0,0]
	v_pk_fma_f32 v[46:47], v[36:37], v[46:47], s[14:15] op_sel_hi:[1,1,0]
	v_pk_mul_f32 v[28:29], v[4:5], v[4:5]
	v_pk_mul_f32 v[32:33], v[32:33], s[10:11] op_sel_hi:[1,0]
	v_exp_f32_e32 v24, v24
	v_exp_f32_e32 v25, v25
	v_pk_fma_f32 v[90:91], v[42:43], s[12:13], v[16:17] op_sel_hi:[1,0,0]
	v_pk_fma_f32 v[84:85], v[38:39], v[84:85], s[14:15] op_sel_hi:[1,1,0]
	v_pk_fma_f32 v[46:47], v[36:37], v[46:47], s[2:3] op_sel_hi:[1,1,0]
	v_and_b32_e32 v35, 0x7fffffff, v9
	v_and_b32_e32 v34, 0x7fffffff, v8
	v_pk_mul_f32 v[28:29], v[28:29], s[10:11] op_sel_hi:[1,0]
	v_exp_f32_e32 v32, v32
	v_exp_f32_e32 v33, v33
	v_pk_fma_f32 v[88:89], v[40:41], s[12:13], v[16:17] op_sel_hi:[1,0,0]
	v_pk_fma_f32 v[90:91], v[42:43], v[90:91], s[14:15] op_sel_hi:[1,1,0]
	v_pk_fma_f32 v[84:85], v[38:39], v[84:85], s[2:3] op_sel_hi:[1,1,0]
	v_pk_fma_f32 v[46:47], v[36:37], v[46:47], s[8:9] op_sel_hi:[1,1,0]
	v_pk_fma_f32 v[44:45], v[34:35], s[16:17], 1.0 op_sel_hi:[1,0,0]
	v_exp_f32_e32 v28, v28
	v_exp_f32_e32 v29, v29
	v_pk_fma_f32 v[88:89], v[40:41], v[88:89], s[14:15] op_sel_hi:[1,1,0]
	v_pk_fma_f32 v[90:91], v[42:43], v[90:91], s[2:3] op_sel_hi:[1,1,0]
	v_pk_fma_f32 v[84:85], v[38:39], v[84:85], s[8:9] op_sel_hi:[1,1,0]
	v_pk_mul_f32 v[36:37], v[36:37], v[46:47]
	v_rcp_f32_e32 v44, v44
	v_pk_fma_f32 v[88:89], v[40:41], v[88:89], s[2:3] op_sel_hi:[1,1,0]
	v_pk_fma_f32 v[90:91], v[42:43], v[90:91], s[8:9] op_sel_hi:[1,1,0]
	v_pk_mul_f32 v[38:39], v[38:39], v[84:85]
	v_pk_fma_f32 v[20:21], v[20:21], v[36:37], 0.5 op_sel_hi:[1,1,0] neg_lo:[1,0,0] neg_hi:[1,0,0]
	v_rcp_f32_e32 v45, v45
	v_pk_fma_f32 v[88:89], v[40:41], v[88:89], s[8:9] op_sel_hi:[1,1,0]
	v_pk_mul_f32 v[42:43], v[42:43], v[90:91]
	v_pk_fma_f32 v[24:25], v[24:25], v[38:39], 0.5 op_sel_hi:[1,1,0] neg_lo:[1,0,0] neg_hi:[1,0,0]
	v_pk_mul_f32 v[18:19], v[18:19], v[20:21]
	v_pk_mul_f32 v[40:41], v[40:41], v[88:89]
	v_pk_mul_f32 v[20:21], v[22:23], v[24:25]
	v_pk_fma_f32 v[0:1], v[0:1], 0.5, v[18:19] op_sel_hi:[1,0,1]
	v_pk_fma_f32 v[18:19], v[32:33], v[42:43], 0.5 op_sel_hi:[1,1,0] neg_lo:[1,0,0] neg_hi:[1,0,0]
	v_pk_fma_f32 v[28:29], v[28:29], v[40:41], 0.5 op_sel_hi:[1,1,0] neg_lo:[1,0,0] neg_hi:[1,0,0]
	v_pk_fma_f32 v[2:3], v[2:3], 0.5, v[20:21] op_sel_hi:[1,0,1]
	v_pk_mul_f32 v[18:19], v[30:31], v[18:19]
	v_pk_mul_f32 v[20:21], v[8:9], v[8:9]
	v_pk_mul_f32 v[22:23], v[26:27], v[28:29]
	v_pk_fma_f32 v[6:7], v[6:7], 0.5, v[18:19] op_sel_hi:[1,0,1]
	v_pk_fma_f32 v[18:19], v[44:45], s[12:13], v[16:17] op_sel_hi:[1,0,0]
	v_pk_mul_f32 v[20:21], v[20:21], s[10:11] op_sel_hi:[1,0]
	v_pk_mul_f32 v[10:11], v[218:219], v[86:87]
	v_pk_fma_f32 v[4:5], v[4:5], 0.5, v[22:23] op_sel_hi:[1,0,1]
	v_pk_fma_f32 v[18:19], v[44:45], v[18:19], s[14:15] op_sel_hi:[1,1,0]
	v_exp_f32_e32 v20, v20
	v_exp_f32_e32 v21, v21
	v_and_b32_e32 v23, 0x7fffffff, v11
	v_and_b32_e32 v22, 0x7fffffff, v10
	v_pk_fma_f32 v[18:19], v[44:45], v[18:19], s[2:3] op_sel_hi:[1,1,0]
	v_pk_fma_f32 v[24:25], v[22:23], s[16:17], 1.0 op_sel_hi:[1,0,0]
	v_pk_fma_f32 v[18:19], v[44:45], v[18:19], s[8:9] op_sel_hi:[1,1,0]
	v_rcp_f32_e32 v24, v24
	v_rcp_f32_e32 v25, v25
	v_pk_mul_f32 v[18:19], v[44:45], v[18:19]
	v_pk_mul_f32 v[12:13], v[220:221], v[80:81]
	v_pk_fma_f32 v[18:19], v[20:21], v[18:19], 0.5 op_sel_hi:[1,1,0] neg_lo:[1,0,0] neg_hi:[1,0,0]
	v_pk_mul_f32 v[20:21], v[10:11], v[10:11]
	v_pk_mul_f32 v[18:19], v[34:35], v[18:19]
	v_pk_mul_f32 v[20:21], v[20:21], s[10:11] op_sel_hi:[1,0]
	v_pk_fma_f32 v[8:9], v[8:9], 0.5, v[18:19] op_sel_hi:[1,0,1]
	v_pk_fma_f32 v[18:19], v[24:25], s[12:13], v[16:17] op_sel_hi:[1,0,0]
	v_exp_f32_e32 v20, v20
	v_pk_fma_f32 v[18:19], v[24:25], v[18:19], s[14:15] op_sel_hi:[1,1,0]
	v_exp_f32_e32 v21, v21
	v_pk_fma_f32 v[18:19], v[24:25], v[18:19], s[2:3] op_sel_hi:[1,1,0]
	v_pk_mul_f32 v[14:15], v[222:223], v[82:83]
	v_pk_fma_f32 v[18:19], v[24:25], v[18:19], s[8:9] op_sel_hi:[1,1,0]
	s_nop 0
	v_pk_mul_f32 v[18:19], v[24:25], v[18:19]
	v_and_b32_e32 v25, 0x7fffffff, v13
	v_and_b32_e32 v24, 0x7fffffff, v12
	v_pk_fma_f32 v[26:27], v[24:25], s[16:17], 1.0 op_sel_hi:[1,0,0]
	v_pk_fma_f32 v[18:19], v[20:21], v[18:19], 0.5 op_sel_hi:[1,1,0] neg_lo:[1,0,0] neg_hi:[1,0,0]
	v_rcp_f32_e32 v26, v26
	v_rcp_f32_e32 v27, v27
	v_pk_mul_f32 v[18:19], v[22:23], v[18:19]
	v_pk_mul_f32 v[20:21], v[12:13], v[12:13]
	v_pk_fma_f32 v[10:11], v[10:11], 0.5, v[18:19] op_sel_hi:[1,0,1]
	v_pk_fma_f32 v[18:19], v[26:27], s[12:13], v[16:17] op_sel_hi:[1,0,0]
	v_pk_mul_f32 v[20:21], v[20:21], s[10:11] op_sel_hi:[1,0]
	v_pk_fma_f32 v[18:19], v[26:27], v[18:19], s[14:15] op_sel_hi:[1,1,0]
	v_exp_f32_e32 v20, v20
	v_pk_fma_f32 v[18:19], v[26:27], v[18:19], s[2:3] op_sel_hi:[1,1,0]
	v_exp_f32_e32 v21, v21
	v_pk_fma_f32 v[18:19], v[26:27], v[18:19], s[8:9] op_sel_hi:[1,1,0]
	v_and_b32_e32 v23, 0x7fffffff, v15
	v_and_b32_e32 v22, 0x7fffffff, v14
	v_pk_mul_f32 v[18:19], v[26:27], v[18:19]
	v_pk_fma_f32 v[26:27], v[22:23], s[16:17], 1.0 op_sel_hi:[1,0,0]
	v_pk_fma_f32 v[18:19], v[20:21], v[18:19], 0.5 op_sel_hi:[1,1,0] neg_lo:[1,0,0] neg_hi:[1,0,0]
	v_rcp_f32_e32 v26, v26
	v_rcp_f32_e32 v27, v27
	v_pk_mul_f32 v[18:19], v[24:25], v[18:19]
	v_pk_fma_f32 v[16:17], v[26:27], s[12:13], v[16:17] op_sel_hi:[1,0,0]
	v_pk_fma_f32 v[12:13], v[12:13], 0.5, v[18:19] op_sel_hi:[1,0,1]
	v_pk_mul_f32 v[18:19], v[14:15], v[14:15]
	v_pk_fma_f32 v[16:17], v[26:27], v[16:17], s[14:15] op_sel_hi:[1,1,0]
	v_pk_mul_f32 v[18:19], v[18:19], s[10:11] op_sel_hi:[1,0]
	v_pk_fma_f32 v[16:17], v[26:27], v[16:17], s[2:3] op_sel_hi:[1,1,0]
	v_exp_f32_e32 v18, v18
	v_exp_f32_e32 v19, v19
	v_pk_fma_f32 v[16:17], v[26:27], v[16:17], s[8:9] op_sel_hi:[1,1,0]
	s_nop 0
	v_pk_mul_f32 v[16:17], v[26:27], v[16:17]
	s_nop 0
	v_pk_fma_f32 v[16:17], v[18:19], v[16:17], 0.5 op_sel_hi:[1,1,0] neg_lo:[1,0,0] neg_hi:[1,0,0]
	v_max_f32_e64 v18, |v6|, |v7|
	v_pk_mul_f32 v[16:17], v[22:23], v[16:17]
	s_nop 0
	v_pk_fma_f32 v[14:15], v[14:15], 0.5, v[16:17] op_sel_hi:[1,0,1]
	v_max_f32_e64 v16, |v0|, |v1|
	v_max_f32_e64 v17, |v2|, |v3|
	v_max3_f32 v16, v16, 0, v17
	v_max_f32_e64 v17, |v4|, |v5|
	v_max3_f32 v16, v16, v17, v18
	v_max_f32_e64 v17, |v8|, |v9|
	v_max_f32_e64 v18, |v10|, |v11|
	v_max3_f32 v16, v16, v17, v18
	v_max_f32_e64 v17, |v12|, |v13|
	v_max_f32_e64 v18, |v14|, |v15|
	v_max3_f32 v16, v16, v17, v18
	v_mov_b32_e32 v17, v16
	s_nop 1
	v_permlane16_swap_b32_e32 v16, v17
	v_max_f32_e32 v17, v17, v17
	v_max_f32_e32 v16, v16, v16
	v_max_f32_e32 v16, v16, v17
	v_lshrrev_b32_e32 v17, 23, v16
	v_and_b32_e32 v16, 0x7fffff, v16
	v_cmp_lt_u32_e32 vcc, s3, v16
	s_nop 1
	v_addc_co_u32_e32 v16, vcc, v17, v96, vcc
	v_med3_i32 v80, v16, s5, v97
	v_lshlrev_b32_e32 v16, 23, v80
	v_sub_u32_e32 v16, 1.0, v16
	v_pk_mul_f32 v[40:41], v[16:17], v[8:9] op_sel_hi:[0,1]
	v_pk_mul_f32 v[42:43], v[16:17], v[10:11] op_sel_hi:[0,1]
	v_pk_mul_f32 v[44:45], v[16:17], v[12:13] op_sel_hi:[0,1]
	v_pk_mul_f32 v[46:47], v[16:17], v[14:15] op_sel_hi:[0,1]
	v_pk_mul_f32 v[32:33], v[16:17], v[0:1] op_sel_hi:[0,1]
	v_pk_mul_f32 v[34:35], v[16:17], v[2:3] op_sel_hi:[0,1]
	v_pk_mul_f32 v[36:37], v[16:17], v[4:5] op_sel_hi:[0,1]
	v_pk_mul_f32 v[38:39], v[16:17], v[6:7] op_sel_hi:[0,1]
	v_cvt_scalef32_2xpk16_fp6_f32 v[82:87], v[32:47], v[40:55], 1.0
	v_cvt_scalef32_pk32_f32_fp6 v[0:31], v[82:87], s9
	v_fma_f32 v16, v32, s4, v0
	v_fma_f32 v17, v33, s4, v2
	v_fma_f32 v18, v34, s4, v4
	v_fma_f32 v19, v35, s4, v6
	v_fma_f32 v20, v36, s4, v8
	v_fma_f32 v21, v37, s4, v10
	v_fma_f32 v22, v38, s4, v12
	v_fma_f32 v23, v39, s4, v14
	v_fma_f32 v24, v40, s4, v1
	v_fma_f32 v25, v41, s4, v3
	v_fma_f32 v26, v42, s4, v5
	v_fma_f32 v27, v43, s4, v7
	v_fma_f32 v28, v44, s4, v9
	v_fma_f32 v29, v45, s4, v11
	v_fma_f32 v30, v46, s4, v13
	v_fma_f32 v31, v47, s4, v15
	v_cvt_scalef32_2xpk16_fp6_f32 v[0:5], v[16:31], v[24:39], 1.0
	v_lshl_add_u64 v[4:5], v[118:119], 0, v[146:147]
	v_lshl_add_u64 v[4:5], v[4:5], 0, v[160:161]
	global_store_dwordx3 v[4:5], v[82:84], off nt
	v_add_co_u32_e32 v4, vcc, 0x1000, v4
	v_xor_b32_e32 v0, 0x20820820, v0
	v_xor_b32_e32 v1, 0x8208208, v1
	v_xor_b32_e32 v2, 0x82082082, v2
	v_addc_co_u32_e32 v5, vcc, 0, v5, vcc
	global_store_dwordx3 v[4:5], v[0:2], off offset:2048 nt
	s_and_saveexec_b64 s[2:3], s[0:1]
	s_cbranch_execz .LBB3_18
	v_mov_b32_e32 v1, 0x7a00
	v_add_u32_e32 v0, 0x7f, v80
	v_lshl_add_u32 v1, v80, 8, v1
	v_mov_b32_e32 v145, 0
	v_or_b32_e32 v2, v1, v0
	v_lshl_add_u64 v[0:1], v[116:117], 0, v[144:145]
	global_store_short v[0:1], v2, off
.LBB3_18:
	s_or_b64 exec, exec, s[2:3]
	v_permlane32_swap_b32_e32 v76, v68
	v_permlane32_swap_b32_e32 v77, v69
	v_permlane32_swap_b32_e32 v78, v70
	v_permlane32_swap_b32_e32 v79, v71
	v_permlane32_swap_b32_e32 v72, v64
	v_permlane32_swap_b32_e32 v73, v65
	s_mov_b32 s12, 0x3e6d3388
	v_permlane32_swap_b32_e32 v74, v66
	v_permlane32_swap_b32_e32 v75, v67
	s_mov_b32 s16, 0xbf3a00e3
	s_mov_b32 s8, 0x3f07dc22
	s_mov_b32 s6, 0xbf38aa3b
	v_mov_b64_e32 v[16:17], s[16:17]
	s_mov_b32 s10, 0x3f35f0e3
	s_mov_b32 s2, 0xbe11a98e
	s_mov_b32 s4, 0x3e027906
	s_mov_b32 s14, 0xc2000000
	v_pk_mul_f32 v[0:1], v[208:209], v[76:77]
	v_pk_mul_f32 v[2:3], v[210:211], v[78:79]
	v_pk_mul_f32 v[4:5], v[212:213], v[72:73]
	v_and_b32_e32 v19, 0x7fffffff, v1
	v_and_b32_e32 v18, 0x7fffffff, v0
	v_and_b32_e32 v23, 0x7fffffff, v3
	v_and_b32_e32 v22, 0x7fffffff, v2
	v_and_b32_e32 v27, 0x7fffffff, v5
	v_and_b32_e32 v26, 0x7fffffff, v4
	v_pk_fma_f32 v[34:35], v[18:19], s[12:13], 1.0 op_sel_hi:[1,0,0]
	v_pk_fma_f32 v[36:37], v[22:23], s[12:13], 1.0 op_sel_hi:[1,0,0]
	v_pk_fma_f32 v[38:39], v[26:27], s[12:13], 1.0 op_sel_hi:[1,0,0]
	v_rcp_f32_e32 v34, v34
	v_rcp_f32_e32 v35, v35
	v_rcp_f32_e32 v36, v36
	v_rcp_f32_e32 v37, v37
	v_rcp_f32_e32 v38, v38
	v_rcp_f32_e32 v39, v39
	v_pk_mul_f32 v[6:7], v[214:215], v[74:75]
	v_pk_mul_f32 v[20:21], v[0:1], v[0:1]
	v_pk_mul_f32 v[24:25], v[2:3], v[2:3]
	v_pk_mul_f32 v[28:29], v[4:5], v[4:5]
	v_and_b32_e32 v31, 0x7fffffff, v7
	v_and_b32_e32 v30, 0x7fffffff, v6
	v_pk_mul_f32 v[20:21], v[20:21], s[6:7] op_sel_hi:[1,0]
	v_pk_mul_f32 v[24:25], v[24:25], s[6:7] op_sel_hi:[1,0]
	v_pk_fma_f32 v[42:43], v[34:35], s[8:9], v[16:17] op_sel_hi:[1,0,0]
	v_pk_fma_f32 v[44:45], v[36:37], s[8:9], v[16:17] op_sel_hi:[1,0,0]
	v_pk_mul_f32 v[28:29], v[28:29], s[6:7] op_sel_hi:[1,0]
	v_pk_fma_f32 v[40:41], v[30:31], s[12:13], 1.0 op_sel_hi:[1,0,0]
	v_exp_f32_e32 v20, v20
	v_exp_f32_e32 v21, v21
	v_exp_f32_e32 v24, v24
	v_exp_f32_e32 v25, v25
	v_pk_fma_f32 v[46:47], v[38:39], s[8:9], v[16:17] op_sel_hi:[1,0,0]
	v_pk_fma_f32 v[42:43], v[34:35], v[42:43], s[10:11] op_sel_hi:[1,1,0]
	v_pk_fma_f32 v[44:45], v[36:37], v[44:45], s[10:11] op_sel_hi:[1,1,0]
	v_exp_f32_e32 v28, v28
	v_exp_f32_e32 v29, v29
	v_rcp_f32_e32 v40, v40
	v_rcp_f32_e32 v41, v41
	v_pk_fma_f32 v[46:47], v[38:39], v[46:47], s[10:11] op_sel_hi:[1,1,0]
	v_pk_fma_f32 v[42:43], v[34:35], v[42:43], s[2:3] op_sel_hi:[1,1,0]
	v_pk_fma_f32 v[44:45], v[36:37], v[44:45], s[2:3] op_sel_hi:[1,1,0]
	v_pk_fma_f32 v[46:47], v[38:39], v[46:47], s[2:3] op_sel_hi:[1,1,0]
	v_pk_fma_f32 v[42:43], v[34:35], v[42:43], s[4:5] op_sel_hi:[1,1,0]
	v_pk_fma_f32 v[44:45], v[36:37], v[44:45], s[4:5] op_sel_hi:[1,1,0]
	v_pk_fma_f32 v[46:47], v[38:39], v[46:47], s[4:5] op_sel_hi:[1,1,0]
	v_pk_mul_f32 v[34:35], v[34:35], v[42:43]
	v_pk_mul_f32 v[36:37], v[36:37], v[44:45]
	v_pk_mul_f32 v[32:33], v[6:7], v[6:7]
	v_pk_mul_f32 v[38:39], v[38:39], v[46:47]
	v_pk_fma_f32 v[20:21], v[20:21], v[34:35], 0.5 op_sel_hi:[1,1,0] neg_lo:[1,0,0] neg_hi:[1,0,0]
	v_pk_fma_f32 v[24:25], v[24:25], v[36:37], 0.5 op_sel_hi:[1,1,0] neg_lo:[1,0,0] neg_hi:[1,0,0]
	v_pk_mul_f32 v[32:33], v[32:33], s[6:7] op_sel_hi:[1,0]
	v_pk_fma_f32 v[72:73], v[40:41], s[8:9], v[16:17] op_sel_hi:[1,0,0]
	v_pk_fma_f32 v[28:29], v[28:29], v[38:39], 0.5 op_sel_hi:[1,1,0] neg_lo:[1,0,0] neg_hi:[1,0,0]
	v_pk_mul_f32 v[18:19], v[18:19], v[20:21]
	v_pk_mul_f32 v[20:21], v[22:23], v[24:25]
	v_pk_mul_f32 v[8:9], v[216:217], v[68:69]
	v_pk_fma_f32 v[72:73], v[40:41], v[72:73], s[10:11] op_sel_hi:[1,1,0]
	v_pk_mul_f32 v[22:23], v[26:27], v[28:29]
	v_pk_fma_f32 v[0:1], v[0:1], 0.5, v[18:19] op_sel_hi:[1,0,1]
	v_pk_fma_f32 v[2:3], v[2:3], 0.5, v[20:21] op_sel_hi:[1,0,1]
	v_exp_f32_e32 v18, v32
	v_exp_f32_e32 v19, v33
	v_and_b32_e32 v21, 0x7fffffff, v9
	v_and_b32_e32 v20, 0x7fffffff, v8
	v_pk_fma_f32 v[72:73], v[40:41], v[72:73], s[2:3] op_sel_hi:[1,1,0]
	v_pk_fma_f32 v[4:5], v[4:5], 0.5, v[22:23] op_sel_hi:[1,0,1]
	v_pk_fma_f32 v[22:23], v[20:21], s[12:13], 1.0 op_sel_hi:[1,0,0]
	v_pk_fma_f32 v[72:73], v[40:41], v[72:73], s[4:5] op_sel_hi:[1,1,0]
	v_rcp_f32_e32 v22, v22
	v_rcp_f32_e32 v23, v23
	v_pk_mul_f32 v[40:41], v[40:41], v[72:73]
	v_pk_mul_f32 v[10:11], v[218:219], v[70:71]
	v_pk_fma_f32 v[18:19], v[18:19], v[40:41], 0.5 op_sel_hi:[1,1,0] neg_lo:[1,0,0] neg_hi:[1,0,0]
	v_and_b32_e32 v25, 0x7fffffff, v11
	v_pk_mul_f32 v[18:19], v[30:31], v[18:19]
	v_and_b32_e32 v24, 0x7fffffff, v10
	v_pk_fma_f32 v[6:7], v[6:7], 0.5, v[18:19] op_sel_hi:[1,0,1]
	v_pk_fma_f32 v[18:19], v[22:23], s[8:9], v[16:17] op_sel_hi:[1,0,0]
	v_pk_fma_f32 v[26:27], v[24:25], s[12:13], 1.0 op_sel_hi:[1,0,0]
	v_pk_fma_f32 v[18:19], v[22:23], v[18:19], s[10:11] op_sel_hi:[1,1,0]
	v_rcp_f32_e32 v26, v26
	v_pk_fma_f32 v[18:19], v[22:23], v[18:19], s[2:3] op_sel_hi:[1,1,0]
	v_rcp_f32_e32 v27, v27
	v_pk_fma_f32 v[18:19], v[22:23], v[18:19], s[4:5] op_sel_hi:[1,1,0]
	v_pk_mul_f32 v[12:13], v[220:221], v[64:65]
	v_pk_mul_f32 v[18:19], v[22:23], v[18:19]
	v_pk_mul_f32 v[22:23], v[8:9], v[8:9]
	v_pk_mul_f32 v[14:15], v[222:223], v[66:67]
	v_pk_mul_f32 v[22:23], v[22:23], s[6:7] op_sel_hi:[1,0]
	v_mov_b32_e32 v64, 0xffffff7f
	v_exp_f32_e32 v22, v22
	v_exp_f32_e32 v23, v23
	v_mov_b32_e32 v65, 0x64
	v_pk_fma_f32 v[18:19], v[22:23], v[18:19], 0.5 op_sel_hi:[1,1,0] neg_lo:[1,0,0] neg_hi:[1,0,0]
	s_nop 0
	v_pk_mul_f32 v[18:19], v[20:21], v[18:19]
	v_pk_mul_f32 v[20:21], v[10:11], v[10:11]
	v_pk_fma_f32 v[8:9], v[8:9], 0.5, v[18:19] op_sel_hi:[1,0,1]
	v_pk_fma_f32 v[18:19], v[26:27], s[8:9], v[16:17] op_sel_hi:[1,0,0]
	v_pk_mul_f32 v[20:21], v[20:21], s[6:7] op_sel_hi:[1,0]
	v_pk_fma_f32 v[18:19], v[26:27], v[18:19], s[10:11] op_sel_hi:[1,1,0]
	v_exp_f32_e32 v20, v20
	v_pk_fma_f32 v[18:19], v[26:27], v[18:19], s[2:3] op_sel_hi:[1,1,0]
	v_exp_f32_e32 v21, v21
	v_pk_fma_f32 v[18:19], v[26:27], v[18:19], s[4:5] op_sel_hi:[1,1,0]
	v_and_b32_e32 v23, 0x7fffffff, v13
	v_and_b32_e32 v22, 0x7fffffff, v12
	v_pk_mul_f32 v[18:19], v[26:27], v[18:19]
	v_pk_fma_f32 v[26:27], v[22:23], s[12:13], 1.0 op_sel_hi:[1,0,0]
	v_pk_fma_f32 v[18:19], v[20:21], v[18:19], 0.5 op_sel_hi:[1,1,0] neg_lo:[1,0,0] neg_hi:[1,0,0]
	v_rcp_f32_e32 v26, v26
	v_rcp_f32_e32 v27, v27
	v_pk_mul_f32 v[18:19], v[24:25], v[18:19]
	v_pk_mul_f32 v[20:21], v[12:13], v[12:13]
	v_pk_fma_f32 v[10:11], v[10:11], 0.5, v[18:19] op_sel_hi:[1,0,1]
	v_pk_fma_f32 v[18:19], v[26:27], s[8:9], v[16:17] op_sel_hi:[1,0,0]
	v_pk_mul_f32 v[20:21], v[20:21], s[6:7] op_sel_hi:[1,0]
	v_pk_fma_f32 v[18:19], v[26:27], v[18:19], s[10:11] op_sel_hi:[1,1,0]
	v_exp_f32_e32 v20, v20
	v_pk_fma_f32 v[18:19], v[26:27], v[18:19], s[2:3] op_sel_hi:[1,1,0]
	v_exp_f32_e32 v21, v21
	v_pk_fma_f32 v[18:19], v[26:27], v[18:19], s[4:5] op_sel_hi:[1,1,0]
	v_and_b32_e32 v25, 0x7fffffff, v15
	v_and_b32_e32 v24, 0x7fffffff, v14
	v_pk_mul_f32 v[18:19], v[26:27], v[18:19]
	v_pk_fma_f32 v[26:27], v[24:25], s[12:13], 1.0 op_sel_hi:[1,0,0]
	v_pk_fma_f32 v[18:19], v[20:21], v[18:19], 0.5 op_sel_hi:[1,1,0] neg_lo:[1,0,0] neg_hi:[1,0,0]
	v_rcp_f32_e32 v26, v26
	v_rcp_f32_e32 v27, v27
	v_pk_mul_f32 v[18:19], v[22:23], v[18:19]
	v_pk_fma_f32 v[16:17], v[26:27], s[8:9], v[16:17] op_sel_hi:[1,0,0]
	v_pk_fma_f32 v[12:13], v[12:13], 0.5, v[18:19] op_sel_hi:[1,0,1]
	v_pk_mul_f32 v[18:19], v[14:15], v[14:15]
	v_pk_fma_f32 v[16:17], v[26:27], v[16:17], s[10:11] op_sel_hi:[1,1,0]
	v_pk_mul_f32 v[18:19], v[18:19], s[6:7] op_sel_hi:[1,0]
	v_pk_fma_f32 v[16:17], v[26:27], v[16:17], s[2:3] op_sel_hi:[1,1,0]
	v_exp_f32_e32 v18, v18
	v_exp_f32_e32 v19, v19
	v_pk_fma_f32 v[16:17], v[26:27], v[16:17], s[4:5] op_sel_hi:[1,1,0]
	s_mov_b32 s3, 0x700000
	v_pk_mul_f32 v[16:17], v[26:27], v[16:17]
	s_mov_b32 s7, 0x42000000
	v_pk_fma_f32 v[16:17], v[18:19], v[16:17], 0.5 op_sel_hi:[1,1,0] neg_lo:[1,0,0] neg_hi:[1,0,0]
	v_max_f32_e64 v18, |v6|, |v7|
	v_pk_mul_f32 v[16:17], v[24:25], v[16:17]
	s_nop 0
	v_pk_fma_f32 v[14:15], v[14:15], 0.5, v[16:17] op_sel_hi:[1,0,1]
	v_max_f32_e64 v16, |v0|, |v1|
	v_max_f32_e64 v17, |v2|, |v3|
	v_max3_f32 v16, v16, 0, v17
	v_max_f32_e64 v17, |v4|, |v5|
	v_max3_f32 v16, v16, v17, v18
	v_max_f32_e64 v17, |v8|, |v9|
	v_max_f32_e64 v18, |v10|, |v11|
	v_max3_f32 v16, v16, v17, v18
	v_max_f32_e64 v17, |v12|, |v13|
	v_max_f32_e64 v18, |v14|, |v15|
	v_max3_f32 v16, v16, v17, v18
	v_mov_b32_e32 v17, v16
	s_nop 1
	v_permlane16_swap_b32_e32 v16, v17
	v_max_f32_e32 v17, v17, v17
	v_max_f32_e32 v16, v16, v16
	v_max_f32_e32 v16, v16, v17
	v_lshrrev_b32_e32 v17, 23, v16
	v_and_b32_e32 v16, 0x7fffff, v16
	v_cmp_lt_u32_e32 vcc, s3, v16
	s_nop 1
	v_addc_co_u32_e32 v16, vcc, v17, v64, vcc
	v_med3_i32 v66, v16, s5, v65
	v_lshlrev_b32_e32 v16, 23, v66
	v_sub_u32_e32 v16, 1.0, v16
	v_pk_mul_f32 v[40:41], v[16:17], v[8:9] op_sel_hi:[0,1]
	v_pk_mul_f32 v[42:43], v[16:17], v[10:11] op_sel_hi:[0,1]
	v_pk_mul_f32 v[44:45], v[16:17], v[12:13] op_sel_hi:[0,1]
	v_pk_mul_f32 v[46:47], v[16:17], v[14:15] op_sel_hi:[0,1]
	v_pk_mul_f32 v[32:33], v[16:17], v[0:1] op_sel_hi:[0,1]
	v_pk_mul_f32 v[34:35], v[16:17], v[2:3] op_sel_hi:[0,1]
	v_pk_mul_f32 v[36:37], v[16:17], v[4:5] op_sel_hi:[0,1]
	v_pk_mul_f32 v[38:39], v[16:17], v[6:7] op_sel_hi:[0,1]
	v_cvt_scalef32_2xpk16_fp6_f32 v[68:73], v[32:47], v[40:55], 1.0
	v_cvt_scalef32_pk32_f32_fp6 v[0:31], v[68:73], s7
	v_fma_f32 v16, v32, s14, v0
	v_fma_f32 v17, v33, s14, v2
	v_fma_f32 v18, v34, s14, v4
	v_fma_f32 v19, v35, s14, v6
	v_fma_f32 v20, v36, s14, v8
	v_fma_f32 v21, v37, s14, v10
	v_fma_f32 v22, v38, s14, v12
	v_fma_f32 v23, v39, s14, v14
	v_fma_f32 v24, v40, s14, v1
	v_fma_f32 v25, v41, s14, v3
	v_fma_f32 v26, v42, s14, v5
	v_fma_f32 v27, v43, s14, v7
	v_fma_f32 v28, v44, s14, v9
	v_fma_f32 v29, v45, s14, v11
	v_fma_f32 v30, v46, s14, v13
	v_fma_f32 v31, v47, s14, v15
	v_cvt_scalef32_2xpk16_fp6_f32 v[0:5], v[16:31], v[24:39], 1.0
	v_lshl_add_u64 v[4:5], v[118:119], 0, v[130:131]
	v_lshl_add_u64 v[4:5], v[4:5], 0, v[160:161]
	global_store_dwordx3 v[4:5], v[68:70], off nt
	v_add_co_u32_e32 v4, vcc, 0x1000, v4
	v_xor_b32_e32 v0, 0x20820820, v0
	v_xor_b32_e32 v1, 0x8208208, v1
	v_xor_b32_e32 v2, 0x82082082, v2
	v_addc_co_u32_e32 v5, vcc, 0, v5, vcc
	global_store_dwordx3 v[4:5], v[0:2], off offset:2048 nt
	s_and_saveexec_b64 s[18:19], s[0:1]
	s_cbranch_execz .LBB3_20
	v_mov_b32_e32 v1, 0x7a00
	v_add_u32_e32 v0, 0x7f, v66
	v_lshl_add_u32 v1, v66, 8, v1
	v_mov_b32_e32 v129, 0
	v_or_b32_e32 v2, v1, v0
	v_lshl_add_u64 v[0:1], v[116:117], 0, v[128:129]
	global_store_short v[0:1], v2, off
.LBB3_20:
	s_or_b64 exec, exec, s[18:19]
	v_permlane32_swap_b32_e32 v60, v52
	v_permlane32_swap_b32_e32 v61, v53
	v_permlane32_swap_b32_e32 v62, v54
	v_permlane32_swap_b32_e32 v63, v55
	v_permlane32_swap_b32_e32 v58, v50
	v_permlane32_swap_b32_e32 v59, v51
	v_permlane32_swap_b32_e32 v56, v48
	v_permlane32_swap_b32_e32 v57, v49
	v_mov_b64_e32 v[16:17], s[16:17]
	v_pk_mul_f32 v[0:1], v[208:209], v[60:61]
	v_pk_mul_f32 v[2:3], v[210:211], v[62:63]
	v_and_b32_e32 v19, 0x7fffffff, v1
	v_and_b32_e32 v18, 0x7fffffff, v0
	v_pk_mul_f32 v[6:7], v[214:215], v[58:59]
	v_and_b32_e32 v23, 0x7fffffff, v3
	v_and_b32_e32 v22, 0x7fffffff, v2
	v_pk_fma_f32 v[36:37], v[18:19], s[12:13], 1.0 op_sel_hi:[1,0,0]
	v_pk_mul_f32 v[4:5], v[212:213], v[56:57]
	v_and_b32_e32 v31, 0x7fffffff, v7
	v_and_b32_e32 v30, 0x7fffffff, v6
	v_pk_fma_f32 v[38:39], v[22:23], s[12:13], 1.0 op_sel_hi:[1,0,0]
	v_rcp_f32_e32 v36, v36
	v_rcp_f32_e32 v37, v37
	v_and_b32_e32 v27, 0x7fffffff, v5
	v_and_b32_e32 v26, 0x7fffffff, v4
	v_pk_fma_f32 v[42:43], v[30:31], s[12:13], 1.0 op_sel_hi:[1,0,0]
	v_rcp_f32_e32 v38, v38
	v_rcp_f32_e32 v39, v39
	v_pk_fma_f32 v[40:41], v[26:27], s[12:13], 1.0 op_sel_hi:[1,0,0]
	v_rcp_f32_e32 v42, v42
	v_rcp_f32_e32 v43, v43
	v_pk_mul_f32 v[20:21], v[0:1], v[0:1]
	v_rcp_f32_e32 v40, v40
	v_rcp_f32_e32 v41, v41
	v_pk_mul_f32 v[24:25], v[2:3], v[2:3]
	v_pk_mul_f32 v[20:21], v[20:21], s[6:7] op_sel_hi:[1,0]
	v_pk_fma_f32 v[46:47], v[36:37], s[8:9], v[16:17] op_sel_hi:[1,0,0]
	v_pk_mul_f32 v[8:9], v[216:217], v[52:53]
	v_pk_mul_f32 v[32:33], v[6:7], v[6:7]
	v_pk_mul_f32 v[24:25], v[24:25], s[6:7] op_sel_hi:[1,0]
	v_exp_f32_e32 v20, v20
	v_exp_f32_e32 v21, v21
	v_pk_fma_f32 v[52:53], v[38:39], s[8:9], v[16:17] op_sel_hi:[1,0,0]
	v_pk_fma_f32 v[46:47], v[36:37], v[46:47], s[10:11] op_sel_hi:[1,1,0]
	v_pk_mul_f32 v[28:29], v[4:5], v[4:5]
	v_pk_mul_f32 v[32:33], v[32:33], s[6:7] op_sel_hi:[1,0]
	v_exp_f32_e32 v24, v24
	v_exp_f32_e32 v25, v25
	v_pk_fma_f32 v[58:59], v[42:43], s[8:9], v[16:17] op_sel_hi:[1,0,0]
	v_pk_fma_f32 v[52:53], v[38:39], v[52:53], s[10:11] op_sel_hi:[1,1,0]
	v_pk_fma_f32 v[46:47], v[36:37], v[46:47], s[2:3] op_sel_hi:[1,1,0]
	v_and_b32_e32 v35, 0x7fffffff, v9
	v_and_b32_e32 v34, 0x7fffffff, v8
	v_pk_mul_f32 v[28:29], v[28:29], s[6:7] op_sel_hi:[1,0]
	v_exp_f32_e32 v32, v32
	v_exp_f32_e32 v33, v33
	v_pk_fma_f32 v[56:57], v[40:41], s[8:9], v[16:17] op_sel_hi:[1,0,0]
	v_pk_fma_f32 v[58:59], v[42:43], v[58:59], s[10:11] op_sel_hi:[1,1,0]
	v_pk_fma_f32 v[52:53], v[38:39], v[52:53], s[2:3] op_sel_hi:[1,1,0]
	v_pk_fma_f32 v[46:47], v[36:37], v[46:47], s[4:5] op_sel_hi:[1,1,0]
	v_pk_fma_f32 v[44:45], v[34:35], s[12:13], 1.0 op_sel_hi:[1,0,0]
	v_exp_f32_e32 v28, v28
	v_exp_f32_e32 v29, v29
	v_pk_fma_f32 v[56:57], v[40:41], v[56:57], s[10:11] op_sel_hi:[1,1,0]
	v_pk_fma_f32 v[58:59], v[42:43], v[58:59], s[2:3] op_sel_hi:[1,1,0]
	v_pk_fma_f32 v[52:53], v[38:39], v[52:53], s[4:5] op_sel_hi:[1,1,0]
	v_pk_mul_f32 v[36:37], v[36:37], v[46:47]
	v_rcp_f32_e32 v44, v44
	v_pk_fma_f32 v[56:57], v[40:41], v[56:57], s[2:3] op_sel_hi:[1,1,0]
	v_pk_fma_f32 v[58:59], v[42:43], v[58:59], s[4:5] op_sel_hi:[1,1,0]
	v_pk_mul_f32 v[38:39], v[38:39], v[52:53]
	v_pk_fma_f32 v[20:21], v[20:21], v[36:37], 0.5 op_sel_hi:[1,1,0] neg_lo:[1,0,0] neg_hi:[1,0,0]
	v_rcp_f32_e32 v45, v45
	v_pk_fma_f32 v[56:57], v[40:41], v[56:57], s[4:5] op_sel_hi:[1,1,0]
	v_pk_mul_f32 v[42:43], v[42:43], v[58:59]
	v_pk_fma_f32 v[24:25], v[24:25], v[38:39], 0.5 op_sel_hi:[1,1,0] neg_lo:[1,0,0] neg_hi:[1,0,0]
	v_pk_mul_f32 v[18:19], v[18:19], v[20:21]
	v_pk_mul_f32 v[40:41], v[40:41], v[56:57]
	v_pk_mul_f32 v[20:21], v[22:23], v[24:25]
	v_pk_fma_f32 v[0:1], v[0:1], 0.5, v[18:19] op_sel_hi:[1,0,1]
	v_pk_fma_f32 v[18:19], v[32:33], v[42:43], 0.5 op_sel_hi:[1,1,0] neg_lo:[1,0,0] neg_hi:[1,0,0]
	v_pk_fma_f32 v[28:29], v[28:29], v[40:41], 0.5 op_sel_hi:[1,1,0] neg_lo:[1,0,0] neg_hi:[1,0,0]
	v_pk_fma_f32 v[2:3], v[2:3], 0.5, v[20:21] op_sel_hi:[1,0,1]
	v_pk_mul_f32 v[18:19], v[30:31], v[18:19]
	v_pk_mul_f32 v[20:21], v[8:9], v[8:9]
	v_pk_mul_f32 v[22:23], v[26:27], v[28:29]
	v_pk_fma_f32 v[6:7], v[6:7], 0.5, v[18:19] op_sel_hi:[1,0,1]
	v_pk_fma_f32 v[18:19], v[44:45], s[8:9], v[16:17] op_sel_hi:[1,0,0]
	v_pk_mul_f32 v[20:21], v[20:21], s[6:7] op_sel_hi:[1,0]
	v_pk_mul_f32 v[10:11], v[218:219], v[54:55]
	v_pk_fma_f32 v[4:5], v[4:5], 0.5, v[22:23] op_sel_hi:[1,0,1]
	v_pk_fma_f32 v[18:19], v[44:45], v[18:19], s[10:11] op_sel_hi:[1,1,0]
	v_exp_f32_e32 v20, v20
	v_exp_f32_e32 v21, v21
	v_and_b32_e32 v23, 0x7fffffff, v11
	v_and_b32_e32 v22, 0x7fffffff, v10
	v_pk_fma_f32 v[18:19], v[44:45], v[18:19], s[2:3] op_sel_hi:[1,1,0]
	v_pk_fma_f32 v[24:25], v[22:23], s[12:13], 1.0 op_sel_hi:[1,0,0]
	v_pk_fma_f32 v[18:19], v[44:45], v[18:19], s[4:5] op_sel_hi:[1,1,0]
	v_rcp_f32_e32 v24, v24
	v_rcp_f32_e32 v25, v25
	v_pk_mul_f32 v[18:19], v[44:45], v[18:19]
	v_pk_mul_f32 v[12:13], v[220:221], v[48:49]
	v_pk_fma_f32 v[18:19], v[20:21], v[18:19], 0.5 op_sel_hi:[1,1,0] neg_lo:[1,0,0] neg_hi:[1,0,0]
	v_pk_mul_f32 v[20:21], v[10:11], v[10:11]
	v_pk_mul_f32 v[18:19], v[34:35], v[18:19]
	v_pk_mul_f32 v[20:21], v[20:21], s[6:7] op_sel_hi:[1,0]
	v_pk_fma_f32 v[8:9], v[8:9], 0.5, v[18:19] op_sel_hi:[1,0,1]
	v_pk_fma_f32 v[18:19], v[24:25], s[8:9], v[16:17] op_sel_hi:[1,0,0]
	v_exp_f32_e32 v20, v20
	v_pk_fma_f32 v[18:19], v[24:25], v[18:19], s[10:11] op_sel_hi:[1,1,0]
	v_exp_f32_e32 v21, v21
	v_pk_fma_f32 v[18:19], v[24:25], v[18:19], s[2:3] op_sel_hi:[1,1,0]
	v_pk_mul_f32 v[14:15], v[222:223], v[50:51]
	v_pk_fma_f32 v[18:19], v[24:25], v[18:19], s[4:5] op_sel_hi:[1,1,0]
	s_nop 0
	v_pk_mul_f32 v[18:19], v[24:25], v[18:19]
	v_and_b32_e32 v25, 0x7fffffff, v13
	v_and_b32_e32 v24, 0x7fffffff, v12
	v_pk_fma_f32 v[26:27], v[24:25], s[12:13], 1.0 op_sel_hi:[1,0,0]
	v_pk_fma_f32 v[18:19], v[20:21], v[18:19], 0.5 op_sel_hi:[1,1,0] neg_lo:[1,0,0] neg_hi:[1,0,0]
	v_rcp_f32_e32 v26, v26
	v_rcp_f32_e32 v27, v27
	v_pk_mul_f32 v[18:19], v[22:23], v[18:19]
	v_pk_mul_f32 v[20:21], v[12:13], v[12:13]
	v_pk_fma_f32 v[10:11], v[10:11], 0.5, v[18:19] op_sel_hi:[1,0,1]
	v_pk_fma_f32 v[18:19], v[26:27], s[8:9], v[16:17] op_sel_hi:[1,0,0]
	v_pk_mul_f32 v[20:21], v[20:21], s[6:7] op_sel_hi:[1,0]
	v_pk_fma_f32 v[18:19], v[26:27], v[18:19], s[10:11] op_sel_hi:[1,1,0]
	v_exp_f32_e32 v20, v20
	v_pk_fma_f32 v[18:19], v[26:27], v[18:19], s[2:3] op_sel_hi:[1,1,0]
	v_exp_f32_e32 v21, v21
	v_pk_fma_f32 v[18:19], v[26:27], v[18:19], s[4:5] op_sel_hi:[1,1,0]
	v_and_b32_e32 v23, 0x7fffffff, v15
	v_and_b32_e32 v22, 0x7fffffff, v14
	v_pk_mul_f32 v[18:19], v[26:27], v[18:19]
	v_pk_fma_f32 v[26:27], v[22:23], s[12:13], 1.0 op_sel_hi:[1,0,0]
	v_pk_fma_f32 v[18:19], v[20:21], v[18:19], 0.5 op_sel_hi:[1,1,0] neg_lo:[1,0,0] neg_hi:[1,0,0]
	v_rcp_f32_e32 v26, v26
	v_rcp_f32_e32 v27, v27
	v_pk_mul_f32 v[18:19], v[24:25], v[18:19]
	v_pk_fma_f32 v[16:17], v[26:27], s[8:9], v[16:17] op_sel_hi:[1,0,0]
	v_pk_fma_f32 v[12:13], v[12:13], 0.5, v[18:19] op_sel_hi:[1,0,1]
	v_pk_mul_f32 v[18:19], v[14:15], v[14:15]
	v_pk_fma_f32 v[16:17], v[26:27], v[16:17], s[10:11] op_sel_hi:[1,1,0]
	v_pk_mul_f32 v[18:19], v[18:19], s[6:7] op_sel_hi:[1,0]
	v_pk_fma_f32 v[16:17], v[26:27], v[16:17], s[2:3] op_sel_hi:[1,1,0]
	v_exp_f32_e32 v18, v18
	v_exp_f32_e32 v19, v19
	v_pk_fma_f32 v[16:17], v[26:27], v[16:17], s[4:5] op_sel_hi:[1,1,0]
	s_nop 0
	v_pk_mul_f32 v[16:17], v[26:27], v[16:17]
	s_nop 0
	v_pk_fma_f32 v[16:17], v[18:19], v[16:17], 0.5 op_sel_hi:[1,1,0] neg_lo:[1,0,0] neg_hi:[1,0,0]
	v_max_f32_e64 v18, |v6|, |v7|
	v_pk_mul_f32 v[16:17], v[22:23], v[16:17]
	s_nop 0
	v_pk_fma_f32 v[14:15], v[14:15], 0.5, v[16:17] op_sel_hi:[1,0,1]
	v_max_f32_e64 v16, |v0|, |v1|
	v_max_f32_e64 v17, |v2|, |v3|
	v_max3_f32 v16, v16, 0, v17
	v_max_f32_e64 v17, |v4|, |v5|
	v_max3_f32 v16, v16, v17, v18
	v_max_f32_e64 v17, |v8|, |v9|
	v_max_f32_e64 v18, |v10|, |v11|
	v_max3_f32 v16, v16, v17, v18
	v_max_f32_e64 v17, |v12|, |v13|
	v_max_f32_e64 v18, |v14|, |v15|
	v_max3_f32 v16, v16, v17, v18
	v_mov_b32_e32 v17, v16
	s_nop 1
	v_permlane16_swap_b32_e32 v16, v17
	v_max_f32_e32 v17, v17, v17
	v_max_f32_e32 v16, v16, v16
	v_max_f32_e32 v16, v16, v17
	v_lshrrev_b32_e32 v17, 23, v16
	v_and_b32_e32 v16, 0x7fffff, v16
	v_cmp_lt_u32_e32 vcc, s3, v16
	s_nop 1
	v_addc_co_u32_e32 v16, vcc, v17, v64, vcc
	v_med3_i32 v48, v16, s5, v65
	v_lshlrev_b32_e32 v16, 23, v48
	v_sub_u32_e32 v16, 1.0, v16
	v_pk_mul_f32 v[40:41], v[16:17], v[8:9] op_sel_hi:[0,1]
	v_pk_mul_f32 v[42:43], v[16:17], v[10:11] op_sel_hi:[0,1]
	v_pk_mul_f32 v[44:45], v[16:17], v[12:13] op_sel_hi:[0,1]
	v_pk_mul_f32 v[46:47], v[16:17], v[14:15] op_sel_hi:[0,1]
	v_pk_mul_f32 v[32:33], v[16:17], v[0:1] op_sel_hi:[0,1]
	v_pk_mul_f32 v[34:35], v[16:17], v[2:3] op_sel_hi:[0,1]
	v_pk_mul_f32 v[36:37], v[16:17], v[4:5] op_sel_hi:[0,1]
	v_pk_mul_f32 v[38:39], v[16:17], v[6:7] op_sel_hi:[0,1]
	v_cvt_scalef32_2xpk16_fp6_f32 v[50:55], v[32:47], v[40:55], 1.0
	v_cvt_scalef32_pk32_f32_fp6 v[0:31], v[50:55], s7
	v_fma_f32 v16, v32, s14, v0
	v_fma_f32 v17, v33, s14, v2
	v_fma_f32 v18, v34, s14, v4
	v_fma_f32 v19, v35, s14, v6
	v_fma_f32 v20, v36, s14, v8
	v_fma_f32 v21, v37, s14, v10
	v_fma_f32 v22, v38, s14, v12
	v_fma_f32 v23, v39, s14, v14
	v_fma_f32 v24, v40, s14, v1
	v_fma_f32 v25, v41, s14, v3
	v_fma_f32 v26, v42, s14, v5
	v_fma_f32 v27, v43, s14, v7
	v_fma_f32 v28, v44, s14, v9
	v_fma_f32 v29, v45, s14, v11
	v_fma_f32 v30, v46, s14, v13
	v_fma_f32 v31, v47, s14, v15
	v_cvt_scalef32_2xpk16_fp6_f32 v[0:5], v[16:31], v[24:39], 1.0
	v_lshl_add_u64 v[4:5], v[118:119], 0, v[114:115]
	v_lshl_add_u64 v[4:5], v[4:5], 0, v[160:161]
	global_store_dwordx3 v[4:5], v[50:52], off nt
	v_add_co_u32_e32 v4, vcc, 0x1000, v4
	v_xor_b32_e32 v0, 0x20820820, v0
	v_xor_b32_e32 v1, 0x8208208, v1
	v_xor_b32_e32 v2, 0x82082082, v2
	v_addc_co_u32_e32 v5, vcc, 0, v5, vcc
	global_store_dwordx3 v[4:5], v[0:2], off offset:2048 nt
	s_and_saveexec_b64 s[2:3], s[0:1]
	s_cbranch_execz .LBB3_22
	v_mov_b32_e32 v1, 0x7a00
	v_add_u32_e32 v0, 0x7f, v48
	v_lshl_add_u32 v1, v48, 8, v1
	v_mov_b32_e32 v113, 0
	v_or_b32_e32 v2, v1, v0
	v_lshl_add_u64 v[0:1], v[116:117], 0, v[112:113]
	global_store_short v[0:1], v2, off
